# union v14 with the permuted epilogue stores pipelined two deep and counted lgkmcnt waits (store k issued at the position of store k+2)
# speedup vs baseline: 1.0207x; 1.0207x over previous
.LBB0_174:
	v_mbcnt_lo_u32_b32 v250, -1, 0
	v_mbcnt_hi_u32_b32 v250, -1, v250
	v_lshrrev_b32_e32 v251, 2, v250
	v_and_b32_e32 v250, 3, v250
	v_lshl_add_u32 v250, v250, 4, v251
	v_lshlrev_b32_e32 v250, 2, v250
	s_ashr_i32 s15, s60, 3
	s_add_i32 s62, s15, s75
	s_lshl_b32 s15, s60, 8
	s_and_b32 s15, s15, 0x700
	s_cmp_eq_u32 s62, 0
	v_lshl_add_u32 v174, s28, 8, v1
	s_cselect_b64 s[26:27], -1, 0
	v_or_b32_e32 v82, s15, v209
	s_and_b64 s[26:27], s[50:51], s[26:27]
	v_or_b32_e32 v180, 16, v174
	v_or_b32_e32 v178, 32, v174
	v_or_b32_e32 v176, 48, v174
	s_mov_b64 s[64:65], -1
	s_and_b64 vcc, exec, s[26:27]
	v_lshlrev_b32_e32 v114, 1, v82
	v_ashrrev_i32_e32 v175, 31, v174
	v_ashrrev_i32_e32 v181, 31, v180
	v_ashrrev_i32_e32 v179, 31, v178
	v_ashrrev_i32_e32 v177, 31, v176
	s_cbranch_vccnz .LBB0_177
	v_lshl_add_u32 v158, s14, 10, v210
	ds_read2_b32 v[88:89], v158 offset1:16
	s_ashr_i32 s63, s62, 31
	s_lshl_b64 s[26:27], s[62:63], 25
	s_add_u32 s26, s84, s26
	s_addc_u32 s27, s85, s27
	v_lshl_add_u64 v[90:91], s[26:27], 0, v[114:115]
	v_lshlrev_b64 v[82:83], 12, v[174:175]
	s_waitcnt lgkmcnt(0)
	v_pk_mul_f32 v[84:85], v[144:145], v[88:89] op_sel_hi:[1,0]
	v_lshl_add_u64 v[82:83], v[90:91], 0, v[82:83]
	v_pk_mul_f32 v[86:87], v[146:147], v[88:89] op_sel_hi:[1,0]
	v_cvt_pk_bf16_f32 v84, v84, v85
	v_pk_mul_f32 v[92:93], v[142:143], v[88:89] op_sel_hi:[1,0]
	v_cvt_pk_bf16_f32 v85, v86, v87
	v_pk_mul_f32 v[94:95], v[140:141], v[88:89] op_sel_hi:[1,0]
	v_cvt_pk_bf16_f32 v87, v92, v93
	v_pk_mul_f32 v[92:93], v[134:135], v[88:89] op_sel_hi:[1,0]
	v_cvt_pk_bf16_f32 v86, v94, v95
	ds_bpermute_b32 v232, v250, v84
	ds_bpermute_b32 v233, v250, v85
	ds_bpermute_b32 v234, v250, v86
	ds_bpermute_b32 v235, v250, v87
	ds_bpermute_b32 v236, v250, v82
	v_pk_mul_f32 v[94:95], v[132:133], v[88:89] op_sel_hi:[1,0]
	s_mov_b32 s15, 0x80000
	v_pk_mul_f32 v[84:85], v[136:137], v[88:89] op_sel_hi:[1,0]
	v_pk_mul_f32 v[86:87], v[138:139], v[88:89] op_sel_hi:[1,0]
	v_cvt_pk_bf16_f32 v84, v84, v85
	v_mov_b32_e32 v88, v89
	v_cvt_pk_bf16_f32 v85, v86, v87
	v_cvt_pk_bf16_f32 v86, v94, v95
	v_cvt_pk_bf16_f32 v87, v92, v93
	ds_bpermute_b32 v238, v250, v84
	ds_bpermute_b32 v239, v250, v85
	ds_bpermute_b32 v240, v250, v86
	ds_bpermute_b32 v241, v250, v87
	ds_bpermute_b32 v242, v250, v82
	v_pk_mul_f32 v[94:95], v[126:127], v[88:89] op_sel_hi:[1,0]
	v_pk_mul_f32 v[96:97], v[124:125], v[88:89] op_sel_hi:[1,0]
	v_lshlrev_b64 v[84:85], 12, v[180:181]
	v_lshl_add_u64 v[92:93], v[90:91], 0, v[84:85]
	v_pk_mul_f32 v[86:87], v[130:131], v[88:89] op_sel_hi:[1,0]
	v_pk_mul_f32 v[84:85], v[128:129], v[88:89] op_sel_hi:[1,0]
	s_mov_b64 s[16:17], 0x80000
	v_cvt_pk_bf16_f32 v84, v84, v85
	v_cvt_pk_bf16_f32 v85, v86, v87
	v_cvt_pk_bf16_f32 v86, v96, v97
	v_cvt_pk_bf16_f32 v87, v94, v95
	s_waitcnt lgkmcnt(5)
	v_subrev_u32_e32 v236, s82, v236
	global_store_dwordx4 v236, v[232:235], s[82:83]
	ds_bpermute_b32 v244, v250, v84
	ds_bpermute_b32 v245, v250, v85
	ds_bpermute_b32 v246, v250, v86
	ds_bpermute_b32 v247, v250, v87
	ds_bpermute_b32 v248, v250, v92
	v_pk_mul_f32 v[94:95], v[118:119], v[88:89] op_sel_hi:[1,0]
	s_nop 0
	v_pk_mul_f32 v[86:87], v[122:123], v[88:89] op_sel_hi:[1,0]
	v_pk_mul_f32 v[84:85], v[120:121], v[88:89] op_sel_hi:[1,0]
	v_pk_mul_f32 v[88:89], v[116:117], v[88:89] op_sel_hi:[1,0]
	v_cvt_pk_bf16_f32 v84, v84, v85
	v_cvt_pk_bf16_f32 v85, v86, v87
	v_cvt_pk_bf16_f32 v87, v94, v95
	s_nop 0
	v_cvt_pk_bf16_f32 v86, v88, v89
	ds_read2_b32 v[88:89], v158 offset0:32 offset1:48
	s_waitcnt lgkmcnt(6)
	v_subrev_u32_e32 v242, s82, v242
	global_store_dwordx4 v242, v[238:241], s[82:83] offset:64
	ds_bpermute_b32 v232, v250, v84
	ds_bpermute_b32 v233, v250, v85
	ds_bpermute_b32 v234, v250, v86
	ds_bpermute_b32 v235, v250, v87
	ds_bpermute_b32 v236, v250, v92
	s_waitcnt lgkmcnt(0)
	v_pk_mul_f32 v[94:95], v[108:109], v[88:89] op_sel_hi:[1,0]
	v_lshlrev_b64 v[84:85], 12, v[178:179]
	v_lshl_add_u64 v[92:93], v[90:91], 0, v[84:85]
	v_pk_mul_f32 v[84:85], v[110:111], v[88:89] op_sel_hi:[1,0]
	v_pk_mul_f32 v[86:87], v[112:113], v[88:89] op_sel_hi:[1,0]
	v_cvt_pk_bf16_f32 v84, v84, v85
	v_pk_mul_f32 v[96:97], v[106:107], v[88:89] op_sel_hi:[1,0]
	v_cvt_pk_bf16_f32 v85, v86, v87
	v_cvt_pk_bf16_f32 v87, v94, v95
	v_pk_mul_f32 v[94:95], v[100:101], v[88:89] op_sel_hi:[1,0]
	v_cvt_pk_bf16_f32 v86, v96, v97
	s_waitcnt lgkmcnt(6)
	v_subrev_u32_e32 v248, s82, v248
	global_store_dwordx4 v248, v[244:247], s[82:83]
	ds_bpermute_b32 v238, v250, v84
	ds_bpermute_b32 v239, v250, v85
	ds_bpermute_b32 v240, v250, v86
	ds_bpermute_b32 v241, v250, v87
	ds_bpermute_b32 v242, v250, v92
	v_pk_mul_f32 v[96:97], v[98:99], v[88:89] op_sel_hi:[1,0]
	s_nop 0
	v_pk_mul_f32 v[84:85], v[102:103], v[88:89] op_sel_hi:[1,0]
	v_pk_mul_f32 v[86:87], v[104:105], v[88:89] op_sel_hi:[1,0]
	v_cvt_pk_bf16_f32 v84, v84, v85
	v_mov_b32_e32 v88, v89
	v_cvt_pk_bf16_f32 v85, v86, v87
	v_cvt_pk_bf16_f32 v86, v96, v97
	v_cvt_pk_bf16_f32 v87, v94, v95
	s_waitcnt lgkmcnt(5)
	v_subrev_u32_e32 v236, s82, v236
	global_store_dwordx4 v236, v[232:235], s[82:83] offset:64
	ds_bpermute_b32 v244, v250, v84
	ds_bpermute_b32 v245, v250, v85
	ds_bpermute_b32 v246, v250, v86
	ds_bpermute_b32 v247, v250, v87
	ds_bpermute_b32 v248, v250, v92
	v_pk_mul_f32 v[94:95], v[74:75], v[88:89] op_sel_hi:[1,0]
	v_pk_mul_f32 v[92:93], v[76:77], v[88:89] op_sel_hi:[1,0]
	v_lshlrev_b64 v[84:85], 12, v[176:177]
	v_lshl_add_u64 v[90:91], v[90:91], 0, v[84:85]
	v_pk_mul_f32 v[86:87], v[80:81], v[88:89] op_sel_hi:[1,0]
	v_pk_mul_f32 v[84:85], v[78:79], v[88:89] op_sel_hi:[1,0]
	s_nop 0
	v_cvt_pk_bf16_f32 v84, v84, v85
	v_cvt_pk_bf16_f32 v85, v86, v87
	v_cvt_pk_bf16_f32 v86, v94, v95
	ds_read2_b32 v[94:95], v158 offset0:128 offset1:144
	v_cvt_pk_bf16_f32 v87, v92, v93
	s_waitcnt lgkmcnt(6)
	v_subrev_u32_e32 v242, s82, v242
	global_store_dwordx4 v242, v[238:241], s[82:83]
	ds_bpermute_b32 v232, v250, v84
	ds_bpermute_b32 v233, v250, v85
	ds_bpermute_b32 v234, v250, v86
	ds_bpermute_b32 v235, v250, v87
	ds_bpermute_b32 v236, v250, v90
	v_pk_mul_f32 v[92:93], v[68:69], v[88:89] op_sel_hi:[1,0]
	s_nop 0
	v_pk_mul_f32 v[86:87], v[72:73], v[88:89] op_sel_hi:[1,0]
	v_pk_mul_f32 v[84:85], v[70:71], v[88:89] op_sel_hi:[1,0]
	v_pk_mul_f32 v[88:89], v[66:67], v[88:89] op_sel_hi:[1,0]
	v_cvt_pk_bf16_f32 v84, v84, v85
	v_cvt_pk_bf16_f32 v85, v86, v87
	v_cvt_pk_bf16_f32 v87, v92, v93
	s_waitcnt lgkmcnt(0)
	v_pk_mul_f32 v[92:93], v[58:59], v[94:95] op_sel_hi:[1,0]
	v_cvt_pk_bf16_f32 v86, v88, v89
	s_waitcnt lgkmcnt(6)
	v_subrev_u32_e32 v248, s82, v248
	global_store_dwordx4 v248, v[244:247], s[82:83] offset:64
	ds_bpermute_b32 v238, v250, v84
	ds_bpermute_b32 v239, v250, v85
	ds_bpermute_b32 v240, v250, v86
	ds_bpermute_b32 v241, v250, v87
	ds_bpermute_b32 v242, v250, v90
	v_pk_mul_f32 v[90:91], v[60:61], v[94:95] op_sel_hi:[1,0]
	v_lshl_add_u64 v[88:89], v[82:83], 0, s[16:17]
	v_pk_mul_f32 v[86:87], v[64:65], v[94:95] op_sel_hi:[1,0]
	v_pk_mul_f32 v[84:85], v[62:63], v[94:95] op_sel_hi:[1,0]
	s_mov_b64 s[16:17], 0x90000
	v_cvt_pk_bf16_f32 v84, v84, v85
	v_cvt_pk_bf16_f32 v85, v86, v87
	v_cvt_pk_bf16_f32 v87, v90, v91
	v_add_co_u32_e32 v90, vcc, s15, v82
	v_cvt_pk_bf16_f32 v86, v92, v93
	v_pk_mul_f32 v[92:93], v[50:51], v[94:95] op_sel_hi:[1,0]
	s_nop 0
	v_addc_co_u32_e32 v91, vcc, 0, v83, vcc
	s_waitcnt lgkmcnt(5)
	v_subrev_u32_e32 v236, s82, v236
	global_store_dwordx4 v236, v[232:235], s[82:83]
	ds_bpermute_b32 v244, v250, v84
	ds_bpermute_b32 v245, v250, v85
	ds_bpermute_b32 v246, v250, v86
	ds_bpermute_b32 v247, v250, v87
	ds_bpermute_b32 v248, v250, v90
	v_pk_mul_f32 v[90:91], v[52:53], v[94:95] op_sel_hi:[1,0]
	s_mov_b32 s15, 0x90000
	v_pk_mul_f32 v[86:87], v[56:57], v[94:95] op_sel_hi:[1,0]
	v_pk_mul_f32 v[84:85], v[54:55], v[94:95] op_sel_hi:[1,0]
	s_nop 0
	v_cvt_pk_bf16_f32 v84, v84, v85
	v_cvt_pk_bf16_f32 v85, v86, v87
	v_cvt_pk_bf16_f32 v86, v92, v93
	v_cvt_pk_bf16_f32 v87, v90, v91
	v_mov_b32_e32 v90, v95
	s_waitcnt lgkmcnt(5)
	v_subrev_u32_e32 v242, s82, v242
	global_store_dwordx4 v242, v[238:241], s[82:83] offset:64
	ds_bpermute_b32 v232, v250, v84
	ds_bpermute_b32 v233, v250, v85
	ds_bpermute_b32 v234, v250, v86
	ds_bpermute_b32 v235, v250, v87
	ds_bpermute_b32 v236, v250, v88
	v_pk_mul_f32 v[94:95], v[42:43], v[90:91] op_sel_hi:[1,0]
	v_pk_mul_f32 v[92:93], v[44:45], v[90:91] op_sel_hi:[1,0]
	v_pk_mul_f32 v[86:87], v[48:49], v[90:91] op_sel_hi:[1,0]
	v_pk_mul_f32 v[84:85], v[46:47], v[90:91] op_sel_hi:[1,0]
	v_lshl_add_u64 v[88:89], v[82:83], 0, s[16:17]
	v_cvt_pk_bf16_f32 v84, v84, v85
	v_cvt_pk_bf16_f32 v85, v86, v87
	v_cvt_pk_bf16_f32 v86, v94, v95
	ds_read2_b32 v[94:95], v158 offset0:160 offset1:176
	v_cvt_pk_bf16_f32 v87, v92, v93
	v_add_co_u32_e32 v92, vcc, s15, v82
	s_mov_b32 s15, 0xa0000
	s_nop 0
	v_addc_co_u32_e32 v93, vcc, 0, v83, vcc
	s_waitcnt lgkmcnt(6)
	v_subrev_u32_e32 v248, s82, v248
	global_store_dwordx4 v248, v[244:247], s[82:83]
	ds_bpermute_b32 v238, v250, v84
	ds_bpermute_b32 v239, v250, v85
	ds_bpermute_b32 v240, v250, v86
	ds_bpermute_b32 v241, v250, v87
	ds_bpermute_b32 v242, v250, v92
	v_pk_mul_f32 v[92:93], v[36:37], v[90:91] op_sel_hi:[1,0]
	s_mov_b64 s[16:17], 0xa0000
	v_pk_mul_f32 v[86:87], v[40:41], v[90:91] op_sel_hi:[1,0]
	v_pk_mul_f32 v[84:85], v[38:39], v[90:91] op_sel_hi:[1,0]
	v_pk_mul_f32 v[90:91], v[34:35], v[90:91] op_sel_hi:[1,0]
	v_cvt_pk_bf16_f32 v84, v84, v85
	v_cvt_pk_bf16_f32 v85, v86, v87
	v_cvt_pk_bf16_f32 v87, v92, v93
	s_waitcnt lgkmcnt(0)
	v_pk_mul_f32 v[92:93], v[26:27], v[94:95] op_sel_hi:[1,0]
	v_cvt_pk_bf16_f32 v86, v90, v91
	s_waitcnt lgkmcnt(6)
	v_subrev_u32_e32 v236, s82, v236
	global_store_dwordx4 v236, v[232:235], s[82:83] offset:64
	ds_bpermute_b32 v244, v250, v84
	ds_bpermute_b32 v245, v250, v85
	ds_bpermute_b32 v246, v250, v86
	ds_bpermute_b32 v247, v250, v87
	ds_bpermute_b32 v248, v250, v88
	v_pk_mul_f32 v[90:91], v[28:29], v[94:95] op_sel_hi:[1,0]
	v_lshl_add_u64 v[88:89], v[82:83], 0, s[16:17]
	v_pk_mul_f32 v[86:87], v[32:33], v[94:95] op_sel_hi:[1,0]
	v_pk_mul_f32 v[84:85], v[30:31], v[94:95] op_sel_hi:[1,0]
	s_mov_b64 s[16:17], 0xb0000
	v_cvt_pk_bf16_f32 v84, v84, v85
	v_cvt_pk_bf16_f32 v85, v86, v87
	v_cvt_pk_bf16_f32 v87, v90, v91
	v_add_co_u32_e32 v90, vcc, s15, v82
	v_cvt_pk_bf16_f32 v86, v92, v93
	s_mov_b32 s15, 0xb0000
	s_nop 0
	v_addc_co_u32_e32 v91, vcc, 0, v83, vcc
	s_waitcnt lgkmcnt(5)
	v_subrev_u32_e32 v242, s82, v242
	global_store_dwordx4 v242, v[238:241], s[82:83]
	ds_bpermute_b32 v232, v250, v84
	ds_bpermute_b32 v233, v250, v85
	ds_bpermute_b32 v234, v250, v86
	ds_bpermute_b32 v235, v250, v87
	ds_bpermute_b32 v236, v250, v90
	v_pk_mul_f32 v[90:91], v[20:21], v[94:95] op_sel_hi:[1,0]
	v_pk_mul_f32 v[92:93], v[18:19], v[94:95] op_sel_hi:[1,0]
	v_pk_mul_f32 v[86:87], v[24:25], v[94:95] op_sel_hi:[1,0]
	v_pk_mul_f32 v[84:85], v[22:23], v[94:95] op_sel_hi:[1,0]
	s_nop 0
	v_cvt_pk_bf16_f32 v84, v84, v85
	v_cvt_pk_bf16_f32 v85, v86, v87
	v_cvt_pk_bf16_f32 v87, v90, v91
	v_mov_b32_e32 v90, v95
	v_cvt_pk_bf16_f32 v86, v92, v93
	s_waitcnt lgkmcnt(5)
	v_subrev_u32_e32 v248, s82, v248
	global_store_dwordx4 v248, v[244:247], s[82:83] offset:64
	ds_bpermute_b32 v238, v250, v84
	ds_bpermute_b32 v239, v250, v85
	ds_bpermute_b32 v240, v250, v86
	ds_bpermute_b32 v241, v250, v87
	ds_bpermute_b32 v242, v250, v88
	v_lshl_add_u64 v[88:89], v[82:83], 0, s[16:17]
	v_add_co_u32_e32 v82, vcc, s15, v82
	v_pk_mul_f32 v[84:85], v[14:15], v[90:91] op_sel_hi:[1,0]
	v_pk_mul_f32 v[86:87], v[16:17], v[90:91] op_sel_hi:[1,0]
	v_cvt_pk_bf16_f32 v84, v84, v85
	v_addc_co_u32_e32 v83, vcc, 0, v83, vcc
	v_cvt_pk_bf16_f32 v85, v86, v87
	v_pk_mul_f32 v[92:93], v[12:13], v[90:91] op_sel_hi:[1,0]
	v_pk_mul_f32 v[94:95], v[10:11], v[90:91] op_sel_hi:[1,0]
	v_cvt_pk_bf16_f32 v87, v92, v93
	s_nop 0
	v_cvt_pk_bf16_f32 v86, v94, v95
	s_waitcnt lgkmcnt(5)
	v_subrev_u32_e32 v236, s82, v236
	global_store_dwordx4 v236, v[232:235], s[82:83]
	ds_bpermute_b32 v244, v250, v84
	ds_bpermute_b32 v245, v250, v85
	ds_bpermute_b32 v246, v250, v86
	ds_bpermute_b32 v247, v250, v87
	ds_bpermute_b32 v248, v250, v82
	v_pk_mul_f32 v[82:83], v[6:7], v[90:91] op_sel_hi:[1,0]
	s_nop 0
	v_pk_mul_f32 v[84:85], v[8:9], v[90:91] op_sel_hi:[1,0]
	v_pk_mul_f32 v[86:87], v[4:5], v[90:91] op_sel_hi:[1,0]
	v_pk_mul_f32 v[90:91], v[2:3], v[90:91] op_sel_hi:[1,0]
	v_cvt_pk_bf16_f32 v82, v82, v83
	v_cvt_pk_bf16_f32 v83, v84, v85
	v_cvt_pk_bf16_f32 v85, v86, v87
	s_nop 0
	v_cvt_pk_bf16_f32 v84, v90, v91
	s_waitcnt lgkmcnt(5)
	v_subrev_u32_e32 v242, s82, v242
	global_store_dwordx4 v242, v[238:241], s[82:83] offset:64
	ds_bpermute_b32 v232, v250, v82
	ds_bpermute_b32 v233, v250, v83
	ds_bpermute_b32 v234, v250, v84
	ds_bpermute_b32 v235, v250, v85
	ds_bpermute_b32 v236, v250, v88
	s_waitcnt lgkmcnt(5)
	v_subrev_u32_e32 v248, s82, v248
	global_store_dwordx4 v248, v[244:247], s[82:83]
	s_waitcnt lgkmcnt(0)
	v_subrev_u32_e32 v236, s82, v236
	global_store_dwordx4 v236, v[232:235], s[82:83] offset:64
	s_cbranch_execz .LBB0_178

.LBB0_178:
	s_lshl_b32 s14, s14, 10
	v_add_u32_e32 v213, s14, v211
	ds_read_b32 v82, v213
	s_waitcnt lgkmcnt(0)
	v_pk_mul_f32 v[84:85], v[146:147], v[82:83] op_sel_hi:[1,0]
	v_pk_mul_f32 v[86:87], v[144:145], v[82:83] op_sel_hi:[1,0]
	v_pk_mul_f32 v[84:85], v[84:85], v[84:85]
	v_pk_mul_f32 v[88:89], v[140:141], v[82:83] op_sel_hi:[1,0]
	v_pk_fma_f32 v[84:85], v[86:87], v[86:87], v[84:85]
	v_pk_mul_f32 v[86:87], v[142:143], v[82:83] op_sel_hi:[1,0]
	s_nop 0
	v_pk_mul_f32 v[86:87], v[86:87], v[86:87]
	s_nop 0
	v_pk_fma_f32 v[86:87], v[88:89], v[88:89], v[86:87]
	v_pk_mul_f32 v[88:89], v[136:137], v[82:83] op_sel_hi:[1,0]
	v_pk_add_f32 v[84:85], v[84:85], v[86:87]
	v_pk_mul_f32 v[86:87], v[138:139], v[82:83] op_sel_hi:[1,0]
	s_nop 0
	v_pk_mul_f32 v[86:87], v[86:87], v[86:87]
	s_nop 0
	v_pk_fma_f32 v[86:87], v[88:89], v[88:89], v[86:87]
	s_nop 0
	v_pk_add_f32 v[84:85], v[86:87], v[84:85]
	v_pk_mul_f32 v[86:87], v[134:135], v[82:83] op_sel_hi:[1,0]
	v_pk_mul_f32 v[82:83], v[132:133], v[82:83] op_sel_hi:[1,0]
	v_pk_mul_f32 v[86:87], v[86:87], v[86:87]
	s_nop 0
	v_pk_fma_f32 v[82:83], v[82:83], v[82:83], v[86:87]
	s_nop 0
	v_pk_add_f32 v[82:83], v[82:83], v[84:85]
	s_nop 0
	v_add_f32_e32 v82, v82, v83
	ds_swizzle_b32 v83, v82 offset:swizzle(SWAP,16)
	s_waitcnt lgkmcnt(0)
	v_add_f32_e32 v82, v82, v83
	v_mov_b32_e32 v83, v82
	s_nop 1
	v_permlane32_swap_b32_e32 v82, v83
	s_and_saveexec_b64 s[62:63], s[38:39]
	v_add_f32_e32 v82, v82, v83
	ds_write_b32 v183, v82
	s_or_b64 exec, exec, s[62:63]
	ds_read_b32 v82, v213 offset:64
	s_waitcnt lgkmcnt(0)
	v_pk_mul_f32 v[84:85], v[130:131], v[82:83] op_sel_hi:[1,0]
	v_pk_mul_f32 v[86:87], v[128:129], v[82:83] op_sel_hi:[1,0]
	v_pk_mul_f32 v[84:85], v[84:85], v[84:85]
	v_pk_mul_f32 v[88:89], v[124:125], v[82:83] op_sel_hi:[1,0]
	v_pk_fma_f32 v[84:85], v[86:87], v[86:87], v[84:85]
	v_pk_mul_f32 v[86:87], v[126:127], v[82:83] op_sel_hi:[1,0]
	s_nop 0
	v_pk_mul_f32 v[86:87], v[86:87], v[86:87]
	s_nop 0
	v_pk_fma_f32 v[86:87], v[88:89], v[88:89], v[86:87]
	v_pk_mul_f32 v[88:89], v[120:121], v[82:83] op_sel_hi:[1,0]
	v_pk_add_f32 v[84:85], v[84:85], v[86:87]
	v_pk_mul_f32 v[86:87], v[122:123], v[82:83] op_sel_hi:[1,0]
	s_nop 0
	v_pk_mul_f32 v[86:87], v[86:87], v[86:87]
	s_nop 0
	v_pk_fma_f32 v[86:87], v[88:89], v[88:89], v[86:87]
	s_nop 0
	v_pk_add_f32 v[84:85], v[86:87], v[84:85]
	v_pk_mul_f32 v[86:87], v[118:119], v[82:83] op_sel_hi:[1,0]
	v_pk_mul_f32 v[82:83], v[116:117], v[82:83] op_sel_hi:[1,0]
	v_pk_mul_f32 v[86:87], v[86:87], v[86:87]
	s_nop 0
	v_pk_fma_f32 v[82:83], v[82:83], v[82:83], v[86:87]
	s_nop 0
	v_pk_add_f32 v[82:83], v[82:83], v[84:85]
	s_nop 0
	v_add_f32_e32 v82, v82, v83
	ds_swizzle_b32 v83, v82 offset:swizzle(SWAP,16)
	s_waitcnt lgkmcnt(0)
	v_add_f32_e32 v82, v82, v83
	v_mov_b32_e32 v83, v82
	s_nop 1
	v_permlane32_swap_b32_e32 v82, v83
	s_and_saveexec_b64 s[62:63], s[38:39]
	v_add_f32_e32 v82, v82, v83
	ds_write_b32 v195, v82
	s_or_b64 exec, exec, s[62:63]
	ds_read_b32 v82, v213 offset:128
	s_waitcnt lgkmcnt(0)
	v_pk_mul_f32 v[84:85], v[112:113], v[82:83] op_sel_hi:[1,0]
	v_pk_mul_f32 v[86:87], v[110:111], v[82:83] op_sel_hi:[1,0]
	v_pk_mul_f32 v[84:85], v[84:85], v[84:85]
	v_pk_mul_f32 v[88:89], v[106:107], v[82:83] op_sel_hi:[1,0]
	v_pk_fma_f32 v[84:85], v[86:87], v[86:87], v[84:85]
	v_pk_mul_f32 v[86:87], v[108:109], v[82:83] op_sel_hi:[1,0]
	s_nop 0
	v_pk_mul_f32 v[86:87], v[86:87], v[86:87]
	s_nop 0
	v_pk_fma_f32 v[86:87], v[88:89], v[88:89], v[86:87]
	v_pk_mul_f32 v[88:89], v[102:103], v[82:83] op_sel_hi:[1,0]
	v_pk_add_f32 v[84:85], v[84:85], v[86:87]
	v_pk_mul_f32 v[86:87], v[104:105], v[82:83] op_sel_hi:[1,0]
	s_nop 0
	v_pk_mul_f32 v[86:87], v[86:87], v[86:87]
	s_nop 0
	v_pk_fma_f32 v[86:87], v[88:89], v[88:89], v[86:87]
	s_nop 0
	v_pk_add_f32 v[84:85], v[86:87], v[84:85]
	v_pk_mul_f32 v[86:87], v[100:101], v[82:83] op_sel_hi:[1,0]
	v_pk_mul_f32 v[82:83], v[98:99], v[82:83] op_sel_hi:[1,0]
	v_pk_mul_f32 v[86:87], v[86:87], v[86:87]
	s_nop 0
	v_pk_fma_f32 v[82:83], v[82:83], v[82:83], v[86:87]
	s_nop 0
	v_pk_add_f32 v[82:83], v[82:83], v[84:85]
	s_nop 0
	v_add_f32_e32 v82, v82, v83
	ds_swizzle_b32 v83, v82 offset:swizzle(SWAP,16)
	s_waitcnt lgkmcnt(0)
	v_add_f32_e32 v82, v82, v83
	v_mov_b32_e32 v83, v82
	s_nop 1
	v_permlane32_swap_b32_e32 v82, v83
	s_and_saveexec_b64 s[62:63], s[38:39]
	v_add_f32_e32 v82, v82, v83
	ds_write_b32 v197, v82
	s_or_b64 exec, exec, s[62:63]
	ds_read_b32 v82, v213 offset:192
	s_waitcnt lgkmcnt(0)
	v_pk_mul_f32 v[84:85], v[80:81], v[82:83] op_sel_hi:[1,0]
	v_pk_mul_f32 v[86:87], v[78:79], v[82:83] op_sel_hi:[1,0]
	v_pk_mul_f32 v[84:85], v[84:85], v[84:85]
	v_pk_mul_f32 v[88:89], v[74:75], v[82:83] op_sel_hi:[1,0]
	v_pk_fma_f32 v[84:85], v[86:87], v[86:87], v[84:85]
	v_pk_mul_f32 v[86:87], v[76:77], v[82:83] op_sel_hi:[1,0]
	s_nop 0
	v_pk_mul_f32 v[86:87], v[86:87], v[86:87]
	s_nop 0
	v_pk_fma_f32 v[86:87], v[88:89], v[88:89], v[86:87]
	v_pk_mul_f32 v[88:89], v[70:71], v[82:83] op_sel_hi:[1,0]
	v_pk_add_f32 v[84:85], v[84:85], v[86:87]
	v_pk_mul_f32 v[86:87], v[72:73], v[82:83] op_sel_hi:[1,0]
	s_nop 0
	v_pk_mul_f32 v[86:87], v[86:87], v[86:87]
	s_nop 0
	v_pk_fma_f32 v[86:87], v[88:89], v[88:89], v[86:87]
	s_nop 0
	v_pk_add_f32 v[84:85], v[86:87], v[84:85]
	v_pk_mul_f32 v[86:87], v[68:69], v[82:83] op_sel_hi:[1,0]
	v_pk_mul_f32 v[82:83], v[66:67], v[82:83] op_sel_hi:[1,0]
	v_pk_mul_f32 v[86:87], v[86:87], v[86:87]
	s_nop 0
	v_pk_fma_f32 v[82:83], v[82:83], v[82:83], v[86:87]
	s_nop 0
	v_pk_add_f32 v[82:83], v[82:83], v[84:85]
	s_nop 0
	v_add_f32_e32 v82, v82, v83
	ds_swizzle_b32 v83, v82 offset:swizzle(SWAP,16)
	s_waitcnt lgkmcnt(0)
	v_add_f32_e32 v82, v82, v83
	v_mov_b32_e32 v83, v82
	s_nop 1
	v_permlane32_swap_b32_e32 v82, v83
	s_and_saveexec_b64 s[62:63], s[38:39]
	v_add_f32_e32 v82, v82, v83
	ds_write_b32 v199, v82
	s_or_b64 exec, exec, s[62:63]
	ds_read_b32 v82, v213 offset:512
	s_waitcnt lgkmcnt(0)
	v_pk_mul_f32 v[84:85], v[64:65], v[82:83] op_sel_hi:[1,0]
	v_pk_mul_f32 v[86:87], v[62:63], v[82:83] op_sel_hi:[1,0]
	v_pk_mul_f32 v[84:85], v[84:85], v[84:85]
	v_pk_mul_f32 v[88:89], v[58:59], v[82:83] op_sel_hi:[1,0]
	v_pk_fma_f32 v[84:85], v[86:87], v[86:87], v[84:85]
	v_pk_mul_f32 v[86:87], v[60:61], v[82:83] op_sel_hi:[1,0]
	s_nop 0
	v_pk_mul_f32 v[86:87], v[86:87], v[86:87]
	s_nop 0
	v_pk_fma_f32 v[86:87], v[88:89], v[88:89], v[86:87]
	v_pk_mul_f32 v[88:89], v[54:55], v[82:83] op_sel_hi:[1,0]
	v_pk_add_f32 v[84:85], v[84:85], v[86:87]
	v_pk_mul_f32 v[86:87], v[56:57], v[82:83] op_sel_hi:[1,0]
	s_nop 0
	v_pk_mul_f32 v[86:87], v[86:87], v[86:87]
	s_nop 0
	v_pk_fma_f32 v[86:87], v[88:89], v[88:89], v[86:87]
	s_nop 0
	v_pk_add_f32 v[84:85], v[86:87], v[84:85]
	v_pk_mul_f32 v[86:87], v[52:53], v[82:83] op_sel_hi:[1,0]
	v_pk_mul_f32 v[82:83], v[50:51], v[82:83] op_sel_hi:[1,0]
	v_pk_mul_f32 v[86:87], v[86:87], v[86:87]
	s_nop 0
	v_pk_fma_f32 v[82:83], v[82:83], v[82:83], v[86:87]
	s_nop 0
	v_pk_add_f32 v[82:83], v[82:83], v[84:85]
	s_nop 0
	v_add_f32_e32 v82, v82, v83
	ds_swizzle_b32 v83, v82 offset:swizzle(SWAP,16)
	s_waitcnt lgkmcnt(0)
	v_add_f32_e32 v82, v82, v83
	v_mov_b32_e32 v83, v82
	s_nop 1
	v_permlane32_swap_b32_e32 v82, v83
	s_and_saveexec_b64 s[62:63], s[38:39]
	v_add_f32_e32 v82, v82, v83
	ds_write_b32 v201, v82
	s_or_b64 exec, exec, s[62:63]
	ds_read_b32 v82, v213 offset:576
	s_waitcnt lgkmcnt(0)
	v_pk_mul_f32 v[84:85], v[48:49], v[82:83] op_sel_hi:[1,0]
	v_pk_mul_f32 v[86:87], v[46:47], v[82:83] op_sel_hi:[1,0]
	v_pk_mul_f32 v[84:85], v[84:85], v[84:85]
	v_pk_mul_f32 v[88:89], v[42:43], v[82:83] op_sel_hi:[1,0]
	v_pk_fma_f32 v[84:85], v[86:87], v[86:87], v[84:85]
	v_pk_mul_f32 v[86:87], v[44:45], v[82:83] op_sel_hi:[1,0]
	s_nop 0
	v_pk_mul_f32 v[86:87], v[86:87], v[86:87]
	s_nop 0
	v_pk_fma_f32 v[86:87], v[88:89], v[88:89], v[86:87]
	v_pk_mul_f32 v[88:89], v[38:39], v[82:83] op_sel_hi:[1,0]
	v_pk_add_f32 v[84:85], v[84:85], v[86:87]
	v_pk_mul_f32 v[86:87], v[40:41], v[82:83] op_sel_hi:[1,0]
	s_nop 0
	v_pk_mul_f32 v[86:87], v[86:87], v[86:87]
	s_nop 0
	v_pk_fma_f32 v[86:87], v[88:89], v[88:89], v[86:87]
	s_nop 0
	v_pk_add_f32 v[84:85], v[86:87], v[84:85]
	v_pk_mul_f32 v[86:87], v[36:37], v[82:83] op_sel_hi:[1,0]
	v_pk_mul_f32 v[82:83], v[34:35], v[82:83] op_sel_hi:[1,0]
	v_pk_mul_f32 v[86:87], v[86:87], v[86:87]
	s_nop 0
	v_pk_fma_f32 v[82:83], v[82:83], v[82:83], v[86:87]
	s_nop 0
	v_pk_add_f32 v[82:83], v[82:83], v[84:85]
	s_nop 0
	v_add_f32_e32 v82, v82, v83
	ds_swizzle_b32 v83, v82 offset:swizzle(SWAP,16)
	s_waitcnt lgkmcnt(0)
	v_add_f32_e32 v82, v82, v83
	v_mov_b32_e32 v83, v82
	s_nop 1
	v_permlane32_swap_b32_e32 v82, v83
	s_and_saveexec_b64 s[62:63], s[38:39]
	v_add_f32_e32 v82, v82, v83
	ds_write_b32 v203, v82
	s_or_b64 exec, exec, s[62:63]
	ds_read_b32 v82, v213 offset:640
	s_waitcnt lgkmcnt(0)
	v_pk_mul_f32 v[84:85], v[32:33], v[82:83] op_sel_hi:[1,0]
	v_pk_mul_f32 v[86:87], v[30:31], v[82:83] op_sel_hi:[1,0]
	v_pk_mul_f32 v[84:85], v[84:85], v[84:85]
	v_pk_mul_f32 v[88:89], v[26:27], v[82:83] op_sel_hi:[1,0]
	v_pk_fma_f32 v[84:85], v[86:87], v[86:87], v[84:85]
	v_pk_mul_f32 v[86:87], v[28:29], v[82:83] op_sel_hi:[1,0]
	s_nop 0
	v_pk_mul_f32 v[86:87], v[86:87], v[86:87]
	s_nop 0
	v_pk_fma_f32 v[86:87], v[88:89], v[88:89], v[86:87]
	v_pk_mul_f32 v[88:89], v[22:23], v[82:83] op_sel_hi:[1,0]
	v_pk_add_f32 v[84:85], v[84:85], v[86:87]
	v_pk_mul_f32 v[86:87], v[24:25], v[82:83] op_sel_hi:[1,0]
	s_nop 0
	v_pk_mul_f32 v[86:87], v[86:87], v[86:87]
	s_nop 0
	v_pk_fma_f32 v[86:87], v[88:89], v[88:89], v[86:87]
	s_nop 0
	v_pk_add_f32 v[84:85], v[86:87], v[84:85]
	v_pk_mul_f32 v[86:87], v[20:21], v[82:83] op_sel_hi:[1,0]
	v_pk_mul_f32 v[82:83], v[18:19], v[82:83] op_sel_hi:[1,0]
	v_pk_mul_f32 v[86:87], v[86:87], v[86:87]
	s_nop 0
	v_pk_fma_f32 v[82:83], v[82:83], v[82:83], v[86:87]
	s_nop 0
	v_pk_add_f32 v[82:83], v[82:83], v[84:85]
	s_nop 0
	v_add_f32_e32 v82, v82, v83
	ds_swizzle_b32 v83, v82 offset:swizzle(SWAP,16)
	s_waitcnt lgkmcnt(0)
	v_add_f32_e32 v82, v82, v83
	v_mov_b32_e32 v83, v82
	s_nop 1
	v_permlane32_swap_b32_e32 v82, v83
	s_and_saveexec_b64 s[62:63], s[38:39]
	v_add_f32_e32 v82, v82, v83
	ds_write_b32 v205, v82
	s_or_b64 exec, exec, s[62:63]
	ds_read_b32 v82, v213 offset:704
	s_waitcnt lgkmcnt(0)
	v_pk_mul_f32 v[84:85], v[16:17], v[82:83] op_sel_hi:[1,0]
	v_pk_mul_f32 v[86:87], v[14:15], v[82:83] op_sel_hi:[1,0]
	v_pk_mul_f32 v[84:85], v[84:85], v[84:85]
	v_pk_mul_f32 v[88:89], v[10:11], v[82:83] op_sel_hi:[1,0]
	v_pk_fma_f32 v[84:85], v[86:87], v[86:87], v[84:85]
	v_pk_mul_f32 v[86:87], v[12:13], v[82:83] op_sel_hi:[1,0]
	s_nop 0
	v_pk_mul_f32 v[86:87], v[86:87], v[86:87]
	s_nop 0
	v_pk_fma_f32 v[86:87], v[88:89], v[88:89], v[86:87]
	v_pk_mul_f32 v[88:89], v[6:7], v[82:83] op_sel_hi:[1,0]
	v_pk_add_f32 v[84:85], v[84:85], v[86:87]
	v_pk_mul_f32 v[86:87], v[8:9], v[82:83] op_sel_hi:[1,0]
	s_nop 0
	v_pk_mul_f32 v[86:87], v[86:87], v[86:87]
	s_nop 0
	v_pk_fma_f32 v[86:87], v[88:89], v[88:89], v[86:87]
	s_nop 0
	v_pk_add_f32 v[84:85], v[86:87], v[84:85]
	v_pk_mul_f32 v[86:87], v[4:5], v[82:83] op_sel_hi:[1,0]
	v_pk_mul_f32 v[82:83], v[2:3], v[82:83] op_sel_hi:[1,0]
	v_pk_mul_f32 v[86:87], v[86:87], v[86:87]
	s_nop 0
	v_pk_fma_f32 v[82:83], v[82:83], v[82:83], v[86:87]
	s_nop 0
	v_pk_add_f32 v[82:83], v[82:83], v[84:85]
	s_nop 0
	v_add_f32_e32 v82, v82, v83
	ds_swizzle_b32 v83, v82 offset:swizzle(SWAP,16)
	s_waitcnt lgkmcnt(0)
	v_add_f32_e32 v82, v82, v83
	v_mov_b32_e32 v83, v82
	s_nop 1
	v_permlane32_swap_b32_e32 v82, v83
	s_and_saveexec_b64 s[62:63], s[38:39]
	v_add_f32_e32 v82, v82, v83
	ds_write_b32 v207, v82
	s_or_b64 exec, exec, s[62:63]
	s_waitcnt lgkmcnt(0)
	s_barrier
	global_load_dwordx4 v[94:97], v[168:169], off offset:16
	global_load_dwordx4 v[90:93], v[168:169], off
	global_load_dwordx4 v[82:85], v[168:169], off offset:144
	global_load_dwordx4 v[86:89], v[168:169], off offset:128
	ds_read_b32 v158, v183
	ds_read_b32 v159, v194
	s_lshl_b32 s14, s60, 1
	s_and_b32 s14, s14, 14
	s_lshl_b32 s15, s28, 1
	s_or_b32 s14, s88, s14
	s_waitcnt lgkmcnt(0)
	v_add_f32_e32 v158, v158, v159
	v_fmamk_f32 v158, v158, 0x3c000000, v185
	v_rsq_f32_e32 v160, v158
	ds_read2_b32 v[158:159], v213 offset1:16
	s_and_b32 s15, s15, 0x7fffff0
	s_or_b32 s14, s15, s14
	s_lshl_b32 s15, s28, 2
	s_and_b32 s15, s15, 28
	s_waitcnt lgkmcnt(0)
	v_mul_f32_e32 v158, v158, v160
	v_lshlrev_b64 v[160:161], 12, v[174:175]
	v_lshl_add_u64 v[160:161], s[46:47], 0, v[160:161]
	v_pk_mul_f32 v[144:145], v[144:145], v[158:159] op_sel_hi:[1,0]
	v_pk_mul_f32 v[146:147], v[146:147], v[158:159] op_sel_hi:[1,0]
	v_pk_mul_f32 v[218:219], v[140:141], v[158:159] op_sel_hi:[1,0]
	v_lshl_add_u64 v[160:161], v[160:161], 0, v[114:115]
	v_pk_mul_f32 v[140:141], v[142:143], v[158:159] op_sel_hi:[1,0]
	s_lshl_b32 s14, s14, 5
	s_add_i32 s15, s15, s8
	s_add_i32 s28, s15, s14
	s_ashr_i32 s29, s28, 31
	s_lshl_b64 s[14:15], s[28:29], 9
	s_waitcnt vmcnt(0)
	v_pk_mul_f32 v[142:143], v[94:95], v[218:219]
	v_pk_mul_f32 v[214:215], v[92:93], v[146:147]
	v_pk_mul_f32 v[216:217], v[90:91], v[144:145]
	v_pk_fma_f32 v[218:219], v[90:91], v[144:145], 0 op_sel_hi:[1,1,0]
	v_cvt_pk_bf16_f32 v144, v216, v217
	v_cvt_pk_bf16_f32 v145, v214, v215
	v_pk_mul_f32 v[140:141], v[96:97], v[140:141]
	v_pk_fma_f32 v[220:221], v[92:93], v[146:147], 0 op_sel_hi:[1,1,0]
	v_cvt_pk_bf16_f32 v146, v142, v143
	v_cvt_pk_bf16_f32 v147, v140, v141
	ds_bpermute_b32 v238, v250, v144
	ds_bpermute_b32 v239, v250, v145
	ds_bpermute_b32 v240, v250, v146
	ds_bpermute_b32 v241, v250, v147
	ds_bpermute_b32 v242, v250, v160
	s_nop 1
	v_pk_mul_f32 v[144:145], v[136:137], v[158:159] op_sel_hi:[1,0]
	v_pk_mul_f32 v[136:137], v[138:139], v[158:159] op_sel_hi:[1,0]
	v_pk_mul_f32 v[138:139], v[86:87], v[144:145]
	v_pk_mul_f32 v[144:145], v[132:133], v[158:159] op_sel_hi:[1,0]
	v_pk_mul_f32 v[132:133], v[134:135], v[158:159] op_sel_hi:[1,0]
	v_pk_mul_f32 v[136:137], v[88:89], v[136:137]
	v_pk_mul_f32 v[132:133], v[84:85], v[132:133]
	v_pk_mul_f32 v[134:135], v[82:83], v[144:145]
	v_cvt_pk_bf16_f32 v144, v138, v139
	v_cvt_pk_bf16_f32 v145, v136, v137
	v_cvt_pk_bf16_f32 v147, v132, v133
	s_nop 0
	v_cvt_pk_bf16_f32 v146, v134, v135
	ds_bpermute_b32 v244, v250, v144
	ds_bpermute_b32 v245, v250, v145
	ds_bpermute_b32 v246, v250, v146
	ds_bpermute_b32 v247, v250, v147
	ds_bpermute_b32 v248, v250, v160
	ds_read_b32 v144, v195
	ds_read_b32 v145, v196
	v_lshlrev_b64 v[146:147], 12, v[180:181]
	v_lshl_add_u64 v[146:147], s[46:47], 0, v[146:147]
	v_lshl_add_u64 v[146:147], v[146:147], 0, v[114:115]
	s_waitcnt lgkmcnt(0)
	v_add_f32_e32 v144, v144, v145
	v_fmamk_f32 v144, v144, 0x3c000000, v185
	v_rsq_f32_e32 v144, v144
	s_nop 0
	v_mul_f32_e32 v144, v159, v144
	v_pk_mul_f32 v[128:129], v[128:129], v[144:145] op_sel_hi:[1,0]
	v_pk_mul_f32 v[130:131], v[130:131], v[144:145] op_sel_hi:[1,0]
	v_pk_mul_f32 v[160:161], v[90:91], v[128:129]
	v_pk_mul_f32 v[158:159], v[92:93], v[130:131]
	v_pk_mul_f32 v[180:181], v[124:125], v[144:145] op_sel_hi:[1,0]
	v_pk_mul_f32 v[124:125], v[126:127], v[144:145] op_sel_hi:[1,0]
	v_pk_fma_f32 v[214:215], v[90:91], v[128:129], v[218:219]
	v_cvt_pk_bf16_f32 v128, v160, v161
	v_cvt_pk_bf16_f32 v129, v158, v159
	v_pk_mul_f32 v[124:125], v[96:97], v[124:125]
	v_pk_mul_f32 v[126:127], v[94:95], v[180:181]
	v_pk_fma_f32 v[180:181], v[92:93], v[130:131], v[220:221]
	v_cvt_pk_bf16_f32 v130, v126, v127
	v_cvt_pk_bf16_f32 v131, v124, v125
	s_waitcnt lgkmcnt(7)
	v_subrev_u32_e32 v242, s82, v242
	global_store_dwordx4 v242, v[238:241], s[82:83]
	ds_bpermute_b32 v232, v250, v128
	ds_bpermute_b32 v233, v250, v129
	ds_bpermute_b32 v234, v250, v130
	ds_bpermute_b32 v235, v250, v131
	ds_bpermute_b32 v236, v250, v146
	s_nop 1
	v_pk_mul_f32 v[128:129], v[120:121], v[144:145] op_sel_hi:[1,0]
	v_pk_mul_f32 v[120:121], v[122:123], v[144:145] op_sel_hi:[1,0]
	v_pk_mul_f32 v[122:123], v[86:87], v[128:129]
	v_pk_mul_f32 v[128:129], v[116:117], v[144:145] op_sel_hi:[1,0]
	v_pk_mul_f32 v[116:117], v[118:119], v[144:145] op_sel_hi:[1,0]
	v_pk_mul_f32 v[120:121], v[88:89], v[120:121]
	v_pk_mul_f32 v[116:117], v[84:85], v[116:117]
	v_pk_mul_f32 v[118:119], v[82:83], v[128:129]
	v_cvt_pk_bf16_f32 v128, v122, v123
	v_cvt_pk_bf16_f32 v129, v120, v121
	v_cvt_pk_bf16_f32 v131, v116, v117
	s_nop 0
	v_cvt_pk_bf16_f32 v130, v118, v119
	s_waitcnt lgkmcnt(7)
	v_subrev_u32_e32 v248, s82, v248
	global_store_dwordx4 v248, v[244:247], s[82:83] offset:64
	ds_bpermute_b32 v238, v250, v128
	ds_bpermute_b32 v239, v250, v129
	ds_bpermute_b32 v240, v250, v130
	ds_bpermute_b32 v241, v250, v131
	ds_bpermute_b32 v242, v250, v146
	ds_read_b32 v128, v197
	ds_read_b32 v129, v198
	s_waitcnt lgkmcnt(0)
	v_add_f32_e32 v128, v128, v129
	v_fmamk_f32 v128, v128, 0x3c000000, v185
	v_rsq_f32_e32 v130, v128
	ds_read2_b32 v[128:129], v213 offset0:32 offset1:48
	s_waitcnt lgkmcnt(0)
	v_mul_f32_e32 v128, v128, v130
	v_lshlrev_b64 v[130:131], 12, v[178:179]
	v_pk_mul_f32 v[110:111], v[110:111], v[128:129] op_sel_hi:[1,0]
	v_lshl_add_u64 v[130:131], s[46:47], 0, v[130:131]
	v_pk_mul_f32 v[112:113], v[112:113], v[128:129] op_sel_hi:[1,0]
	v_pk_mul_f32 v[144:145], v[90:91], v[110:111]
	v_lshl_add_u64 v[130:131], v[130:131], 0, v[114:115]
	v_pk_mul_f32 v[146:147], v[92:93], v[112:113]
	v_pk_mul_f32 v[158:159], v[106:107], v[128:129] op_sel_hi:[1,0]
	v_pk_mul_f32 v[106:107], v[108:109], v[128:129] op_sel_hi:[1,0]
	v_cvt_pk_bf16_f32 v144, v144, v145
	v_cvt_pk_bf16_f32 v145, v146, v147
	v_pk_mul_f32 v[108:109], v[94:95], v[158:159]
	v_pk_mul_f32 v[106:107], v[96:97], v[106:107]
	v_cvt_pk_bf16_f32 v146, v108, v109
	v_pk_fma_f32 v[110:111], v[90:91], v[110:111], v[214:215]
	v_cvt_pk_bf16_f32 v147, v106, v107
	s_waitcnt lgkmcnt(8)
	v_subrev_u32_e32 v236, s82, v236
	global_store_dwordx4 v236, v[232:235], s[82:83]
	ds_bpermute_b32 v244, v250, v144
	ds_bpermute_b32 v245, v250, v145
	ds_bpermute_b32 v246, v250, v146
	ds_bpermute_b32 v247, v250, v147
	ds_bpermute_b32 v248, v250, v130
	v_pk_fma_f32 v[112:113], v[92:93], v[112:113], v[180:181]
	s_nop 0
	v_pk_mul_f32 v[144:145], v[102:103], v[128:129] op_sel_hi:[1,0]
	v_pk_mul_f32 v[102:103], v[104:105], v[128:129] op_sel_hi:[1,0]
	v_pk_mul_f32 v[104:105], v[86:87], v[144:145]
	v_pk_mul_f32 v[144:145], v[98:99], v[128:129] op_sel_hi:[1,0]
	v_pk_mul_f32 v[98:99], v[100:101], v[128:129] op_sel_hi:[1,0]
	v_pk_mul_f32 v[102:103], v[88:89], v[102:103]
	v_pk_mul_f32 v[98:99], v[84:85], v[98:99]
	v_pk_mul_f32 v[100:101], v[82:83], v[144:145]
	v_cvt_pk_bf16_f32 v144, v104, v105
	v_cvt_pk_bf16_f32 v145, v102, v103
	v_cvt_pk_bf16_f32 v147, v98, v99
	s_nop 0
	v_cvt_pk_bf16_f32 v146, v100, v101
	s_waitcnt lgkmcnt(8)
	v_subrev_u32_e32 v242, s82, v242
	global_store_dwordx4 v242, v[238:241], s[82:83] offset:64
	ds_bpermute_b32 v232, v250, v144
	ds_bpermute_b32 v233, v250, v145
	ds_bpermute_b32 v234, v250, v146
	ds_bpermute_b32 v235, v250, v147
	ds_bpermute_b32 v236, v250, v130
	ds_read_b32 v128, v199
	ds_read_b32 v130, v200
	s_waitcnt lgkmcnt(0)
	v_add_f32_e32 v128, v128, v130
	v_fmamk_f32 v128, v128, 0x3c000000, v185
	v_rsq_f32_e32 v128, v128
	v_lshlrev_b64 v[130:131], 12, v[176:177]
	v_lshl_add_u64 v[130:131], s[46:47], 0, v[130:131]
	v_lshl_add_u64 v[130:131], v[130:131], 0, v[114:115]
	v_mul_f32_e32 v128, v129, v128
	v_pk_mul_f32 v[144:145], v[78:79], v[128:129] op_sel_hi:[1,0]
	v_pk_mul_f32 v[80:81], v[80:81], v[128:129] op_sel_hi:[1,0]
	v_pk_mul_f32 v[74:75], v[74:75], v[128:129] op_sel_hi:[1,0]
	v_pk_mul_f32 v[76:77], v[76:77], v[128:129] op_sel_hi:[1,0]
	v_pk_mul_f32 v[146:147], v[92:93], v[80:81]
	v_pk_mul_f32 v[158:159], v[90:91], v[144:145]
	v_pk_mul_f32 v[76:77], v[96:97], v[76:77]
	v_pk_mul_f32 v[78:79], v[94:95], v[74:75]
	v_pk_fma_f32 v[160:161], v[92:93], v[80:81], v[112:113]
	v_pk_fma_f32 v[80:81], v[90:91], v[144:145], v[110:111]
	v_cvt_pk_bf16_f32 v110, v158, v159
	v_cvt_pk_bf16_f32 v111, v146, v147
	v_cvt_pk_bf16_f32 v112, v78, v79
	v_cvt_pk_bf16_f32 v113, v76, v77
	v_pk_mul_f32 v[70:71], v[70:71], v[128:129] op_sel_hi:[1,0]
	v_pk_mul_f32 v[72:73], v[72:73], v[128:129] op_sel_hi:[1,0]
	v_pk_mul_f32 v[66:67], v[66:67], v[128:129] op_sel_hi:[1,0]
	v_pk_mul_f32 v[68:69], v[68:69], v[128:129] op_sel_hi:[1,0]
	s_waitcnt lgkmcnt(7)
	v_subrev_u32_e32 v248, s82, v248
	global_store_dwordx4 v248, v[244:247], s[82:83]
	ds_bpermute_b32 v238, v250, v110
	ds_bpermute_b32 v239, v250, v111
	ds_bpermute_b32 v240, v250, v112
	ds_bpermute_b32 v241, v250, v113
	ds_bpermute_b32 v242, v250, v130
	v_pk_mul_f32 v[72:73], v[88:89], v[72:73]
	v_pk_mul_f32 v[74:75], v[86:87], v[70:71]
	v_pk_mul_f32 v[68:69], v[84:85], v[68:69]
	v_pk_mul_f32 v[70:71], v[82:83], v[66:67]
	v_cvt_pk_bf16_f32 v110, v74, v75
	v_cvt_pk_bf16_f32 v111, v72, v73
	v_cvt_pk_bf16_f32 v113, v68, v69
	v_lshl_add_u64 v[66:67], v[166:167], 0, s[14:15]
	v_cvt_pk_bf16_f32 v112, v70, v71
	s_waitcnt lgkmcnt(7)
	v_subrev_u32_e32 v236, s82, v236
	global_store_dwordx4 v236, v[232:235], s[82:83] offset:64
	ds_bpermute_b32 v244, v250, v110
	ds_bpermute_b32 v245, v250, v111
	ds_bpermute_b32 v246, v250, v112
	ds_bpermute_b32 v247, v250, v113
	ds_bpermute_b32 v248, v250, v130
	ds_swizzle_b32 v110, v80 offset:swizzle(SWAP,1)
	ds_swizzle_b32 v111, v81 offset:swizzle(SWAP,1)
	ds_swizzle_b32 v112, v160 offset:swizzle(SWAP,1)
	ds_swizzle_b32 v113, v161 offset:swizzle(SWAP,1)
	s_waitcnt lgkmcnt(2)
	v_pk_add_f32 v[80:81], v[80:81], v[110:111]
	ds_swizzle_b32 v110, v80 offset:swizzle(SWAP,2)
	s_waitcnt lgkmcnt(1)
	v_pk_add_f32 v[112:113], v[160:161], v[112:113]
	ds_swizzle_b32 v111, v81 offset:swizzle(SWAP,2)
	ds_swizzle_b32 v128, v112 offset:swizzle(SWAP,2)
	ds_swizzle_b32 v129, v113 offset:swizzle(SWAP,2)
	s_waitcnt lgkmcnt(2)
	v_pk_add_f32 v[80:81], v[80:81], v[110:111]
	ds_swizzle_b32 v110, v80 offset:swizzle(SWAP,4)
	s_waitcnt lgkmcnt(1)
	v_pk_add_f32 v[112:113], v[112:113], v[128:129]
	ds_swizzle_b32 v111, v81 offset:swizzle(SWAP,4)
	ds_swizzle_b32 v128, v112 offset:swizzle(SWAP,4)
	ds_swizzle_b32 v129, v113 offset:swizzle(SWAP,4)
	s_waitcnt lgkmcnt(2)
	v_pk_add_f32 v[80:81], v[80:81], v[110:111]
	ds_swizzle_b32 v110, v80 offset:swizzle(SWAP,8)
	s_waitcnt lgkmcnt(1)
	v_pk_add_f32 v[112:113], v[112:113], v[128:129]
	ds_swizzle_b32 v111, v81 offset:swizzle(SWAP,8)
	ds_swizzle_b32 v128, v112 offset:swizzle(SWAP,8)
	ds_swizzle_b32 v129, v113 offset:swizzle(SWAP,8)
	s_waitcnt lgkmcnt(15)
	v_subrev_u32_e32 v242, s82, v242
	global_store_dwordx4 v242, v[238:241], s[82:83]
	s_waitcnt lgkmcnt(15)
	v_subrev_u32_e32 v248, s82, v248
	global_store_dwordx4 v248, v[244:247], s[82:83] offset:64
	s_and_saveexec_b64 s[60:61], s[40:41]
	s_cbranch_execz .LBB0_196
	s_waitcnt lgkmcnt(0)
	v_pk_add_f32 v[112:113], v[112:113], v[128:129]
	v_pk_add_f32 v[110:111], v[80:81], v[110:111]
	global_store_dwordx4 v[66:67], v[110:113], off

.LBB0_202:
	s_or_b64 exec, exec, s[60:61]
	ds_read_b32 v66, v201
	ds_read_b32 v67, v202
	ds_read2_b32 v[68:69], v213 offset0:128 offset1:144
	s_mov_b64 s[14:15], 0x80000
	s_waitcnt lgkmcnt(1)
	v_add_f32_e32 v66, v66, v67
	v_fmamk_f32 v66, v66, 0x3c000000, v185
	v_rsq_f32_e32 v66, v66
	s_waitcnt lgkmcnt(0)
	v_mul_f32_e32 v68, v68, v66
	v_lshlrev_b64 v[66:67], 12, v[174:175]
	v_lshl_add_u64 v[66:67], s[46:47], 0, v[66:67]
	v_lshl_add_u64 v[66:67], v[66:67], 0, v[114:115]
	v_pk_mul_f32 v[64:65], v[64:65], v[68:69] op_sel_hi:[1,0]
	v_lshl_add_u64 v[70:71], v[66:67], 0, s[14:15]
	v_pk_mul_f32 v[62:63], v[62:63], v[68:69] op_sel_hi:[1,0]
	v_pk_mul_f32 v[72:73], v[92:93], v[64:65]
	v_pk_mul_f32 v[76:77], v[58:59], v[68:69] op_sel_hi:[1,0]
	s_mov_b32 s14, 0x80000
	v_pk_mul_f32 v[74:75], v[90:91], v[62:63]
	v_pk_mul_f32 v[58:59], v[60:61], v[68:69] op_sel_hi:[1,0]
	v_pk_mul_f32 v[60:61], v[94:95], v[76:77]
	v_pk_fma_f32 v[76:77], v[90:91], v[62:63], 0 op_sel_hi:[1,1,0]
	v_cvt_pk_bf16_f32 v63, v72, v73
	v_add_co_u32_e32 v72, vcc, s14, v66
	v_cvt_pk_bf16_f32 v62, v74, v75
	v_pk_mul_f32 v[58:59], v[96:97], v[58:59]
	s_nop 0
	v_addc_co_u32_e32 v73, vcc, 0, v67, vcc
	v_pk_fma_f32 v[78:79], v[92:93], v[64:65], 0 op_sel_hi:[1,1,0]
	v_cvt_pk_bf16_f32 v64, v60, v61
	v_cvt_pk_bf16_f32 v65, v58, v59
	ds_bpermute_b32 v232, v250, v62
	ds_bpermute_b32 v233, v250, v63
	ds_bpermute_b32 v234, v250, v64
	ds_bpermute_b32 v235, v250, v65
	ds_bpermute_b32 v236, v250, v72
	s_mov_b64 s[14:15], 0x90000
	s_nop 0
	v_pk_mul_f32 v[62:63], v[54:55], v[68:69] op_sel_hi:[1,0]
	v_pk_mul_f32 v[54:55], v[56:57], v[68:69] op_sel_hi:[1,0]
	v_pk_mul_f32 v[56:57], v[86:87], v[62:63]
	v_pk_mul_f32 v[62:63], v[50:51], v[68:69] op_sel_hi:[1,0]
	v_pk_mul_f32 v[50:51], v[52:53], v[68:69] op_sel_hi:[1,0]
	v_pk_mul_f32 v[54:55], v[88:89], v[54:55]
	v_pk_mul_f32 v[50:51], v[84:85], v[50:51]
	v_pk_mul_f32 v[52:53], v[82:83], v[62:63]
	v_cvt_pk_bf16_f32 v62, v56, v57
	v_cvt_pk_bf16_f32 v63, v54, v55
	v_cvt_pk_bf16_f32 v65, v50, v51
	s_nop 0
	v_cvt_pk_bf16_f32 v64, v52, v53
	ds_bpermute_b32 v238, v250, v62
	ds_bpermute_b32 v239, v250, v63
	ds_bpermute_b32 v240, v250, v64
	ds_bpermute_b32 v241, v250, v65
	ds_bpermute_b32 v242, v250, v70
	ds_read_b32 v62, v203
	ds_read_b32 v63, v204
	v_lshl_add_u64 v[64:65], v[66:67], 0, s[14:15]
	s_mov_b32 s14, 0x90000
	s_waitcnt lgkmcnt(0)
	v_add_f32_e32 v62, v62, v63
	v_fmamk_f32 v62, v62, 0x3c000000, v185
	v_rsq_f32_e32 v62, v62
	s_nop 0
	v_mul_f32_e32 v62, v69, v62
	v_pk_mul_f32 v[48:49], v[48:49], v[62:63] op_sel_hi:[1,0]
	v_pk_mul_f32 v[46:47], v[46:47], v[62:63] op_sel_hi:[1,0]
	v_pk_mul_f32 v[68:69], v[92:93], v[48:49]
	v_pk_mul_f32 v[70:71], v[90:91], v[46:47]
	v_pk_fma_f32 v[74:75], v[90:91], v[46:47], v[76:77]
	v_cvt_pk_bf16_f32 v47, v68, v69
	v_add_co_u32_e32 v68, vcc, s14, v66
	v_pk_mul_f32 v[72:73], v[42:43], v[62:63] op_sel_hi:[1,0]
	v_pk_mul_f32 v[42:43], v[44:45], v[62:63] op_sel_hi:[1,0]
	v_cvt_pk_bf16_f32 v46, v70, v71
	v_addc_co_u32_e32 v69, vcc, 0, v67, vcc
	v_pk_mul_f32 v[42:43], v[96:97], v[42:43]
	v_pk_mul_f32 v[44:45], v[94:95], v[72:73]
	v_pk_fma_f32 v[72:73], v[92:93], v[48:49], v[78:79]
	v_cvt_pk_bf16_f32 v48, v44, v45
	v_cvt_pk_bf16_f32 v49, v42, v43
	s_waitcnt lgkmcnt(7)
	v_subrev_u32_e32 v236, s82, v236
	global_store_dwordx4 v236, v[232:235], s[82:83]
	ds_bpermute_b32 v244, v250, v46
	ds_bpermute_b32 v245, v250, v47
	ds_bpermute_b32 v246, v250, v48
	ds_bpermute_b32 v247, v250, v49
	ds_bpermute_b32 v248, v250, v68
	s_mov_b64 s[14:15], 0xa0000
	s_nop 0
	v_pk_mul_f32 v[46:47], v[38:39], v[62:63] op_sel_hi:[1,0]
	v_pk_mul_f32 v[38:39], v[40:41], v[62:63] op_sel_hi:[1,0]
	v_pk_mul_f32 v[40:41], v[86:87], v[46:47]
	v_pk_mul_f32 v[46:47], v[34:35], v[62:63] op_sel_hi:[1,0]
	v_pk_mul_f32 v[34:35], v[36:37], v[62:63] op_sel_hi:[1,0]
	v_pk_mul_f32 v[38:39], v[88:89], v[38:39]
	v_pk_mul_f32 v[34:35], v[84:85], v[34:35]
	v_pk_mul_f32 v[36:37], v[82:83], v[46:47]
	v_cvt_pk_bf16_f32 v46, v40, v41
	v_cvt_pk_bf16_f32 v47, v38, v39
	v_cvt_pk_bf16_f32 v49, v34, v35
	s_nop 0
	v_cvt_pk_bf16_f32 v48, v36, v37
	s_waitcnt lgkmcnt(7)
	v_subrev_u32_e32 v242, s82, v242
	global_store_dwordx4 v242, v[238:241], s[82:83] offset:64
	ds_bpermute_b32 v232, v250, v46
	ds_bpermute_b32 v233, v250, v47
	ds_bpermute_b32 v234, v250, v48
	ds_bpermute_b32 v235, v250, v49
	ds_bpermute_b32 v236, v250, v64
	ds_read_b32 v46, v205
	ds_read_b32 v47, v206
	s_waitcnt lgkmcnt(0)
	v_add_f32_e32 v46, v46, v47
	v_fmamk_f32 v46, v46, 0x3c000000, v185
	v_rsq_f32_e32 v48, v46
	ds_read2_b32 v[46:47], v213 offset0:160 offset1:176
	s_waitcnt lgkmcnt(0)
	v_mul_f32_e32 v46, v46, v48
	v_lshl_add_u64 v[48:49], v[66:67], 0, s[14:15]
	v_pk_mul_f32 v[30:31], v[30:31], v[46:47] op_sel_hi:[1,0]
	v_pk_mul_f32 v[68:69], v[26:27], v[46:47] op_sel_hi:[1,0]
	s_mov_b32 s14, 0xa0000
	v_pk_mul_f32 v[32:33], v[32:33], v[46:47] op_sel_hi:[1,0]
	v_pk_mul_f32 v[62:63], v[90:91], v[30:31]
	v_pk_mul_f32 v[26:27], v[28:29], v[46:47] op_sel_hi:[1,0]
	v_pk_mul_f32 v[28:29], v[94:95], v[68:69]
	v_add_co_u32_e32 v68, vcc, s14, v66
	v_pk_mul_f32 v[64:65], v[92:93], v[32:33]
	v_cvt_pk_bf16_f32 v62, v62, v63
	s_nop 0
	v_addc_co_u32_e32 v69, vcc, 0, v67, vcc
	v_cvt_pk_bf16_f32 v63, v64, v65
	v_pk_mul_f32 v[26:27], v[96:97], v[26:27]
	v_cvt_pk_bf16_f32 v64, v28, v29
	s_mov_b64 s[14:15], 0xb0000
	v_cvt_pk_bf16_f32 v65, v26, v27
	s_waitcnt lgkmcnt(8)
	v_subrev_u32_e32 v248, s82, v248
	global_store_dwordx4 v248, v[244:247], s[82:83]
	ds_bpermute_b32 v238, v250, v62
	ds_bpermute_b32 v239, v250, v63
	ds_bpermute_b32 v240, v250, v64
	ds_bpermute_b32 v241, v250, v65
	ds_bpermute_b32 v242, v250, v68
	v_pk_fma_f32 v[30:31], v[90:91], v[30:31], v[74:75]
	v_pk_fma_f32 v[32:33], v[92:93], v[32:33], v[72:73]
	v_pk_mul_f32 v[62:63], v[22:23], v[46:47] op_sel_hi:[1,0]
	v_pk_mul_f32 v[22:23], v[24:25], v[46:47] op_sel_hi:[1,0]
	v_pk_mul_f32 v[24:25], v[86:87], v[62:63]
	v_pk_mul_f32 v[62:63], v[18:19], v[46:47] op_sel_hi:[1,0]
	v_pk_mul_f32 v[18:19], v[20:21], v[46:47] op_sel_hi:[1,0]
	v_pk_mul_f32 v[22:23], v[88:89], v[22:23]
	v_pk_mul_f32 v[18:19], v[84:85], v[18:19]
	v_pk_mul_f32 v[20:21], v[82:83], v[62:63]
	v_cvt_pk_bf16_f32 v62, v24, v25
	v_cvt_pk_bf16_f32 v63, v22, v23
	v_cvt_pk_bf16_f32 v65, v18, v19
	s_nop 0
	v_cvt_pk_bf16_f32 v64, v20, v21
	s_waitcnt lgkmcnt(8)
	v_subrev_u32_e32 v236, s82, v236
	global_store_dwordx4 v236, v[232:235], s[82:83] offset:64
	ds_bpermute_b32 v244, v250, v62
	ds_bpermute_b32 v245, v250, v63
	ds_bpermute_b32 v246, v250, v64
	ds_bpermute_b32 v247, v250, v65
	ds_bpermute_b32 v248, v250, v48
	ds_read_b32 v46, v207
	ds_read_b32 v48, v208
	s_waitcnt lgkmcnt(0)
	v_add_f32_e32 v46, v46, v48
	v_fmamk_f32 v46, v46, 0x3c000000, v185
	v_rsq_f32_e32 v46, v46
	v_lshl_add_u64 v[48:49], v[66:67], 0, s[14:15]
	s_mov_b32 s14, 0xb0000
	v_mul_f32_e32 v46, v47, v46
	v_pk_mul_f32 v[10:11], v[10:11], v[46:47] op_sel_hi:[1,0]
	v_pk_mul_f32 v[62:63], v[14:15], v[46:47] op_sel_hi:[1,0]
	v_pk_mul_f32 v[16:17], v[16:17], v[46:47] op_sel_hi:[1,0]
	v_pk_mul_f32 v[12:13], v[12:13], v[46:47] op_sel_hi:[1,0]
	v_pk_mul_f32 v[14:15], v[94:95], v[10:11]
	v_add_co_u32_e32 v10, vcc, s14, v66
	v_pk_mul_f32 v[64:65], v[92:93], v[16:17]
	v_pk_mul_f32 v[68:69], v[90:91], v[62:63]
	v_pk_mul_f32 v[12:13], v[96:97], v[12:13]
	v_pk_fma_f32 v[70:71], v[92:93], v[16:17], v[32:33]
	v_pk_fma_f32 v[16:17], v[90:91], v[62:63], v[30:31]
	v_cvt_pk_bf16_f32 v30, v68, v69
	v_cvt_pk_bf16_f32 v31, v64, v65
	v_cvt_pk_bf16_f32 v32, v14, v15
	v_cvt_pk_bf16_f32 v33, v12, v13
	v_addc_co_u32_e32 v11, vcc, 0, v67, vcc
	v_pk_mul_f32 v[6:7], v[6:7], v[46:47] op_sel_hi:[1,0]
	v_pk_mul_f32 v[8:9], v[8:9], v[46:47] op_sel_hi:[1,0]
	v_pk_mul_f32 v[2:3], v[2:3], v[46:47] op_sel_hi:[1,0]
	v_pk_mul_f32 v[4:5], v[4:5], v[46:47] op_sel_hi:[1,0]
	s_waitcnt lgkmcnt(7)
	v_subrev_u32_e32 v242, s82, v242
	global_store_dwordx4 v242, v[238:241], s[82:83]
	ds_bpermute_b32 v232, v250, v30
	ds_bpermute_b32 v233, v250, v31
	ds_bpermute_b32 v234, v250, v32
	ds_bpermute_b32 v235, v250, v33
	ds_bpermute_b32 v236, v250, v10
	v_pk_mul_f32 v[8:9], v[88:89], v[8:9]
	v_pk_mul_f32 v[10:11], v[86:87], v[6:7]
	v_pk_mul_f32 v[4:5], v[84:85], v[4:5]
	v_pk_mul_f32 v[6:7], v[82:83], v[2:3]
	v_cvt_pk_bf16_f32 v30, v10, v11
	v_cvt_pk_bf16_f32 v31, v8, v9
	v_cvt_pk_bf16_f32 v33, v4, v5
	s_add_i32 s14, s28, 2
	v_cvt_pk_bf16_f32 v32, v6, v7
	s_waitcnt lgkmcnt(7)
	v_subrev_u32_e32 v248, s82, v248
	global_store_dwordx4 v248, v[244:247], s[82:83] offset:64
	ds_bpermute_b32 v238, v250, v30
	ds_bpermute_b32 v239, v250, v31
	ds_bpermute_b32 v240, v250, v32
	ds_bpermute_b32 v241, v250, v33
	ds_bpermute_b32 v242, v250, v48
	ds_swizzle_b32 v30, v16 offset:swizzle(SWAP,1)
	ds_swizzle_b32 v31, v17 offset:swizzle(SWAP,1)
	ds_swizzle_b32 v32, v70 offset:swizzle(SWAP,1)
	ds_swizzle_b32 v33, v71 offset:swizzle(SWAP,1)
	s_ashr_i32 s15, s14, 31
	s_lshl_b64 s[14:15], s[14:15], 9
	s_waitcnt lgkmcnt(2)
	v_pk_add_f32 v[16:17], v[16:17], v[30:31]
	ds_swizzle_b32 v30, v16 offset:swizzle(SWAP,2)
	s_waitcnt lgkmcnt(1)
	v_pk_add_f32 v[32:33], v[70:71], v[32:33]
	ds_swizzle_b32 v31, v17 offset:swizzle(SWAP,2)
	ds_swizzle_b32 v46, v32 offset:swizzle(SWAP,2)
	ds_swizzle_b32 v47, v33 offset:swizzle(SWAP,2)
	v_lshl_add_u64 v[2:3], v[166:167], 0, s[14:15]
	s_waitcnt lgkmcnt(2)
	v_pk_add_f32 v[16:17], v[16:17], v[30:31]
	ds_swizzle_b32 v30, v16 offset:swizzle(SWAP,4)
	s_waitcnt lgkmcnt(1)
	v_pk_add_f32 v[32:33], v[32:33], v[46:47]
	ds_swizzle_b32 v31, v17 offset:swizzle(SWAP,4)
	ds_swizzle_b32 v46, v32 offset:swizzle(SWAP,4)
	ds_swizzle_b32 v47, v33 offset:swizzle(SWAP,4)
	s_waitcnt lgkmcnt(2)
	v_pk_add_f32 v[16:17], v[16:17], v[30:31]
	ds_swizzle_b32 v30, v16 offset:swizzle(SWAP,8)
	s_waitcnt lgkmcnt(1)
	v_pk_add_f32 v[32:33], v[32:33], v[46:47]
	ds_swizzle_b32 v31, v17 offset:swizzle(SWAP,8)
	ds_swizzle_b32 v46, v32 offset:swizzle(SWAP,8)
	ds_swizzle_b32 v47, v33 offset:swizzle(SWAP,8)
	s_waitcnt lgkmcnt(15)
	v_subrev_u32_e32 v236, s82, v236
	global_store_dwordx4 v236, v[232:235], s[82:83]
	s_waitcnt lgkmcnt(15)
	v_subrev_u32_e32 v242, s82, v242
	global_store_dwordx4 v242, v[238:241], s[82:83] offset:64
	s_and_saveexec_b64 s[28:29], s[40:41]
	s_cbranch_execz .LBB0_204
	s_waitcnt lgkmcnt(0)
	v_pk_add_f32 v[32:33], v[32:33], v[46:47]
	v_pk_add_f32 v[30:31], v[16:17], v[30:31]
	global_store_dwordx4 v[2:3], v[30:33], off

.LBB0_349:
	v_mbcnt_lo_u32_b32 v250, -1, 0
	v_mbcnt_hi_u32_b32 v250, -1, v250
	v_lshrrev_b32_e32 v251, 2, v250
	v_and_b32_e32 v250, 3, v250
	v_lshl_add_u32 v250, v250, 4, v251
	v_lshlrev_b32_e32 v250, 2, v250
	s_lshl_b32 s14, s14, 10
	v_add_u32_e32 v176, s14, v174
	ds_read_b32 v154, v176
	s_lshl_b32 s15, s28, 8
	s_ashr_i32 s58, s28, 3
	s_and_b32 s14, s15, 0x700
	v_readlane_b32 s70, v255, 13
	v_readlane_b32 s74, v255, 15
	v_lshl_add_u32 v152, s40, 8, v1
	v_or_b32_e32 v177, s14, v173
	s_cmp_lg_u32 s58, 1
	s_mov_b64 s[40:41], -1
	v_readlane_b32 s71, v255, 14
	v_readlane_b32 s75, v255, 16
	s_cbranch_scc0 .LBB0_384
	s_cmp_lt_u32 s28, 8
	s_cselect_b64 s[56:57], -1, 0
	s_cmp_gt_u32 s28, 7
	s_waitcnt lgkmcnt(0)
	v_pk_mul_f32 v[134:135], v[130:131], v[154:155] op_sel_hi:[1,0]
	v_pk_mul_f32 v[166:167], v[128:129], v[154:155] op_sel_hi:[1,0]
	v_pk_mul_f32 v[138:139], v[126:127], v[154:155] op_sel_hi:[1,0]
	v_pk_mul_f32 v[168:169], v[124:125], v[154:155] op_sel_hi:[1,0]
	s_cbranch_scc1 .LBB0_352
	v_max_f32_e32 v114, v166, v166
	v_max_f32_e32 v132, 0xc2a00000, v114
	v_max_f32_e32 v114, v168, v168
	v_max_f32_e32 v136, 0xc2a00000, v114
	v_mul_f32_e32 v114, 0xbfb8aa3b, v132
	v_exp_f32_e32 v114, v114
	v_mul_f32_e32 v133, 0xbfb8aa3b, v136
	v_exp_f32_e32 v133, v133
	v_max_f32_e32 v137, v169, v169
	v_add_f32_e32 v114, 1.0, v114
	v_rcp_f32_e32 v158, v114
	v_add_f32_e32 v114, 1.0, v133
	v_max_f32_e32 v133, v167, v167
	v_max_f32_e32 v133, 0xc2a00000, v133
	v_max_f32_e32 v137, 0xc2a00000, v137
	v_mul_f32_e32 v153, 0xbfb8aa3b, v133
	v_exp_f32_e32 v153, v153
	v_mul_f32_e32 v155, 0xbfb8aa3b, v137
	v_exp_f32_e32 v155, v155
	v_max_f32_e32 v134, v134, v134
	v_max_f32_e32 v134, 0xc2a00000, v134
	v_max_f32_e32 v138, v138, v138
	v_rcp_f32_e32 v160, v114
	v_add_f32_e32 v114, 1.0, v153
	v_max_f32_e32 v138, 0xc2a00000, v138
	v_mul_f32_e32 v153, 0xbfb8aa3b, v134
	v_rcp_f32_e32 v159, v114
	v_add_f32_e32 v114, 1.0, v155
	v_exp_f32_e32 v153, v153
	v_mul_f32_e32 v155, 0xbfb8aa3b, v138
	v_exp_f32_e32 v155, v155
	v_max_f32_e32 v135, v135, v135
	v_max_f32_e32 v135, 0xc2a00000, v135
	v_max_f32_e32 v139, v139, v139
	v_rcp_f32_e32 v161, v114
	v_add_f32_e32 v114, 1.0, v153
	v_max_f32_e32 v139, 0xc2a00000, v139
	v_mul_f32_e32 v153, 0xbfb8aa3b, v135
	v_rcp_f32_e32 v168, v114
	v_add_f32_e32 v114, 1.0, v155
	v_exp_f32_e32 v153, v153
	v_mul_f32_e32 v155, 0xbfb8aa3b, v139
	v_exp_f32_e32 v155, v155
	v_rcp_f32_e32 v170, v114
	v_add_f32_e32 v114, 1.0, v153
	v_rcp_f32_e32 v169, v114
	v_add_f32_e32 v114, 1.0, v155
	v_rcp_f32_e32 v171, v114
	v_pk_mul_f32 v[166:167], v[132:133], v[158:159]
	v_pk_mul_f32 v[134:135], v[134:135], v[168:169]
	v_pk_mul_f32 v[168:169], v[136:137], v[160:161]
	v_pk_mul_f32 v[138:139], v[138:139], v[170:171]
.LBB0_352:
	s_ashr_i32 s59, s58, 31
	s_lshl_b64 s[14:15], s[58:59], 25
	s_add_u32 s14, s37, s14
	s_addc_u32 s15, s64, s15
	v_lshlrev_b32_e32 v114, 1, v177
	v_ashrrev_i32_e32 v153, 31, v152
	v_lshl_add_u64 v[132:133], s[14:15], 0, v[114:115]
	v_lshlrev_b64 v[136:137], 12, v[152:153]
	v_mov_b32_e32 v155, v154
	v_lshl_add_u64 v[136:137], v[132:133], 0, v[136:137]
	v_cvt_pk_bf16_f32 v166, v166, v167
	v_cvt_pk_bf16_f32 v167, v134, v135
	v_cvt_pk_bf16_f32 v168, v168, v169
	v_cvt_pk_bf16_f32 v169, v138, v139
	v_mov_b32_e32 v158, v154
	v_mov_b32_e32 v159, v154
	v_cndmask_b32_e64 v114, 0, 1, s[56:57]
	ds_bpermute_b32 v232, v250, v166
	ds_bpermute_b32 v233, v250, v167
	ds_bpermute_b32 v234, v250, v168
	ds_bpermute_b32 v235, v250, v169
	ds_bpermute_b32 v236, v250, v136
	v_pk_mul_f32 v[138:139], v[122:123], v[158:159]
	v_pk_mul_f32 v[134:135], v[120:121], v[154:155]
	v_pk_mul_f32 v[166:167], v[118:119], v[158:159]
	v_cmp_ne_u32_e64 s[40:41], 1, v114
	s_andn2_b64 vcc, exec, s[56:57]
	v_pk_mul_f32 v[168:169], v[116:117], v[154:155]
	s_waitcnt lgkmcnt(0)
	v_subrev_u32_e32 v236, s82, v236
	global_store_dwordx4 v236, v[232:235], s[82:83]
	s_cbranch_vccnz .LBB0_354
	v_max_f32_e32 v114, v134, v134
	v_max_f32_e32 v134, 0xc2a00000, v114
	v_max_f32_e32 v114, v168, v168
	v_max_f32_e32 v158, 0xc2a00000, v114
	v_mul_f32_e32 v114, 0xbfb8aa3b, v134
	v_exp_f32_e32 v114, v114
	v_mul_f32_e32 v155, 0xbfb8aa3b, v158
	v_exp_f32_e32 v155, v155
	v_max_f32_e32 v135, v135, v135
	v_add_f32_e32 v114, 1.0, v114
	v_rcp_f32_e32 v160, v114
	v_add_f32_e32 v114, 1.0, v155
	v_max_f32_e32 v135, 0xc2a00000, v135
	v_max_f32_e32 v155, v169, v169
	v_max_f32_e32 v159, 0xc2a00000, v155
	v_mul_f32_e32 v155, 0xbfb8aa3b, v135
	v_exp_f32_e32 v155, v155
	v_mul_f32_e32 v161, 0xbfb8aa3b, v159
	v_exp_f32_e32 v169, v161
	v_max_f32_e32 v138, v138, v138
	v_rcp_f32_e32 v168, v114
	v_add_f32_e32 v114, 1.0, v155
	v_max_f32_e32 v138, 0xc2a00000, v138
	v_max_f32_e32 v155, v166, v166
	v_max_f32_e32 v166, 0xc2a00000, v155
	v_mul_f32_e32 v155, 0xbfb8aa3b, v138
	v_exp_f32_e32 v155, v155
	v_rcp_f32_e32 v161, v114
	v_add_f32_e32 v114, 1.0, v169
	v_mul_f32_e32 v169, 0xbfb8aa3b, v166
	v_exp_f32_e32 v171, v169
	v_max_f32_e32 v139, v139, v139
	v_rcp_f32_e32 v169, v114
	v_add_f32_e32 v114, 1.0, v155
	v_max_f32_e32 v139, 0xc2a00000, v139
	v_max_f32_e32 v155, v167, v167
	v_max_f32_e32 v167, 0xc2a00000, v155
	v_mul_f32_e32 v155, 0xbfb8aa3b, v139
	v_rcp_f32_e32 v170, v114
	v_add_f32_e32 v114, 1.0, v171
	v_exp_f32_e32 v155, v155
	v_mul_f32_e32 v171, 0xbfb8aa3b, v167
	v_exp_f32_e32 v179, v171
	v_rcp_f32_e32 v178, v114
	v_add_f32_e32 v114, 1.0, v155
	v_rcp_f32_e32 v171, v114
	v_add_f32_e32 v114, 1.0, v179
	v_rcp_f32_e32 v179, v114
	v_pk_mul_f32 v[134:135], v[134:135], v[160:161]
	v_pk_mul_f32 v[138:139], v[138:139], v[170:171]
	v_pk_mul_f32 v[168:169], v[158:159], v[168:169]
	v_pk_mul_f32 v[166:167], v[166:167], v[178:179]
.LBB0_354:
	v_cvt_pk_bf16_f32 v178, v134, v135
	ds_read_b32 v134, v176 offset:64
	v_cvt_pk_bf16_f32 v179, v138, v139
	v_cvt_pk_bf16_f32 v180, v168, v169
	v_cvt_pk_bf16_f32 v181, v166, v167
	s_and_b64 vcc, exec, s[40:41]
	s_waitcnt lgkmcnt(0)
	v_pk_mul_f32 v[138:139], v[112:113], v[134:135] op_sel_hi:[1,0]
	v_pk_mul_f32 v[168:169], v[110:111], v[134:135] op_sel_hi:[1,0]
	v_pk_mul_f32 v[166:167], v[108:109], v[134:135] op_sel_hi:[1,0]
	v_pk_mul_f32 v[170:171], v[106:107], v[134:135] op_sel_hi:[1,0]
	ds_bpermute_b32 v238, v250, v178
	ds_bpermute_b32 v239, v250, v179
	ds_bpermute_b32 v240, v250, v180
	ds_bpermute_b32 v241, v250, v181
	ds_bpermute_b32 v242, v250, v136
	s_waitcnt lgkmcnt(0)
	v_subrev_u32_e32 v242, s82, v242
	global_store_dwordx4 v242, v[238:241], s[82:83] offset:64
	s_cbranch_vccnz .LBB0_356
	v_max_f32_e32 v114, v168, v168
	v_max_f32_e32 v136, 0xc2a00000, v114
	v_max_f32_e32 v114, v170, v170
	v_max_f32_e32 v158, 0xc2a00000, v114
	v_mul_f32_e32 v114, 0xbfb8aa3b, v136
	v_exp_f32_e32 v114, v114
	v_mul_f32_e32 v135, 0xbfb8aa3b, v158
	v_exp_f32_e32 v135, v135
	v_add_f32_e32 v114, 1.0, v114
	v_rcp_f32_e32 v160, v114
	v_add_f32_e32 v114, 1.0, v135
	v_max_f32_e32 v135, v169, v169
	v_max_f32_e32 v137, 0xc2a00000, v135
	v_max_f32_e32 v135, v171, v171
	v_max_f32_e32 v159, 0xc2a00000, v135
	v_mul_f32_e32 v135, 0xbfb8aa3b, v137
	v_exp_f32_e32 v135, v135
	v_mul_f32_e32 v155, 0xbfb8aa3b, v159
	v_rcp_f32_e32 v170, v114
	v_exp_f32_e32 v155, v155
	v_add_f32_e32 v114, 1.0, v135
	v_max_f32_e32 v135, v138, v138
	v_max_f32_e32 v138, 0xc2a00000, v135
	v_max_f32_e32 v135, v166, v166
	v_max_f32_e32 v166, 0xc2a00000, v135
	v_mul_f32_e32 v135, 0xbfb8aa3b, v138
	v_exp_f32_e32 v135, v135
	v_rcp_f32_e32 v161, v114
	v_add_f32_e32 v114, 1.0, v155
	v_mul_f32_e32 v155, 0xbfb8aa3b, v166
	v_exp_f32_e32 v155, v155
	v_rcp_f32_e32 v171, v114
	v_add_f32_e32 v114, 1.0, v135
	v_max_f32_e32 v135, v139, v139
	v_max_f32_e32 v139, 0xc2a00000, v135
	v_max_f32_e32 v135, v167, v167
	v_max_f32_e32 v167, 0xc2a00000, v135
	v_mul_f32_e32 v135, 0xbfb8aa3b, v139
	v_rcp_f32_e32 v178, v114
	v_add_f32_e32 v114, 1.0, v155
	v_exp_f32_e32 v135, v135
	v_mul_f32_e32 v155, 0xbfb8aa3b, v167
	v_exp_f32_e32 v155, v155
	v_rcp_f32_e32 v180, v114
	v_add_f32_e32 v114, 1.0, v135
	v_rcp_f32_e32 v179, v114
	v_add_f32_e32 v114, 1.0, v155
	v_rcp_f32_e32 v181, v114
	v_pk_mul_f32 v[168:169], v[136:137], v[160:161]
	v_pk_mul_f32 v[138:139], v[138:139], v[178:179]
	v_pk_mul_f32 v[170:171], v[158:159], v[170:171]
	v_pk_mul_f32 v[166:167], v[166:167], v[180:181]
.LBB0_356:
	v_or_b32_e32 v136, 16, v152
	v_ashrrev_i32_e32 v137, 31, v136
	v_lshlrev_b64 v[136:137], 12, v[136:137]
	v_mov_b32_e32 v135, v134
	v_lshl_add_u64 v[136:137], v[132:133], 0, v[136:137]
	v_cvt_pk_bf16_f32 v168, v168, v169
	v_cvt_pk_bf16_f32 v169, v138, v139
	v_cvt_pk_bf16_f32 v170, v170, v171
	v_cvt_pk_bf16_f32 v171, v166, v167
	v_mov_b32_e32 v158, v134
	v_mov_b32_e32 v159, v134
	ds_bpermute_b32 v244, v250, v168
	ds_bpermute_b32 v245, v250, v169
	ds_bpermute_b32 v246, v250, v170
	ds_bpermute_b32 v247, v250, v171
	ds_bpermute_b32 v248, v250, v136
	v_pk_mul_f32 v[138:139], v[104:105], v[158:159]
	v_pk_mul_f32 v[166:167], v[100:101], v[158:159]
	v_pk_mul_f32 v[168:169], v[102:103], v[134:135]
	s_and_b64 vcc, exec, s[40:41]
	v_pk_mul_f32 v[170:171], v[98:99], v[134:135]
	s_waitcnt lgkmcnt(0)
	v_subrev_u32_e32 v248, s82, v248
	global_store_dwordx4 v248, v[244:247], s[82:83]
	s_cbranch_vccnz .LBB0_358
	v_max_f32_e32 v114, v168, v168
	v_max_f32_e32 v134, 0xc2a00000, v114
	v_max_f32_e32 v114, v170, v170
	v_max_f32_e32 v158, 0xc2a00000, v114
	v_mul_f32_e32 v114, 0xbfb8aa3b, v134
	v_exp_f32_e32 v114, v114
	v_mul_f32_e32 v135, 0xbfb8aa3b, v158
	v_exp_f32_e32 v135, v135
	v_max_f32_e32 v155, v171, v171
	v_add_f32_e32 v114, 1.0, v114
	v_rcp_f32_e32 v160, v114
	v_add_f32_e32 v114, 1.0, v135
	v_max_f32_e32 v135, v169, v169
	v_max_f32_e32 v135, 0xc2a00000, v135
	v_max_f32_e32 v159, 0xc2a00000, v155
	v_mul_f32_e32 v155, 0xbfb8aa3b, v135
	v_exp_f32_e32 v155, v155
	v_mul_f32_e32 v161, 0xbfb8aa3b, v159
	v_exp_f32_e32 v168, v161
	v_max_f32_e32 v138, v138, v138
	v_rcp_f32_e32 v170, v114
	v_add_f32_e32 v114, 1.0, v155
	v_max_f32_e32 v138, 0xc2a00000, v138
	v_max_f32_e32 v155, v166, v166
	v_max_f32_e32 v166, 0xc2a00000, v155
	v_mul_f32_e32 v155, 0xbfb8aa3b, v138
	v_exp_f32_e32 v155, v155
	v_rcp_f32_e32 v161, v114
	v_add_f32_e32 v114, 1.0, v168
	v_mul_f32_e32 v168, 0xbfb8aa3b, v166
	v_exp_f32_e32 v168, v168
	v_max_f32_e32 v139, v139, v139
	v_rcp_f32_e32 v171, v114
	v_add_f32_e32 v114, 1.0, v155
	v_max_f32_e32 v139, 0xc2a00000, v139
	v_max_f32_e32 v155, v167, v167
	v_max_f32_e32 v167, 0xc2a00000, v155
	v_mul_f32_e32 v155, 0xbfb8aa3b, v139
	v_rcp_f32_e32 v178, v114
	v_add_f32_e32 v114, 1.0, v168
	v_exp_f32_e32 v155, v155
	v_mul_f32_e32 v168, 0xbfb8aa3b, v167
	v_exp_f32_e32 v168, v168
	v_rcp_f32_e32 v180, v114
	v_add_f32_e32 v114, 1.0, v155
	v_rcp_f32_e32 v179, v114
	v_add_f32_e32 v114, 1.0, v168
	v_rcp_f32_e32 v181, v114
	v_pk_mul_f32 v[168:169], v[134:135], v[160:161]
	v_pk_mul_f32 v[138:139], v[138:139], v[178:179]
	v_pk_mul_f32 v[170:171], v[158:159], v[170:171]
	v_pk_mul_f32 v[166:167], v[166:167], v[180:181]
.LBB0_358:
	ds_read_b32 v134, v176 offset:128
	v_cvt_pk_bf16_f32 v168, v168, v169
	v_cvt_pk_bf16_f32 v169, v138, v139
	v_cvt_pk_bf16_f32 v170, v170, v171
	v_cvt_pk_bf16_f32 v171, v166, v167
	ds_bpermute_b32 v232, v250, v168
	ds_bpermute_b32 v233, v250, v169
	ds_bpermute_b32 v234, v250, v170
	ds_bpermute_b32 v235, v250, v171
	ds_bpermute_b32 v236, v250, v136
	s_waitcnt lgkmcnt(0)
	v_pk_mul_f32 v[138:139], v[96:97], v[134:135] op_sel_hi:[1,0]
	v_pk_mul_f32 v[166:167], v[92:93], v[134:135] op_sel_hi:[1,0]
	v_pk_mul_f32 v[168:169], v[94:95], v[134:135] op_sel_hi:[1,0]
	s_and_b64 vcc, exec, s[40:41]
	v_pk_mul_f32 v[170:171], v[90:91], v[134:135] op_sel_hi:[1,0]
	s_waitcnt lgkmcnt(0)
	v_subrev_u32_e32 v236, s82, v236
	global_store_dwordx4 v236, v[232:235], s[82:83] offset:64
	s_cbranch_vccnz .LBB0_360
	v_max_f32_e32 v114, v168, v168
	v_max_f32_e32 v136, 0xc2a00000, v114
	v_max_f32_e32 v114, v170, v170
	v_max_f32_e32 v158, 0xc2a00000, v114
	v_mul_f32_e32 v114, 0xbfb8aa3b, v136
	v_exp_f32_e32 v114, v114
	v_mul_f32_e32 v135, 0xbfb8aa3b, v158
	v_exp_f32_e32 v135, v135
	v_add_f32_e32 v114, 1.0, v114
	v_rcp_f32_e32 v160, v114
	v_add_f32_e32 v114, 1.0, v135
	v_max_f32_e32 v135, v169, v169
	v_max_f32_e32 v137, 0xc2a00000, v135
	v_max_f32_e32 v135, v171, v171
	v_max_f32_e32 v159, 0xc2a00000, v135
	v_mul_f32_e32 v135, 0xbfb8aa3b, v137
	v_exp_f32_e32 v135, v135
	v_mul_f32_e32 v155, 0xbfb8aa3b, v159
	v_rcp_f32_e32 v170, v114
	v_exp_f32_e32 v155, v155
	v_add_f32_e32 v114, 1.0, v135
	v_max_f32_e32 v135, v138, v138
	v_max_f32_e32 v138, 0xc2a00000, v135
	v_max_f32_e32 v135, v166, v166
	v_max_f32_e32 v166, 0xc2a00000, v135
	v_mul_f32_e32 v135, 0xbfb8aa3b, v138
	v_exp_f32_e32 v135, v135
	v_rcp_f32_e32 v161, v114
	v_add_f32_e32 v114, 1.0, v155
	v_mul_f32_e32 v155, 0xbfb8aa3b, v166
	v_exp_f32_e32 v155, v155
	v_rcp_f32_e32 v171, v114
	v_add_f32_e32 v114, 1.0, v135
	v_max_f32_e32 v135, v139, v139
	v_max_f32_e32 v139, 0xc2a00000, v135
	v_max_f32_e32 v135, v167, v167
	v_max_f32_e32 v167, 0xc2a00000, v135
	v_mul_f32_e32 v135, 0xbfb8aa3b, v139
	v_rcp_f32_e32 v178, v114
	v_add_f32_e32 v114, 1.0, v155
	v_exp_f32_e32 v135, v135
	v_mul_f32_e32 v155, 0xbfb8aa3b, v167
	v_exp_f32_e32 v155, v155
	v_rcp_f32_e32 v180, v114
	v_add_f32_e32 v114, 1.0, v135
	v_rcp_f32_e32 v179, v114
	v_add_f32_e32 v114, 1.0, v155
	v_rcp_f32_e32 v181, v114
	v_pk_mul_f32 v[168:169], v[136:137], v[160:161]
	v_pk_mul_f32 v[138:139], v[138:139], v[178:179]
	v_pk_mul_f32 v[170:171], v[158:159], v[170:171]
	v_pk_mul_f32 v[166:167], v[166:167], v[180:181]
.LBB0_360:
	v_or_b32_e32 v136, 32, v152
	v_ashrrev_i32_e32 v137, 31, v136
	v_lshlrev_b64 v[136:137], 12, v[136:137]
	v_mov_b32_e32 v135, v134
	v_lshl_add_u64 v[136:137], v[132:133], 0, v[136:137]
	v_cvt_pk_bf16_f32 v168, v168, v169
	v_cvt_pk_bf16_f32 v169, v138, v139
	v_cvt_pk_bf16_f32 v170, v170, v171
	v_cvt_pk_bf16_f32 v171, v166, v167
	v_mov_b32_e32 v158, v134
	v_mov_b32_e32 v159, v134
	ds_bpermute_b32 v238, v250, v168
	ds_bpermute_b32 v239, v250, v169
	ds_bpermute_b32 v240, v250, v170
	ds_bpermute_b32 v241, v250, v171
	ds_bpermute_b32 v242, v250, v136
	v_pk_mul_f32 v[138:139], v[88:89], v[158:159]
	v_pk_mul_f32 v[166:167], v[84:85], v[158:159]
	v_pk_mul_f32 v[168:169], v[86:87], v[134:135]
	s_and_b64 vcc, exec, s[40:41]
	v_pk_mul_f32 v[170:171], v[82:83], v[134:135]
	s_waitcnt lgkmcnt(0)
	v_subrev_u32_e32 v242, s82, v242
	global_store_dwordx4 v242, v[238:241], s[82:83]
	s_cbranch_vccnz .LBB0_362
	v_max_f32_e32 v114, v168, v168
	v_max_f32_e32 v134, 0xc2a00000, v114
	v_max_f32_e32 v114, v170, v170
	v_max_f32_e32 v158, 0xc2a00000, v114
	v_mul_f32_e32 v114, 0xbfb8aa3b, v134
	v_exp_f32_e32 v114, v114
	v_mul_f32_e32 v135, 0xbfb8aa3b, v158
	v_exp_f32_e32 v135, v135
	v_max_f32_e32 v155, v171, v171
	v_add_f32_e32 v114, 1.0, v114
	v_rcp_f32_e32 v160, v114
	v_add_f32_e32 v114, 1.0, v135
	v_max_f32_e32 v135, v169, v169
	v_max_f32_e32 v135, 0xc2a00000, v135
	v_max_f32_e32 v159, 0xc2a00000, v155
	v_mul_f32_e32 v155, 0xbfb8aa3b, v135
	v_exp_f32_e32 v155, v155
	v_mul_f32_e32 v161, 0xbfb8aa3b, v159
	v_exp_f32_e32 v168, v161
	v_max_f32_e32 v138, v138, v138
	v_rcp_f32_e32 v170, v114
	v_add_f32_e32 v114, 1.0, v155
	v_max_f32_e32 v138, 0xc2a00000, v138
	v_max_f32_e32 v155, v166, v166
	v_max_f32_e32 v166, 0xc2a00000, v155
	v_mul_f32_e32 v155, 0xbfb8aa3b, v138
	v_exp_f32_e32 v155, v155
	v_rcp_f32_e32 v161, v114
	v_add_f32_e32 v114, 1.0, v168
	v_mul_f32_e32 v168, 0xbfb8aa3b, v166
	v_exp_f32_e32 v168, v168
	v_max_f32_e32 v139, v139, v139
	v_rcp_f32_e32 v171, v114
	v_add_f32_e32 v114, 1.0, v155
	v_max_f32_e32 v139, 0xc2a00000, v139
	v_max_f32_e32 v155, v167, v167
	v_max_f32_e32 v167, 0xc2a00000, v155
	v_mul_f32_e32 v155, 0xbfb8aa3b, v139
	v_rcp_f32_e32 v178, v114
	v_add_f32_e32 v114, 1.0, v168
	v_exp_f32_e32 v155, v155
	v_mul_f32_e32 v168, 0xbfb8aa3b, v167
	v_exp_f32_e32 v168, v168
	v_rcp_f32_e32 v180, v114
	v_add_f32_e32 v114, 1.0, v155
	v_rcp_f32_e32 v179, v114
	v_add_f32_e32 v114, 1.0, v168
	v_rcp_f32_e32 v181, v114
	v_pk_mul_f32 v[168:169], v[134:135], v[160:161]
	v_pk_mul_f32 v[138:139], v[138:139], v[178:179]
	v_pk_mul_f32 v[170:171], v[158:159], v[170:171]
	v_pk_mul_f32 v[166:167], v[166:167], v[180:181]
.LBB0_362:
	ds_read_b32 v134, v176 offset:192
	v_cvt_pk_bf16_f32 v168, v168, v169
	v_cvt_pk_bf16_f32 v169, v138, v139
	v_cvt_pk_bf16_f32 v170, v170, v171
	v_cvt_pk_bf16_f32 v171, v166, v167
	ds_bpermute_b32 v244, v250, v168
	ds_bpermute_b32 v245, v250, v169
	ds_bpermute_b32 v246, v250, v170
	ds_bpermute_b32 v247, v250, v171
	ds_bpermute_b32 v248, v250, v136
	s_waitcnt lgkmcnt(0)
	v_pk_mul_f32 v[138:139], v[80:81], v[134:135] op_sel_hi:[1,0]
	v_pk_mul_f32 v[166:167], v[76:77], v[134:135] op_sel_hi:[1,0]
	v_pk_mul_f32 v[168:169], v[78:79], v[134:135] op_sel_hi:[1,0]
	s_and_b64 vcc, exec, s[40:41]
	v_pk_mul_f32 v[170:171], v[74:75], v[134:135] op_sel_hi:[1,0]
	s_waitcnt lgkmcnt(0)
	v_subrev_u32_e32 v248, s82, v248
	global_store_dwordx4 v248, v[244:247], s[82:83] offset:64
	s_cbranch_vccnz .LBB0_364
	v_max_f32_e32 v114, v168, v168
	v_max_f32_e32 v136, 0xc2a00000, v114
	v_max_f32_e32 v114, v170, v170
	v_max_f32_e32 v158, 0xc2a00000, v114
	v_mul_f32_e32 v114, 0xbfb8aa3b, v136
	v_exp_f32_e32 v114, v114
	v_mul_f32_e32 v135, 0xbfb8aa3b, v158
	v_exp_f32_e32 v135, v135
	v_add_f32_e32 v114, 1.0, v114
	v_rcp_f32_e32 v160, v114
	v_add_f32_e32 v114, 1.0, v135
	v_max_f32_e32 v135, v169, v169
	v_max_f32_e32 v137, 0xc2a00000, v135
	v_max_f32_e32 v135, v171, v171
	v_max_f32_e32 v159, 0xc2a00000, v135
	v_mul_f32_e32 v135, 0xbfb8aa3b, v137
	v_exp_f32_e32 v135, v135
	v_mul_f32_e32 v155, 0xbfb8aa3b, v159
	v_rcp_f32_e32 v170, v114
	v_exp_f32_e32 v155, v155
	v_add_f32_e32 v114, 1.0, v135
	v_max_f32_e32 v135, v138, v138
	v_max_f32_e32 v138, 0xc2a00000, v135
	v_max_f32_e32 v135, v166, v166
	v_max_f32_e32 v166, 0xc2a00000, v135
	v_mul_f32_e32 v135, 0xbfb8aa3b, v138
	v_exp_f32_e32 v135, v135
	v_rcp_f32_e32 v161, v114
	v_add_f32_e32 v114, 1.0, v155
	v_mul_f32_e32 v155, 0xbfb8aa3b, v166
	v_exp_f32_e32 v155, v155
	v_rcp_f32_e32 v171, v114
	v_add_f32_e32 v114, 1.0, v135
	v_max_f32_e32 v135, v139, v139
	v_max_f32_e32 v139, 0xc2a00000, v135
	v_max_f32_e32 v135, v167, v167
	v_max_f32_e32 v167, 0xc2a00000, v135
	v_mul_f32_e32 v135, 0xbfb8aa3b, v139
	v_rcp_f32_e32 v178, v114
	v_add_f32_e32 v114, 1.0, v155
	v_exp_f32_e32 v135, v135
	v_mul_f32_e32 v155, 0xbfb8aa3b, v167
	v_exp_f32_e32 v155, v155
	v_rcp_f32_e32 v180, v114
	v_add_f32_e32 v114, 1.0, v135
	v_rcp_f32_e32 v179, v114
	v_add_f32_e32 v114, 1.0, v155
	v_rcp_f32_e32 v181, v114
	v_pk_mul_f32 v[168:169], v[136:137], v[160:161]
	v_pk_mul_f32 v[138:139], v[138:139], v[178:179]
	v_pk_mul_f32 v[170:171], v[158:159], v[170:171]
	v_pk_mul_f32 v[166:167], v[166:167], v[180:181]
.LBB0_364:
	v_or_b32_e32 v136, 48, v152
	v_ashrrev_i32_e32 v137, 31, v136
	v_lshlrev_b64 v[136:137], 12, v[136:137]
	v_mov_b32_e32 v135, v134
	v_lshl_add_u64 v[136:137], v[132:133], 0, v[136:137]
	v_cvt_pk_bf16_f32 v168, v168, v169
	v_cvt_pk_bf16_f32 v169, v138, v139
	v_cvt_pk_bf16_f32 v170, v170, v171
	v_cvt_pk_bf16_f32 v171, v166, v167
	v_mov_b32_e32 v158, v134
	v_mov_b32_e32 v159, v134
	ds_bpermute_b32 v232, v250, v168
	ds_bpermute_b32 v233, v250, v169
	ds_bpermute_b32 v234, v250, v170
	ds_bpermute_b32 v235, v250, v171
	ds_bpermute_b32 v236, v250, v136
	v_pk_mul_f32 v[138:139], v[72:73], v[158:159]
	v_pk_mul_f32 v[166:167], v[68:69], v[158:159]
	v_pk_mul_f32 v[168:169], v[70:71], v[134:135]
	s_and_b64 vcc, exec, s[40:41]
	v_pk_mul_f32 v[170:171], v[66:67], v[134:135]
	s_waitcnt lgkmcnt(0)
	v_subrev_u32_e32 v236, s82, v236
	global_store_dwordx4 v236, v[232:235], s[82:83]
	s_cbranch_vccnz .LBB0_366
	v_max_f32_e32 v114, v168, v168
	v_max_f32_e32 v134, 0xc2a00000, v114
	v_max_f32_e32 v114, v170, v170
	v_max_f32_e32 v158, 0xc2a00000, v114
	v_mul_f32_e32 v114, 0xbfb8aa3b, v134
	v_exp_f32_e32 v114, v114
	v_mul_f32_e32 v135, 0xbfb8aa3b, v158
	v_exp_f32_e32 v135, v135
	v_max_f32_e32 v155, v171, v171
	v_add_f32_e32 v114, 1.0, v114
	v_rcp_f32_e32 v160, v114
	v_add_f32_e32 v114, 1.0, v135
	v_max_f32_e32 v135, v169, v169
	v_max_f32_e32 v135, 0xc2a00000, v135
	v_max_f32_e32 v159, 0xc2a00000, v155
	v_mul_f32_e32 v155, 0xbfb8aa3b, v135
	v_exp_f32_e32 v155, v155
	v_mul_f32_e32 v161, 0xbfb8aa3b, v159
	v_exp_f32_e32 v168, v161
	v_max_f32_e32 v138, v138, v138
	v_rcp_f32_e32 v170, v114
	v_add_f32_e32 v114, 1.0, v155
	v_max_f32_e32 v138, 0xc2a00000, v138
	v_max_f32_e32 v155, v166, v166
	v_max_f32_e32 v166, 0xc2a00000, v155
	v_mul_f32_e32 v155, 0xbfb8aa3b, v138
	v_exp_f32_e32 v155, v155
	v_rcp_f32_e32 v161, v114
	v_add_f32_e32 v114, 1.0, v168
	v_mul_f32_e32 v168, 0xbfb8aa3b, v166
	v_exp_f32_e32 v168, v168
	v_max_f32_e32 v139, v139, v139
	v_rcp_f32_e32 v171, v114
	v_add_f32_e32 v114, 1.0, v155
	v_max_f32_e32 v139, 0xc2a00000, v139
	v_max_f32_e32 v155, v167, v167
	v_max_f32_e32 v167, 0xc2a00000, v155
	v_mul_f32_e32 v155, 0xbfb8aa3b, v139
	v_rcp_f32_e32 v178, v114
	v_add_f32_e32 v114, 1.0, v168
	v_exp_f32_e32 v155, v155
	v_mul_f32_e32 v168, 0xbfb8aa3b, v167
	v_exp_f32_e32 v168, v168
	v_rcp_f32_e32 v180, v114
	v_add_f32_e32 v114, 1.0, v155
	v_rcp_f32_e32 v179, v114
	v_add_f32_e32 v114, 1.0, v168
	v_rcp_f32_e32 v181, v114
	v_pk_mul_f32 v[168:169], v[134:135], v[160:161]
	v_pk_mul_f32 v[138:139], v[138:139], v[178:179]
	v_pk_mul_f32 v[170:171], v[158:159], v[170:171]
	v_pk_mul_f32 v[166:167], v[166:167], v[180:181]
.LBB0_366:
	ds_read_b32 v134, v176 offset:512
	v_cvt_pk_bf16_f32 v168, v168, v169
	v_cvt_pk_bf16_f32 v169, v138, v139
	v_cvt_pk_bf16_f32 v170, v170, v171
	v_cvt_pk_bf16_f32 v171, v166, v167
	ds_bpermute_b32 v238, v250, v168
	ds_bpermute_b32 v239, v250, v169
	ds_bpermute_b32 v240, v250, v170
	ds_bpermute_b32 v241, v250, v171
	ds_bpermute_b32 v242, v250, v136
	s_waitcnt lgkmcnt(0)
	v_pk_mul_f32 v[138:139], v[64:65], v[134:135] op_sel_hi:[1,0]
	v_pk_mul_f32 v[166:167], v[60:61], v[134:135] op_sel_hi:[1,0]
	v_pk_mul_f32 v[168:169], v[62:63], v[134:135] op_sel_hi:[1,0]
	s_and_b64 vcc, exec, s[40:41]
	v_pk_mul_f32 v[170:171], v[58:59], v[134:135] op_sel_hi:[1,0]
	s_waitcnt lgkmcnt(0)
	v_subrev_u32_e32 v242, s82, v242
	global_store_dwordx4 v242, v[238:241], s[82:83] offset:64
	s_cbranch_vccnz .LBB0_368
	v_max_f32_e32 v114, v168, v168
	v_max_f32_e32 v136, 0xc2a00000, v114
	v_max_f32_e32 v114, v170, v170
	v_max_f32_e32 v158, 0xc2a00000, v114
	v_mul_f32_e32 v114, 0xbfb8aa3b, v136
	v_exp_f32_e32 v114, v114
	v_mul_f32_e32 v135, 0xbfb8aa3b, v158
	v_exp_f32_e32 v135, v135
	v_add_f32_e32 v114, 1.0, v114
	v_rcp_f32_e32 v160, v114
	v_add_f32_e32 v114, 1.0, v135
	v_max_f32_e32 v135, v169, v169
	v_max_f32_e32 v137, 0xc2a00000, v135
	v_max_f32_e32 v135, v171, v171
	v_max_f32_e32 v159, 0xc2a00000, v135
	v_mul_f32_e32 v135, 0xbfb8aa3b, v137
	v_exp_f32_e32 v135, v135
	v_mul_f32_e32 v155, 0xbfb8aa3b, v159
	v_rcp_f32_e32 v170, v114
	v_exp_f32_e32 v155, v155
	v_add_f32_e32 v114, 1.0, v135
	v_max_f32_e32 v135, v138, v138
	v_max_f32_e32 v138, 0xc2a00000, v135
	v_max_f32_e32 v135, v166, v166
	v_max_f32_e32 v166, 0xc2a00000, v135
	v_mul_f32_e32 v135, 0xbfb8aa3b, v138
	v_exp_f32_e32 v135, v135
	v_rcp_f32_e32 v161, v114
	v_add_f32_e32 v114, 1.0, v155
	v_mul_f32_e32 v155, 0xbfb8aa3b, v166
	v_exp_f32_e32 v155, v155
	v_rcp_f32_e32 v171, v114
	v_add_f32_e32 v114, 1.0, v135
	v_max_f32_e32 v135, v139, v139
	v_max_f32_e32 v139, 0xc2a00000, v135
	v_max_f32_e32 v135, v167, v167
	v_max_f32_e32 v167, 0xc2a00000, v135
	v_mul_f32_e32 v135, 0xbfb8aa3b, v139
	v_rcp_f32_e32 v178, v114
	v_add_f32_e32 v114, 1.0, v155
	v_exp_f32_e32 v135, v135
	v_mul_f32_e32 v155, 0xbfb8aa3b, v167
	v_exp_f32_e32 v155, v155
	v_rcp_f32_e32 v180, v114
	v_add_f32_e32 v114, 1.0, v135
	v_rcp_f32_e32 v179, v114
	v_add_f32_e32 v114, 1.0, v155
	v_rcp_f32_e32 v181, v114
	v_pk_mul_f32 v[168:169], v[136:137], v[160:161]
	v_pk_mul_f32 v[138:139], v[138:139], v[178:179]
	v_pk_mul_f32 v[170:171], v[158:159], v[170:171]
	v_pk_mul_f32 v[166:167], v[166:167], v[180:181]
.LBB0_368:
	v_lshlrev_b64 v[136:137], 12, v[152:153]
	v_lshl_add_u64 v[136:137], v[132:133], 0, v[136:137]
	s_mov_b32 s14, 0x80000
	v_cvt_pk_bf16_f32 v168, v168, v169
	v_cvt_pk_bf16_f32 v169, v138, v139
	v_add_co_u32_e32 v138, vcc, s14, v136
	v_mov_b32_e32 v135, v134
	v_cvt_pk_bf16_f32 v170, v170, v171
	v_cvt_pk_bf16_f32 v171, v166, v167
	s_nop 0
	v_addc_co_u32_e32 v139, vcc, 0, v137, vcc
	v_mov_b32_e32 v158, v134
	v_mov_b32_e32 v159, v134
	ds_bpermute_b32 v244, v250, v168
	ds_bpermute_b32 v245, v250, v169
	ds_bpermute_b32 v246, v250, v170
	ds_bpermute_b32 v247, v250, v171
	ds_bpermute_b32 v248, v250, v138
	v_pk_mul_f32 v[138:139], v[56:57], v[158:159]
	v_pk_mul_f32 v[166:167], v[52:53], v[158:159]
	v_pk_mul_f32 v[168:169], v[54:55], v[134:135]
	s_and_b64 vcc, exec, s[40:41]
	v_pk_mul_f32 v[170:171], v[50:51], v[134:135]
	s_waitcnt lgkmcnt(0)
	v_subrev_u32_e32 v248, s82, v248
	global_store_dwordx4 v248, v[244:247], s[82:83]
	s_cbranch_vccnz .LBB0_370
	v_max_f32_e32 v114, v168, v168
	v_max_f32_e32 v134, 0xc2a00000, v114
	v_max_f32_e32 v114, v170, v170
	v_max_f32_e32 v158, 0xc2a00000, v114
	v_mul_f32_e32 v114, 0xbfb8aa3b, v134
	v_exp_f32_e32 v114, v114
	v_mul_f32_e32 v135, 0xbfb8aa3b, v158
	v_exp_f32_e32 v135, v135
	v_max_f32_e32 v155, v171, v171
	v_add_f32_e32 v114, 1.0, v114
	v_rcp_f32_e32 v160, v114
	v_add_f32_e32 v114, 1.0, v135
	v_max_f32_e32 v135, v169, v169
	v_max_f32_e32 v135, 0xc2a00000, v135
	v_max_f32_e32 v159, 0xc2a00000, v155
	v_mul_f32_e32 v155, 0xbfb8aa3b, v135
	v_exp_f32_e32 v155, v155
	v_mul_f32_e32 v161, 0xbfb8aa3b, v159
	v_exp_f32_e32 v168, v161
	v_max_f32_e32 v138, v138, v138
	v_rcp_f32_e32 v170, v114
	v_add_f32_e32 v114, 1.0, v155
	v_max_f32_e32 v138, 0xc2a00000, v138
	v_max_f32_e32 v155, v166, v166
	v_max_f32_e32 v166, 0xc2a00000, v155
	v_mul_f32_e32 v155, 0xbfb8aa3b, v138
	v_exp_f32_e32 v155, v155
	v_rcp_f32_e32 v161, v114
	v_add_f32_e32 v114, 1.0, v168
	v_mul_f32_e32 v168, 0xbfb8aa3b, v166
	v_exp_f32_e32 v168, v168
	v_max_f32_e32 v139, v139, v139
	v_rcp_f32_e32 v171, v114
	v_add_f32_e32 v114, 1.0, v155
	v_max_f32_e32 v139, 0xc2a00000, v139
	v_max_f32_e32 v155, v167, v167
	v_max_f32_e32 v167, 0xc2a00000, v155
	v_mul_f32_e32 v155, 0xbfb8aa3b, v139
	v_rcp_f32_e32 v178, v114
	v_add_f32_e32 v114, 1.0, v168
	v_exp_f32_e32 v155, v155
	v_mul_f32_e32 v168, 0xbfb8aa3b, v167
	v_exp_f32_e32 v168, v168
	v_rcp_f32_e32 v180, v114
	v_add_f32_e32 v114, 1.0, v155
	v_rcp_f32_e32 v179, v114
	v_add_f32_e32 v114, 1.0, v168
	v_rcp_f32_e32 v181, v114
	v_pk_mul_f32 v[168:169], v[134:135], v[160:161]
	v_pk_mul_f32 v[138:139], v[138:139], v[178:179]
	v_pk_mul_f32 v[170:171], v[158:159], v[170:171]
	v_pk_mul_f32 v[166:167], v[166:167], v[180:181]
.LBB0_370:
	ds_read_b32 v134, v176 offset:576
	s_mov_b64 s[14:15], 0x80000
	v_lshl_add_u64 v[158:159], v[136:137], 0, s[14:15]
	v_cvt_pk_bf16_f32 v137, v138, v139
	v_cvt_pk_bf16_f32 v138, v170, v171
	v_cvt_pk_bf16_f32 v139, v166, v167
	v_cvt_pk_bf16_f32 v136, v168, v169
	ds_bpermute_b32 v232, v250, v136
	ds_bpermute_b32 v233, v250, v137
	ds_bpermute_b32 v234, v250, v138
	ds_bpermute_b32 v235, v250, v139
	ds_bpermute_b32 v236, v250, v158
	s_waitcnt lgkmcnt(0)
	v_pk_mul_f32 v[168:169], v[46:47], v[134:135] op_sel_hi:[1,0]
	v_pk_mul_f32 v[166:167], v[44:45], v[134:135] op_sel_hi:[1,0]
	v_pk_mul_f32 v[138:139], v[48:49], v[134:135] op_sel_hi:[1,0]
	s_and_b64 vcc, exec, s[40:41]
	v_pk_mul_f32 v[170:171], v[42:43], v[134:135] op_sel_hi:[1,0]
	s_waitcnt lgkmcnt(0)
	v_subrev_u32_e32 v236, s82, v236
	global_store_dwordx4 v236, v[232:235], s[82:83] offset:64
	s_cbranch_vccnz .LBB0_372
	v_max_f32_e32 v114, v168, v168
	v_max_f32_e32 v136, 0xc2a00000, v114
	v_max_f32_e32 v114, v170, v170
	v_max_f32_e32 v158, 0xc2a00000, v114
	v_mul_f32_e32 v114, 0xbfb8aa3b, v136
	v_exp_f32_e32 v114, v114
	v_mul_f32_e32 v135, 0xbfb8aa3b, v158
	v_exp_f32_e32 v135, v135
	v_add_f32_e32 v114, 1.0, v114
	v_rcp_f32_e32 v160, v114
	v_add_f32_e32 v114, 1.0, v135
	v_max_f32_e32 v135, v169, v169
	v_max_f32_e32 v137, 0xc2a00000, v135
	v_max_f32_e32 v135, v171, v171
	v_max_f32_e32 v159, 0xc2a00000, v135
	v_mul_f32_e32 v135, 0xbfb8aa3b, v137
	v_exp_f32_e32 v135, v135
	v_mul_f32_e32 v155, 0xbfb8aa3b, v159
	v_rcp_f32_e32 v170, v114
	v_exp_f32_e32 v155, v155
	v_add_f32_e32 v114, 1.0, v135
	v_max_f32_e32 v135, v138, v138
	v_max_f32_e32 v138, 0xc2a00000, v135
	v_max_f32_e32 v135, v166, v166
	v_max_f32_e32 v166, 0xc2a00000, v135
	v_mul_f32_e32 v135, 0xbfb8aa3b, v138
	v_exp_f32_e32 v135, v135
	v_rcp_f32_e32 v161, v114
	v_add_f32_e32 v114, 1.0, v155
	v_mul_f32_e32 v155, 0xbfb8aa3b, v166
	v_exp_f32_e32 v155, v155
	v_rcp_f32_e32 v171, v114
	v_add_f32_e32 v114, 1.0, v135
	v_max_f32_e32 v135, v139, v139
	v_max_f32_e32 v139, 0xc2a00000, v135
	v_max_f32_e32 v135, v167, v167
	v_max_f32_e32 v167, 0xc2a00000, v135
	v_mul_f32_e32 v135, 0xbfb8aa3b, v139
	v_rcp_f32_e32 v178, v114
	v_add_f32_e32 v114, 1.0, v155
	v_exp_f32_e32 v135, v135
	v_mul_f32_e32 v155, 0xbfb8aa3b, v167
	v_exp_f32_e32 v155, v155
	v_rcp_f32_e32 v180, v114
	v_add_f32_e32 v114, 1.0, v135
	v_rcp_f32_e32 v179, v114
	v_add_f32_e32 v114, 1.0, v155
	v_rcp_f32_e32 v181, v114
	v_pk_mul_f32 v[168:169], v[136:137], v[160:161]
	v_pk_mul_f32 v[138:139], v[138:139], v[178:179]
	v_pk_mul_f32 v[170:171], v[158:159], v[170:171]
	v_pk_mul_f32 v[166:167], v[166:167], v[180:181]
.LBB0_372:
	v_lshlrev_b64 v[136:137], 12, v[152:153]
	v_lshl_add_u64 v[136:137], v[132:133], 0, v[136:137]
	s_mov_b32 s14, 0x90000
	v_cvt_pk_bf16_f32 v168, v168, v169
	v_cvt_pk_bf16_f32 v169, v138, v139
	v_add_co_u32_e32 v138, vcc, s14, v136
	v_mov_b32_e32 v135, v134
	v_cvt_pk_bf16_f32 v170, v170, v171
	v_cvt_pk_bf16_f32 v171, v166, v167
	s_nop 0
	v_addc_co_u32_e32 v139, vcc, 0, v137, vcc
	v_mov_b32_e32 v158, v134
	v_mov_b32_e32 v159, v134
	ds_bpermute_b32 v238, v250, v168
	ds_bpermute_b32 v239, v250, v169
	ds_bpermute_b32 v240, v250, v170
	ds_bpermute_b32 v241, v250, v171
	ds_bpermute_b32 v242, v250, v138
	v_pk_mul_f32 v[138:139], v[40:41], v[158:159]
	v_pk_mul_f32 v[166:167], v[36:37], v[158:159]
	v_pk_mul_f32 v[168:169], v[38:39], v[134:135]
	s_and_b64 vcc, exec, s[40:41]
	v_pk_mul_f32 v[170:171], v[34:35], v[134:135]
	s_waitcnt lgkmcnt(0)
	v_subrev_u32_e32 v242, s82, v242
	global_store_dwordx4 v242, v[238:241], s[82:83]
	s_cbranch_vccnz .LBB0_374
	v_max_f32_e32 v114, v168, v168
	v_max_f32_e32 v134, 0xc2a00000, v114
	v_max_f32_e32 v114, v170, v170
	v_max_f32_e32 v158, 0xc2a00000, v114
	v_mul_f32_e32 v114, 0xbfb8aa3b, v134
	v_exp_f32_e32 v114, v114
	v_mul_f32_e32 v135, 0xbfb8aa3b, v158
	v_exp_f32_e32 v135, v135
	v_max_f32_e32 v155, v171, v171
	v_add_f32_e32 v114, 1.0, v114
	v_rcp_f32_e32 v160, v114
	v_add_f32_e32 v114, 1.0, v135
	v_max_f32_e32 v135, v169, v169
	v_max_f32_e32 v135, 0xc2a00000, v135
	v_max_f32_e32 v159, 0xc2a00000, v155
	v_mul_f32_e32 v155, 0xbfb8aa3b, v135
	v_exp_f32_e32 v155, v155
	v_mul_f32_e32 v161, 0xbfb8aa3b, v159
	v_exp_f32_e32 v168, v161
	v_max_f32_e32 v138, v138, v138
	v_rcp_f32_e32 v170, v114
	v_add_f32_e32 v114, 1.0, v155
	v_max_f32_e32 v138, 0xc2a00000, v138
	v_max_f32_e32 v155, v166, v166
	v_max_f32_e32 v166, 0xc2a00000, v155
	v_mul_f32_e32 v155, 0xbfb8aa3b, v138
	v_exp_f32_e32 v155, v155
	v_rcp_f32_e32 v161, v114
	v_add_f32_e32 v114, 1.0, v168
	v_mul_f32_e32 v168, 0xbfb8aa3b, v166
	v_exp_f32_e32 v168, v168
	v_max_f32_e32 v139, v139, v139
	v_rcp_f32_e32 v171, v114
	v_add_f32_e32 v114, 1.0, v155
	v_max_f32_e32 v139, 0xc2a00000, v139
	v_max_f32_e32 v155, v167, v167
	v_max_f32_e32 v167, 0xc2a00000, v155
	v_mul_f32_e32 v155, 0xbfb8aa3b, v139
	v_rcp_f32_e32 v178, v114
	v_add_f32_e32 v114, 1.0, v168
	v_exp_f32_e32 v155, v155
	v_mul_f32_e32 v168, 0xbfb8aa3b, v167
	v_exp_f32_e32 v168, v168
	v_rcp_f32_e32 v180, v114
	v_add_f32_e32 v114, 1.0, v155
	v_rcp_f32_e32 v179, v114
	v_add_f32_e32 v114, 1.0, v168
	v_rcp_f32_e32 v181, v114
	v_pk_mul_f32 v[168:169], v[134:135], v[160:161]
	v_pk_mul_f32 v[138:139], v[138:139], v[178:179]
	v_pk_mul_f32 v[170:171], v[158:159], v[170:171]
	v_pk_mul_f32 v[166:167], v[166:167], v[180:181]
.LBB0_374:
	ds_read_b32 v134, v176 offset:640
	s_mov_b64 s[14:15], 0x90000
	v_lshl_add_u64 v[158:159], v[136:137], 0, s[14:15]
	v_cvt_pk_bf16_f32 v137, v138, v139
	v_cvt_pk_bf16_f32 v138, v170, v171
	v_cvt_pk_bf16_f32 v139, v166, v167
	v_cvt_pk_bf16_f32 v136, v168, v169
	ds_bpermute_b32 v244, v250, v136
	ds_bpermute_b32 v245, v250, v137
	ds_bpermute_b32 v246, v250, v138
	ds_bpermute_b32 v247, v250, v139
	ds_bpermute_b32 v248, v250, v158
	s_waitcnt lgkmcnt(0)
	v_pk_mul_f32 v[168:169], v[30:31], v[134:135] op_sel_hi:[1,0]
	v_pk_mul_f32 v[166:167], v[28:29], v[134:135] op_sel_hi:[1,0]
	v_pk_mul_f32 v[138:139], v[32:33], v[134:135] op_sel_hi:[1,0]
	s_and_b64 vcc, exec, s[40:41]
	v_pk_mul_f32 v[170:171], v[26:27], v[134:135] op_sel_hi:[1,0]
	s_waitcnt lgkmcnt(0)
	v_subrev_u32_e32 v248, s82, v248
	global_store_dwordx4 v248, v[244:247], s[82:83] offset:64
	s_cbranch_vccnz .LBB0_376
	v_max_f32_e32 v114, v168, v168
	v_max_f32_e32 v136, 0xc2a00000, v114
	v_max_f32_e32 v114, v170, v170
	v_max_f32_e32 v158, 0xc2a00000, v114
	v_mul_f32_e32 v114, 0xbfb8aa3b, v136
	v_exp_f32_e32 v114, v114
	v_mul_f32_e32 v135, 0xbfb8aa3b, v158
	v_exp_f32_e32 v135, v135
	v_add_f32_e32 v114, 1.0, v114
	v_rcp_f32_e32 v160, v114
	v_add_f32_e32 v114, 1.0, v135
	v_max_f32_e32 v135, v169, v169
	v_max_f32_e32 v137, 0xc2a00000, v135
	v_max_f32_e32 v135, v171, v171
	v_max_f32_e32 v159, 0xc2a00000, v135
	v_mul_f32_e32 v135, 0xbfb8aa3b, v137
	v_exp_f32_e32 v135, v135
	v_mul_f32_e32 v155, 0xbfb8aa3b, v159
	v_rcp_f32_e32 v170, v114
	v_exp_f32_e32 v155, v155
	v_add_f32_e32 v114, 1.0, v135
	v_max_f32_e32 v135, v138, v138
	v_max_f32_e32 v138, 0xc2a00000, v135
	v_max_f32_e32 v135, v166, v166
	v_max_f32_e32 v166, 0xc2a00000, v135
	v_mul_f32_e32 v135, 0xbfb8aa3b, v138
	v_exp_f32_e32 v135, v135
	v_rcp_f32_e32 v161, v114
	v_add_f32_e32 v114, 1.0, v155
	v_mul_f32_e32 v155, 0xbfb8aa3b, v166
	v_exp_f32_e32 v155, v155
	v_rcp_f32_e32 v171, v114
	v_add_f32_e32 v114, 1.0, v135
	v_max_f32_e32 v135, v139, v139
	v_max_f32_e32 v139, 0xc2a00000, v135
	v_max_f32_e32 v135, v167, v167
	v_max_f32_e32 v167, 0xc2a00000, v135
	v_mul_f32_e32 v135, 0xbfb8aa3b, v139
	v_rcp_f32_e32 v178, v114
	v_add_f32_e32 v114, 1.0, v155
	v_exp_f32_e32 v135, v135
	v_mul_f32_e32 v155, 0xbfb8aa3b, v167
	v_exp_f32_e32 v155, v155
	v_rcp_f32_e32 v180, v114
	v_add_f32_e32 v114, 1.0, v135
	v_rcp_f32_e32 v179, v114
	v_add_f32_e32 v114, 1.0, v155
	v_rcp_f32_e32 v181, v114
	v_pk_mul_f32 v[168:169], v[136:137], v[160:161]
	v_pk_mul_f32 v[138:139], v[138:139], v[178:179]
	v_pk_mul_f32 v[170:171], v[158:159], v[170:171]
	v_pk_mul_f32 v[166:167], v[166:167], v[180:181]
.LBB0_376:
	v_lshlrev_b64 v[136:137], 12, v[152:153]
	v_lshl_add_u64 v[136:137], v[132:133], 0, v[136:137]
	s_mov_b32 s14, 0xa0000
	v_cvt_pk_bf16_f32 v168, v168, v169
	v_cvt_pk_bf16_f32 v169, v138, v139
	v_add_co_u32_e32 v138, vcc, s14, v136
	v_mov_b32_e32 v135, v134
	v_cvt_pk_bf16_f32 v170, v170, v171
	v_cvt_pk_bf16_f32 v171, v166, v167
	s_nop 0
	v_addc_co_u32_e32 v139, vcc, 0, v137, vcc
	v_mov_b32_e32 v158, v134
	v_mov_b32_e32 v159, v134
	ds_bpermute_b32 v232, v250, v168
	ds_bpermute_b32 v233, v250, v169
	ds_bpermute_b32 v234, v250, v170
	ds_bpermute_b32 v235, v250, v171
	ds_bpermute_b32 v236, v250, v138
	v_pk_mul_f32 v[138:139], v[24:25], v[158:159]
	v_pk_mul_f32 v[166:167], v[20:21], v[158:159]
	v_pk_mul_f32 v[168:169], v[22:23], v[134:135]
	s_and_b64 vcc, exec, s[40:41]
	v_pk_mul_f32 v[170:171], v[18:19], v[134:135]
	s_waitcnt lgkmcnt(0)
	v_subrev_u32_e32 v236, s82, v236
	global_store_dwordx4 v236, v[232:235], s[82:83]
	s_cbranch_vccnz .LBB0_378
	v_max_f32_e32 v114, v168, v168
	v_max_f32_e32 v134, 0xc2a00000, v114
	v_max_f32_e32 v114, v170, v170
	v_max_f32_e32 v158, 0xc2a00000, v114
	v_mul_f32_e32 v114, 0xbfb8aa3b, v134
	v_exp_f32_e32 v114, v114
	v_mul_f32_e32 v135, 0xbfb8aa3b, v158
	v_exp_f32_e32 v135, v135
	v_max_f32_e32 v155, v171, v171
	v_add_f32_e32 v114, 1.0, v114
	v_rcp_f32_e32 v160, v114
	v_add_f32_e32 v114, 1.0, v135
	v_max_f32_e32 v135, v169, v169
	v_max_f32_e32 v135, 0xc2a00000, v135
	v_max_f32_e32 v159, 0xc2a00000, v155
	v_mul_f32_e32 v155, 0xbfb8aa3b, v135
	v_exp_f32_e32 v155, v155
	v_mul_f32_e32 v161, 0xbfb8aa3b, v159
	v_exp_f32_e32 v168, v161
	v_max_f32_e32 v138, v138, v138
	v_rcp_f32_e32 v170, v114
	v_add_f32_e32 v114, 1.0, v155
	v_max_f32_e32 v138, 0xc2a00000, v138
	v_max_f32_e32 v155, v166, v166
	v_max_f32_e32 v166, 0xc2a00000, v155
	v_mul_f32_e32 v155, 0xbfb8aa3b, v138
	v_exp_f32_e32 v155, v155
	v_rcp_f32_e32 v161, v114
	v_add_f32_e32 v114, 1.0, v168
	v_mul_f32_e32 v168, 0xbfb8aa3b, v166
	v_exp_f32_e32 v168, v168
	v_max_f32_e32 v139, v139, v139
	v_rcp_f32_e32 v171, v114
	v_add_f32_e32 v114, 1.0, v155
	v_max_f32_e32 v139, 0xc2a00000, v139
	v_max_f32_e32 v155, v167, v167
	v_max_f32_e32 v167, 0xc2a00000, v155
	v_mul_f32_e32 v155, 0xbfb8aa3b, v139
	v_rcp_f32_e32 v178, v114
	v_add_f32_e32 v114, 1.0, v168
	v_exp_f32_e32 v155, v155
	v_mul_f32_e32 v168, 0xbfb8aa3b, v167
	v_exp_f32_e32 v168, v168
	v_rcp_f32_e32 v180, v114
	v_add_f32_e32 v114, 1.0, v155
	v_rcp_f32_e32 v179, v114
	v_add_f32_e32 v114, 1.0, v168
	v_rcp_f32_e32 v181, v114
	v_pk_mul_f32 v[168:169], v[134:135], v[160:161]
	v_pk_mul_f32 v[138:139], v[138:139], v[178:179]
	v_pk_mul_f32 v[170:171], v[158:159], v[170:171]
	v_pk_mul_f32 v[166:167], v[166:167], v[180:181]
.LBB0_378:
	ds_read_b32 v134, v176 offset:704
	s_mov_b64 s[14:15], 0xa0000
	v_lshl_add_u64 v[158:159], v[136:137], 0, s[14:15]
	v_cvt_pk_bf16_f32 v136, v168, v169
	v_cvt_pk_bf16_f32 v137, v138, v139
	v_cvt_pk_bf16_f32 v138, v170, v171
	v_cvt_pk_bf16_f32 v139, v166, v167
	ds_bpermute_b32 v238, v250, v136
	ds_bpermute_b32 v239, v250, v137
	ds_bpermute_b32 v240, v250, v138
	ds_bpermute_b32 v241, v250, v139
	ds_bpermute_b32 v242, v250, v158
	s_waitcnt lgkmcnt(0)
	v_pk_mul_f32 v[166:167], v[14:15], v[134:135] op_sel_hi:[1,0]
	s_and_b64 vcc, exec, s[40:41]
	v_pk_mul_f32 v[136:137], v[16:17], v[134:135] op_sel_hi:[1,0]
	v_pk_mul_f32 v[138:139], v[12:13], v[134:135] op_sel_hi:[1,0]
	v_pk_mul_f32 v[168:169], v[10:11], v[134:135] op_sel_hi:[1,0]
	s_waitcnt lgkmcnt(0)
	v_subrev_u32_e32 v242, s82, v242
	global_store_dwordx4 v242, v[238:241], s[82:83] offset:64
	s_cbranch_vccnz .LBB0_380
	v_max_f32_e32 v114, v166, v166
	v_max_f32_e32 v158, 0xc2a00000, v114
	v_max_f32_e32 v114, v168, v168
	v_max_f32_e32 v160, 0xc2a00000, v114
	v_mul_f32_e32 v114, 0xbfb8aa3b, v158
	v_exp_f32_e32 v114, v114
	v_mul_f32_e32 v135, 0xbfb8aa3b, v160
	v_exp_f32_e32 v135, v135
	v_add_f32_e32 v114, 1.0, v114
	v_rcp_f32_e32 v166, v114
	v_add_f32_e32 v114, 1.0, v135
	v_max_f32_e32 v135, v167, v167
	v_max_f32_e32 v159, 0xc2a00000, v135
	v_max_f32_e32 v135, v169, v169
	v_max_f32_e32 v161, 0xc2a00000, v135
	v_mul_f32_e32 v135, 0xbfb8aa3b, v159
	v_exp_f32_e32 v135, v135
	v_mul_f32_e32 v155, 0xbfb8aa3b, v161
	v_rcp_f32_e32 v168, v114
	v_exp_f32_e32 v155, v155
	v_add_f32_e32 v114, 1.0, v135
	v_max_f32_e32 v135, v136, v136
	v_max_f32_e32 v136, 0xc2a00000, v135
	v_max_f32_e32 v135, v138, v138
	v_max_f32_e32 v138, 0xc2a00000, v135
	v_mul_f32_e32 v135, 0xbfb8aa3b, v136
	v_exp_f32_e32 v135, v135
	v_rcp_f32_e32 v167, v114
	v_add_f32_e32 v114, 1.0, v155
	v_mul_f32_e32 v155, 0xbfb8aa3b, v138
	v_exp_f32_e32 v155, v155
	v_rcp_f32_e32 v169, v114
	v_add_f32_e32 v114, 1.0, v135
	v_max_f32_e32 v135, v137, v137
	v_max_f32_e32 v137, 0xc2a00000, v135
	v_max_f32_e32 v135, v139, v139
	v_max_f32_e32 v139, 0xc2a00000, v135
	v_mul_f32_e32 v135, 0xbfb8aa3b, v137
	v_rcp_f32_e32 v170, v114
	v_add_f32_e32 v114, 1.0, v155
	v_exp_f32_e32 v135, v135
	v_mul_f32_e32 v155, 0xbfb8aa3b, v139
	v_exp_f32_e32 v155, v155
	v_rcp_f32_e32 v178, v114
	v_add_f32_e32 v114, 1.0, v135
	v_rcp_f32_e32 v171, v114
	v_add_f32_e32 v114, 1.0, v155
	v_rcp_f32_e32 v179, v114
	v_pk_mul_f32 v[166:167], v[158:159], v[166:167]
	v_pk_mul_f32 v[136:137], v[136:137], v[170:171]
	v_pk_mul_f32 v[168:169], v[160:161], v[168:169]
	v_pk_mul_f32 v[138:139], v[138:139], v[178:179]
.LBB0_380:
	v_lshlrev_b64 v[158:159], 12, v[152:153]
	v_lshl_add_u64 v[132:133], v[132:133], 0, v[158:159]
	s_mov_b32 s14, 0xb0000
	v_cvt_pk_bf16_f32 v166, v166, v167
	v_cvt_pk_bf16_f32 v167, v136, v137
	v_add_co_u32_e32 v136, vcc, s14, v132
	v_mov_b32_e32 v135, v134
	s_nop 0
	v_addc_co_u32_e32 v137, vcc, 0, v133, vcc
	v_cvt_pk_bf16_f32 v168, v168, v169
	v_cvt_pk_bf16_f32 v169, v138, v139
	ds_bpermute_b32 v244, v250, v166
	ds_bpermute_b32 v245, v250, v167
	ds_bpermute_b32 v246, v250, v168
	ds_bpermute_b32 v247, v250, v169
	ds_bpermute_b32 v248, v250, v136
	v_mov_b32_e32 v136, v134
	v_mov_b32_e32 v137, v134
	v_pk_mul_f32 v[138:139], v[8:9], v[136:137]
	v_pk_mul_f32 v[168:169], v[6:7], v[134:135]
	v_pk_mul_f32 v[166:167], v[4:5], v[136:137]
	s_and_b64 vcc, exec, s[40:41]
	v_pk_mul_f32 v[134:135], v[2:3], v[134:135]
	s_waitcnt lgkmcnt(0)
	v_subrev_u32_e32 v248, s82, v248
	global_store_dwordx4 v248, v[244:247], s[82:83]
	s_cbranch_vccnz .LBB0_382
	v_max_f32_e32 v114, v168, v168
	v_max_f32_e32 v136, 0xc2a00000, v114
	v_max_f32_e32 v114, v134, v134
	v_max_f32_e32 v134, 0xc2a00000, v114
	v_mul_f32_e32 v114, 0xbfb8aa3b, v136
	v_exp_f32_e32 v114, v114
	v_mul_f32_e32 v137, 0xbfb8aa3b, v134
	v_exp_f32_e32 v137, v137
	v_max_f32_e32 v135, v135, v135
	v_add_f32_e32 v114, 1.0, v114
	v_rcp_f32_e32 v158, v114
	v_add_f32_e32 v114, 1.0, v137
	v_max_f32_e32 v137, v169, v169
	v_max_f32_e32 v137, 0xc2a00000, v137
	v_mul_f32_e32 v153, 0xbfb8aa3b, v137
	v_exp_f32_e32 v153, v153
	v_max_f32_e32 v135, 0xc2a00000, v135
	v_mul_f32_e32 v155, 0xbfb8aa3b, v135
	v_exp_f32_e32 v155, v155
	v_max_f32_e32 v138, v138, v138
	v_rcp_f32_e32 v160, v114
	v_add_f32_e32 v114, 1.0, v153
	v_max_f32_e32 v138, 0xc2a00000, v138
	v_max_f32_e32 v153, v166, v166
	v_max_f32_e32 v166, 0xc2a00000, v153
	v_mul_f32_e32 v153, 0xbfb8aa3b, v138
	v_exp_f32_e32 v153, v153
	v_rcp_f32_e32 v159, v114
	v_add_f32_e32 v114, 1.0, v155
	v_mul_f32_e32 v155, 0xbfb8aa3b, v166
	v_exp_f32_e32 v155, v155
	v_max_f32_e32 v139, v139, v139
	v_rcp_f32_e32 v161, v114
	v_add_f32_e32 v114, 1.0, v153
	v_max_f32_e32 v139, 0xc2a00000, v139
	v_max_f32_e32 v153, v167, v167
	v_max_f32_e32 v167, 0xc2a00000, v153
	v_mul_f32_e32 v153, 0xbfb8aa3b, v139
	v_rcp_f32_e32 v170, v114
	v_add_f32_e32 v114, 1.0, v155
	v_exp_f32_e32 v153, v153
	v_mul_f32_e32 v155, 0xbfb8aa3b, v167
	v_exp_f32_e32 v155, v155
	v_rcp_f32_e32 v178, v114
	v_add_f32_e32 v114, 1.0, v153
	v_rcp_f32_e32 v171, v114
	v_add_f32_e32 v114, 1.0, v155
	v_rcp_f32_e32 v179, v114
	v_pk_mul_f32 v[168:169], v[136:137], v[158:159]
	v_pk_mul_f32 v[138:139], v[138:139], v[170:171]
	v_pk_mul_f32 v[134:135], v[134:135], v[160:161]
	v_pk_mul_f32 v[166:167], v[166:167], v[178:179]

.LBB0_383:
	s_andn2_b64 vcc, exec, s[38:39]
	s_mov_b64 s[28:29], -1
	ds_bpermute_b32 v232, v250, v132
	ds_bpermute_b32 v233, v250, v133
	ds_bpermute_b32 v234, v250, v134
	ds_bpermute_b32 v235, v250, v135
	ds_bpermute_b32 v236, v250, v136
	s_waitcnt lgkmcnt(0)
	v_subrev_u32_e32 v236, s82, v236
	global_store_dwordx4 v236, v[232:235], s[82:83] offset:64
	s_cbranch_vccnz .LBB0_338
	s_branch .LBB0_386
.LBB0_384:
	s_and_b64 vcc, exec, s[40:41]
	s_cbranch_vccz .LBB0_383
	v_lshlrev_b32_e32 v155, 2, v177
	global_load_dwordx4 v[136:139], v155, s[44:45]
	global_load_dwordx4 v[132:135], v155, s[44:45] offset:16
	s_waitcnt lgkmcnt(0)
	v_mul_f32_e32 v160, v128, v154
	v_mul_f32_e32 v161, v129, v154
	v_mul_f32_e32 v166, v130, v154
	v_mul_f32_e32 v167, v131, v154
	v_mul_f32_e32 v168, v124, v154
	v_mul_f32_e32 v169, v125, v154
	v_mul_f32_e32 v170, v126, v154
	v_mul_f32_e32 v171, v127, v154
	global_load_dwordx4 v[124:127], v155, s[44:45] offset:144
	global_load_dwordx4 v[128:131], v155, s[44:45] offset:128
	v_ashrrev_i32_e32 v153, 31, v152
	v_lshlrev_b64 v[158:159], 12, v[152:153]
	v_max_f32_e32 v153, 0xc2a00000, v160
	v_max_f32_e32 v155, 0xc2a00000, v161
	v_max_f32_e32 v160, 0xc2a00000, v166
	v_max_f32_e32 v161, 0xc2a00000, v167
	v_max_f32_e32 v166, 0xc2a00000, v168
	v_max_f32_e32 v167, 0xc2a00000, v169
	v_max_f32_e32 v168, 0xc2a00000, v170
	v_max_f32_e32 v169, 0xc2a00000, v171
	v_mul_f32_e32 v153, 0xbfb8aa3b, v153
	v_mul_f32_e32 v155, 0xbfb8aa3b, v155
	v_mul_f32_e32 v168, 0xbfb8aa3b, v168
	v_mul_f32_e32 v169, 0xbfb8aa3b, v169
	v_exp_f32_e32 v153, v153
	v_exp_f32_e32 v155, v155
	v_mul_f32_e32 v160, 0xbfb8aa3b, v160
	v_mul_f32_e32 v161, 0xbfb8aa3b, v161
	v_exp_f32_e32 v168, v168
	v_exp_f32_e32 v169, v169
	v_exp_f32_e32 v160, v160
	v_exp_f32_e32 v161, v161
	v_mul_f32_e32 v120, v120, v154
	v_max_f32_e32 v120, 0xc2a00000, v120
	v_add_f32_e32 v153, 1.0, v153
	v_add_f32_e32 v155, 1.0, v155
	v_mul_f32_e32 v121, v121, v154
	v_lshlrev_b32_e32 v114, 1, v177
	v_mul_f32_e32 v166, 0xbfb8aa3b, v166
	v_mul_f32_e32 v167, 0xbfb8aa3b, v167
	v_lshl_add_u64 v[158:159], s[42:43], 0, v[158:159]
	v_add_f32_e32 v168, 1.0, v168
	v_add_f32_e32 v169, 1.0, v169
	v_rcp_f32_e32 v153, v153
	v_rcp_f32_e32 v181, v155
	v_mul_f32_e32 v120, 0xbfb8aa3b, v120
	v_max_f32_e32 v121, 0xc2a00000, v121
	v_exp_f32_e32 v170, v166
	v_exp_f32_e32 v171, v167
	v_lshl_add_u64 v[166:167], v[158:159], 0, v[114:115]
	v_add_f32_e32 v158, 1.0, v160
	v_add_f32_e32 v159, 1.0, v161
	v_rcp_f32_e32 v168, v168
	v_rcp_f32_e32 v182, v169
	v_exp_f32_e32 v120, v120
	v_mul_f32_e32 v121, 0xbfb8aa3b, v121
	v_rcp_f32_e32 v158, v158
	v_rcp_f32_e32 v159, v159
	v_exp_f32_e32 v121, v121
	v_add_f32_e32 v120, 1.0, v120
	v_rcp_f32_e32 v120, v120
	v_mul_f32_e32 v116, v116, v154
	v_add_f32_e32 v121, 1.0, v121
	v_rcp_f32_e32 v121, v121
	v_add_f32_e32 v160, 1.0, v170
	v_add_f32_e32 v161, 1.0, v171
	v_max_f32_e32 v116, 0xc2a00000, v116
	v_mul_f32_e32 v117, v117, v154
	v_rcp_f32_e32 v160, v160
	v_rcp_f32_e32 v161, v161
	v_mul_f32_e32 v116, 0xbfb8aa3b, v116
	v_max_f32_e32 v117, 0xc2a00000, v117
	v_exp_f32_e32 v116, v116
	v_mul_f32_e32 v117, 0xbfb8aa3b, v117
	v_exp_f32_e32 v117, v117
	s_mov_b64 s[14:15], 0x80000
	v_add_f32_e32 v116, 1.0, v116
	v_rcp_f32_e32 v116, v116
	v_add_f32_e32 v117, 1.0, v117
	s_waitcnt vmcnt(0)
	v_sub_f32_e32 v180, 1.0, v136
	v_sub_f32_e32 v179, 1.0, v137
	v_sub_f32_e32 v169, 1.0, v134
	v_sub_f32_e32 v155, 1.0, v135
	v_fma_f32 v153, v180, v153, v136
	v_fma_f32 v181, v179, v181, v137
	v_sub_f32_e32 v178, 1.0, v138
	v_sub_f32_e32 v177, 1.0, v139
	v_fma_f32 v168, v169, v168, v134
	v_fma_f32 v182, v155, v182, v135
	v_log_f32_e32 v153, v153
	v_log_f32_e32 v181, v181
	v_fma_f32 v158, v178, v158, v138
	v_fma_f32 v159, v177, v159, v139
	v_log_f32_e32 v168, v168
	v_log_f32_e32 v182, v182
	v_log_f32_e32 v158, v158
	v_log_f32_e32 v159, v159
	v_cvt_pk_f16_f32 v194, v153, v181
	v_sub_f32_e32 v153, 1.0, v128
	v_cvt_pk_f16_f32 v197, v168, v182
	v_fma_f32 v120, v153, v120, v128
	v_sub_f32_e32 v168, 1.0, v129
	v_cvt_pk_f16_f32 v195, v158, v159
	v_log_f32_e32 v158, v120
	v_fma_f32 v120, v168, v121, v129
	v_log_f32_e32 v159, v120
	v_mul_f32_e32 v120, v122, v154
	v_max_f32_e32 v120, 0xc2a00000, v120
	v_mul_f32_e32 v121, v123, v154
	v_mul_f32_e32 v120, 0xbfb8aa3b, v120
	v_max_f32_e32 v121, 0xc2a00000, v121
	v_exp_f32_e32 v120, v120
	v_mul_f32_e32 v121, 0xbfb8aa3b, v121
	v_exp_f32_e32 v122, v121
	v_sub_f32_e32 v171, 1.0, v132
	v_sub_f32_e32 v170, 1.0, v133
	v_add_f32_e32 v120, 1.0, v120
	v_fma_f32 v160, v171, v160, v132
	v_fma_f32 v161, v170, v161, v133
	v_rcp_f32_e32 v120, v120
	v_add_f32_e32 v122, 1.0, v122
	v_log_f32_e32 v160, v160
	v_log_f32_e32 v161, v161
	v_rcp_f32_e32 v123, v122
	v_sub_f32_e32 v121, 1.0, v130
	v_rcp_f32_e32 v117, v117
	v_fma_f32 v120, v121, v120, v130
	v_sub_f32_e32 v122, 1.0, v131
	v_cvt_pk_f16_f32 v196, v160, v161
	v_log_f32_e32 v160, v120
	v_fma_f32 v120, v122, v123, v131
	v_sub_f32_e32 v123, 1.0, v124
	v_log_f32_e32 v161, v120
	v_fma_f32 v116, v123, v116, v124
	v_sub_f32_e32 v120, 1.0, v125
	v_log_f32_e32 v181, v116
	v_fma_f32 v116, v120, v117, v125
	v_log_f32_e32 v182, v116
	v_mul_f32_e32 v116, v118, v154
	v_max_f32_e32 v116, 0xc2a00000, v116
	v_mul_f32_e32 v117, v119, v154
	v_mul_f32_e32 v116, 0xbfb8aa3b, v116
	v_max_f32_e32 v117, 0xc2a00000, v117
	v_exp_f32_e32 v116, v116
	v_mul_f32_e32 v117, 0xbfb8aa3b, v117
	v_exp_f32_e32 v117, v117
	v_sub_f32_e32 v118, 1.0, v126
	v_add_f32_e32 v116, 1.0, v116
	v_rcp_f32_e32 v116, v116
	v_add_f32_e32 v117, 1.0, v117
	v_rcp_f32_e32 v117, v117
	v_sub_f32_e32 v119, 1.0, v127
	v_fma_f32 v116, v118, v116, v126
	v_log_f32_e32 v154, v116
	v_fma_f32 v116, v119, v117, v127
	v_log_f32_e32 v183, v116
	ds_read2_b32 v[116:117], v176 offset0:16 offset1:32
	ds_bpermute_b32 v238, v250, v194
	ds_bpermute_b32 v239, v250, v195
	ds_bpermute_b32 v240, v250, v196
	ds_bpermute_b32 v241, v250, v197
	ds_bpermute_b32 v242, v250, v166
	s_waitcnt lgkmcnt(0)
	v_mul_f32_e32 v106, v106, v116
	v_max_f32_e32 v106, 0xc2a00000, v106
	v_mul_f32_e32 v106, 0xbfb8aa3b, v106
	v_exp_f32_e32 v106, v106
	v_mul_f32_e32 v110, v110, v116
	v_max_f32_e32 v110, 0xc2a00000, v110
	v_mul_f32_e32 v111, v111, v116
	v_mul_f32_e32 v110, 0xbfb8aa3b, v110
	v_max_f32_e32 v111, 0xc2a00000, v111
	v_mul_f32_e32 v107, v107, v116
	v_exp_f32_e32 v110, v110
	v_mul_f32_e32 v111, 0xbfb8aa3b, v111
	v_add_f32_e32 v106, 1.0, v106
	v_max_f32_e32 v107, 0xc2a00000, v107
	v_exp_f32_e32 v111, v111
	v_rcp_f32_e32 v106, v106
	v_mul_f32_e32 v107, 0xbfb8aa3b, v107
	v_exp_f32_e32 v107, v107
	v_cvt_pk_f16_f32 v194, v158, v159
	v_or_b32_e32 v158, 16, v152
	v_add_f32_e32 v110, 1.0, v110
	v_mul_f32_e32 v112, v112, v116
	v_mul_f32_e32 v113, v113, v116
	v_cvt_pk_f16_f32 v197, v154, v183
	v_ashrrev_i32_e32 v159, 31, v158
	v_rcp_f32_e32 v154, v110
	v_add_f32_e32 v110, 1.0, v111
	v_max_f32_e32 v112, 0xc2a00000, v112
	v_max_f32_e32 v113, 0xc2a00000, v113
	v_fma_f32 v106, v171, v106, v132
	v_cvt_pk_f16_f32 v195, v160, v161
	v_rcp_f32_e32 v160, v110
	v_lshlrev_b64 v[110:111], 12, v[158:159]
	v_mul_f32_e32 v112, 0xbfb8aa3b, v112
	v_mul_f32_e32 v113, 0xbfb8aa3b, v113
	v_log_f32_e32 v159, v106
	v_add_f32_e32 v106, 1.0, v107
	v_mul_f32_e32 v107, v108, v116
	v_exp_f32_e32 v112, v112
	v_exp_f32_e32 v113, v113
	v_max_f32_e32 v107, 0xc2a00000, v107
	v_mul_f32_e32 v108, v109, v116
	v_mul_f32_e32 v107, 0xbfb8aa3b, v107
	v_max_f32_e32 v108, 0xc2a00000, v108
	v_exp_f32_e32 v107, v107
	v_mul_f32_e32 v108, 0xbfb8aa3b, v108
	v_exp_f32_e32 v108, v108
	v_add_f32_e32 v112, 1.0, v112
	v_add_f32_e32 v113, 1.0, v113
	v_rcp_f32_e32 v112, v112
	v_rcp_f32_e32 v113, v113
	v_mul_f32_e32 v98, v98, v116
	v_rcp_f32_e32 v106, v106
	v_add_f32_e32 v107, 1.0, v107
	v_max_f32_e32 v98, 0xc2a00000, v98
	v_rcp_f32_e32 v107, v107
	v_add_f32_e32 v108, 1.0, v108
	v_mul_f32_e32 v98, 0xbfb8aa3b, v98
	v_rcp_f32_e32 v108, v108
	v_exp_f32_e32 v98, v98
	v_fma_f32 v112, v178, v112, v138
	v_fma_f32 v113, v177, v113, v139
	v_log_f32_e32 v112, v112
	v_log_f32_e32 v113, v113
	v_fma_f32 v106, v170, v106, v133
	v_log_f32_e32 v109, v106
	v_fma_f32 v106, v169, v107, v134
	v_mul_f32_e32 v102, v102, v116
	v_mul_f32_e32 v99, v99, v116
	v_fma_f32 v154, v180, v154, v136
	v_fma_f32 v158, v179, v160, v137
	v_log_f32_e32 v160, v106
	v_fma_f32 v106, v155, v108, v135
	v_max_f32_e32 v102, 0xc2a00000, v102
	v_add_f32_e32 v98, 1.0, v98
	v_max_f32_e32 v99, 0xc2a00000, v99
	v_log_f32_e32 v154, v154
	v_log_f32_e32 v158, v158
	v_log_f32_e32 v161, v106
	v_mul_f32_e32 v102, 0xbfb8aa3b, v102
	v_rcp_f32_e32 v98, v98
	v_mul_f32_e32 v99, 0xbfb8aa3b, v99
	v_cvt_pk_f16_f32 v107, v112, v113
	v_exp_f32_e32 v112, v102
	v_mul_f32_e32 v102, v103, v116
	v_exp_f32_e32 v99, v99
	v_max_f32_e32 v102, 0xc2a00000, v102
	v_lshl_add_u64 v[110:111], s[42:43], 0, v[110:111]
	v_mul_f32_e32 v102, 0xbfb8aa3b, v102
	v_cvt_pk_f16_f32 v106, v154, v158
	v_cvt_pk_f16_f32 v108, v159, v109
	v_cvt_pk_f16_f32 v109, v160, v161
	v_exp_f32_e32 v113, v102
	v_lshl_add_u64 v[102:103], v[110:111], 0, v[114:115]
	v_fma_f32 v98, v123, v98, v124
	ds_bpermute_b32 v244, v250, v106
	ds_bpermute_b32 v245, v250, v107
	ds_bpermute_b32 v246, v250, v108
	ds_bpermute_b32 v247, v250, v109
	ds_bpermute_b32 v248, v250, v102
	v_mul_f32_e32 v104, v104, v116
	v_mul_f32_e32 v105, v105, v116
	v_log_f32_e32 v108, v98
	v_add_f32_e32 v98, 1.0, v99
	v_mul_f32_e32 v99, v100, v116
	v_max_f32_e32 v99, 0xc2a00000, v99
	v_mul_f32_e32 v100, v101, v116
	v_max_f32_e32 v104, 0xc2a00000, v104
	v_max_f32_e32 v105, 0xc2a00000, v105
	v_mul_f32_e32 v99, 0xbfb8aa3b, v99
	v_max_f32_e32 v100, 0xc2a00000, v100
	v_mul_f32_e32 v104, 0xbfb8aa3b, v104
	v_mul_f32_e32 v105, 0xbfb8aa3b, v105
	v_exp_f32_e32 v99, v99
	v_mul_f32_e32 v100, 0xbfb8aa3b, v100
	v_exp_f32_e32 v104, v104
	v_exp_f32_e32 v105, v105
	v_exp_f32_e32 v100, v100
	v_rcp_f32_e32 v98, v98
	v_add_f32_e32 v99, 1.0, v99
	v_add_f32_e32 v110, 1.0, v112
	v_add_f32_e32 v111, 1.0, v113
	v_add_f32_e32 v104, 1.0, v104
	v_add_f32_e32 v105, 1.0, v105
	v_rcp_f32_e32 v99, v99
	v_add_f32_e32 v100, 1.0, v100
	v_rcp_f32_e32 v110, v110
	v_rcp_f32_e32 v111, v111
	v_rcp_f32_e32 v104, v104
	v_rcp_f32_e32 v105, v105
	v_rcp_f32_e32 v100, v100
	v_mul_f32_e32 v90, v90, v117
	v_fma_f32 v98, v120, v98, v125
	v_mul_f32_e32 v94, v94, v117
	v_max_f32_e32 v90, 0xc2a00000, v90
	v_log_f32_e32 v101, v98
	v_fma_f32 v98, v118, v99, v126
	v_max_f32_e32 v94, 0xc2a00000, v94
	v_mul_f32_e32 v90, 0xbfb8aa3b, v90
	v_fma_f32 v106, v153, v110, v128
	v_fma_f32 v107, v168, v111, v129
	v_fma_f32 v104, v121, v104, v130
	v_fma_f32 v105, v122, v105, v131
	v_log_f32_e32 v109, v98
	v_fma_f32 v98, v119, v100, v127
	v_mul_f32_e32 v94, 0xbfb8aa3b, v94
	v_exp_f32_e32 v90, v90
	v_log_f32_e32 v106, v106
	v_log_f32_e32 v107, v107
	v_log_f32_e32 v104, v104
	v_log_f32_e32 v105, v105
	v_log_f32_e32 v110, v98
	v_exp_f32_e32 v94, v94
	v_mul_f32_e32 v95, v95, v117
	v_max_f32_e32 v95, 0xc2a00000, v95
	v_mul_f32_e32 v91, v91, v117
	v_mul_f32_e32 v95, 0xbfb8aa3b, v95
	v_add_f32_e32 v90, 1.0, v90
	v_max_f32_e32 v91, 0xc2a00000, v91
	v_cvt_pk_f16_f32 v98, v106, v107
	v_cvt_pk_f16_f32 v99, v104, v105
	v_cvt_pk_f16_f32 v100, v108, v101
	v_cvt_pk_f16_f32 v101, v109, v110
	v_exp_f32_e32 v95, v95
	v_add_f32_e32 v94, 1.0, v94
	v_rcp_f32_e32 v90, v90
	v_mul_f32_e32 v91, 0xbfb8aa3b, v91
	s_waitcnt lgkmcnt(5)
	v_subrev_u32_e32 v242, s82, v242
	global_store_dwordx4 v242, v[238:241], s[82:83]
	ds_bpermute_b32 v232, v250, v98
	ds_bpermute_b32 v233, v250, v99
	ds_bpermute_b32 v234, v250, v100
	ds_bpermute_b32 v235, v250, v101
	ds_bpermute_b32 v236, v250, v102
	v_exp_f32_e32 v91, v91
	v_fma_f32 v90, v171, v90, v132
	v_rcp_f32_e32 v100, v94
	v_or_b32_e32 v98, 32, v152
	v_ashrrev_i32_e32 v99, 31, v98
	v_add_f32_e32 v94, 1.0, v95
	v_rcp_f32_e32 v101, v94
	v_lshlrev_b64 v[94:95], 12, v[98:99]
	v_fma_f32 v98, v180, v100, v136
	v_log_f32_e32 v100, v90
	v_add_f32_e32 v90, 1.0, v91
	v_mul_f32_e32 v91, v92, v117
	v_mul_f32_e32 v96, v96, v117
	v_mul_f32_e32 v97, v97, v117
	v_max_f32_e32 v91, 0xc2a00000, v91
	v_mul_f32_e32 v92, v93, v117
	v_max_f32_e32 v96, 0xc2a00000, v96
	v_max_f32_e32 v97, 0xc2a00000, v97
	v_mul_f32_e32 v91, 0xbfb8aa3b, v91
	v_max_f32_e32 v92, 0xc2a00000, v92
	v_mul_f32_e32 v96, 0xbfb8aa3b, v96
	v_mul_f32_e32 v97, 0xbfb8aa3b, v97
	v_exp_f32_e32 v91, v91
	v_mul_f32_e32 v92, 0xbfb8aa3b, v92
	v_exp_f32_e32 v96, v96
	v_exp_f32_e32 v97, v97
	v_exp_f32_e32 v92, v92
	v_mul_f32_e32 v82, v82, v117
	v_rcp_f32_e32 v90, v90
	v_add_f32_e32 v91, 1.0, v91
	v_max_f32_e32 v82, 0xc2a00000, v82
	v_add_f32_e32 v96, 1.0, v96
	v_add_f32_e32 v97, 1.0, v97
	v_rcp_f32_e32 v91, v91
	v_add_f32_e32 v92, 1.0, v92
	v_mul_f32_e32 v82, 0xbfb8aa3b, v82
	v_rcp_f32_e32 v96, v96
	v_rcp_f32_e32 v97, v97
	v_rcp_f32_e32 v92, v92
	v_exp_f32_e32 v82, v82
	v_fma_f32 v90, v170, v90, v133
	v_log_f32_e32 v93, v90
	v_fma_f32 v90, v169, v91, v134
	v_mul_f32_e32 v83, v83, v117
	v_fma_f32 v99, v179, v101, v137
	v_fma_f32 v96, v178, v96, v138
	v_fma_f32 v97, v177, v97, v139
	v_log_f32_e32 v101, v90
	v_fma_f32 v90, v155, v92, v135
	v_add_f32_e32 v82, 1.0, v82
	v_max_f32_e32 v83, 0xc2a00000, v83
	v_log_f32_e32 v98, v98
	v_log_f32_e32 v99, v99
	v_log_f32_e32 v96, v96
	v_log_f32_e32 v97, v97
	v_log_f32_e32 v102, v90
	v_rcp_f32_e32 v82, v82
	v_mul_f32_e32 v83, 0xbfb8aa3b, v83
	v_exp_f32_e32 v83, v83
	v_lshl_add_u64 v[94:95], s[42:43], 0, v[94:95]
	v_cvt_pk_f16_f32 v90, v98, v99
	v_cvt_pk_f16_f32 v91, v96, v97
	v_cvt_pk_f16_f32 v92, v100, v93
	v_cvt_pk_f16_f32 v93, v101, v102
	v_lshl_add_u64 v[94:95], v[94:95], 0, v[114:115]
	v_fma_f32 v82, v123, v82, v124
	s_waitcnt lgkmcnt(5)
	v_subrev_u32_e32 v248, s82, v248
	global_store_dwordx4 v248, v[244:247], s[82:83]
	ds_bpermute_b32 v238, v250, v90
	ds_bpermute_b32 v239, v250, v91
	ds_bpermute_b32 v240, v250, v92
	ds_bpermute_b32 v241, v250, v93
	ds_bpermute_b32 v242, v250, v94
	v_mul_f32_e32 v86, v86, v117
	v_mul_f32_e32 v87, v87, v117
	v_log_f32_e32 v90, v82
	v_add_f32_e32 v82, 1.0, v83
	v_mul_f32_e32 v83, v84, v117
	v_max_f32_e32 v83, 0xc2a00000, v83
	v_mul_f32_e32 v84, v85, v117
	v_mul_f32_e32 v83, 0xbfb8aa3b, v83
	v_max_f32_e32 v84, 0xc2a00000, v84
	v_exp_f32_e32 v83, v83
	v_mul_f32_e32 v84, 0xbfb8aa3b, v84
	v_exp_f32_e32 v84, v84
	v_rcp_f32_e32 v82, v82
	v_add_f32_e32 v83, 1.0, v83
	v_rcp_f32_e32 v83, v83
	v_add_f32_e32 v84, 1.0, v84
	v_rcp_f32_e32 v84, v84
	v_mul_f32_e32 v88, v88, v117
	v_mul_f32_e32 v89, v89, v117
	v_max_f32_e32 v86, 0xc2a00000, v86
	v_max_f32_e32 v87, 0xc2a00000, v87
	v_max_f32_e32 v88, 0xc2a00000, v88
	v_max_f32_e32 v89, 0xc2a00000, v89
	v_fma_f32 v82, v120, v82, v125
	v_mul_f32_e32 v86, 0xbfb8aa3b, v86
	v_mul_f32_e32 v87, 0xbfb8aa3b, v87
	v_mul_f32_e32 v88, 0xbfb8aa3b, v88
	v_mul_f32_e32 v89, 0xbfb8aa3b, v89
	v_log_f32_e32 v91, v82
	v_fma_f32 v82, v118, v83, v126
	v_exp_f32_e32 v86, v86
	v_exp_f32_e32 v87, v87
	v_exp_f32_e32 v88, v88
	v_exp_f32_e32 v89, v89
	v_log_f32_e32 v92, v82
	v_fma_f32 v82, v119, v84, v127
	v_log_f32_e32 v93, v82
	ds_read2_b32 v[82:83], v176 offset0:48 offset1:128
	v_add_f32_e32 v86, 1.0, v86
	v_add_f32_e32 v87, 1.0, v87
	v_add_f32_e32 v88, 1.0, v88
	v_add_f32_e32 v89, 1.0, v89
	v_rcp_f32_e32 v86, v86
	v_rcp_f32_e32 v87, v87
	v_rcp_f32_e32 v88, v88
	v_rcp_f32_e32 v89, v89
	s_waitcnt lgkmcnt(0)
	v_mul_f32_e32 v74, v74, v82
	v_mul_f32_e32 v78, v78, v82
	v_max_f32_e32 v74, 0xc2a00000, v74
	v_max_f32_e32 v78, 0xc2a00000, v78
	v_mul_f32_e32 v74, 0xbfb8aa3b, v74
	v_fma_f32 v86, v153, v86, v128
	v_fma_f32 v87, v168, v87, v129
	v_fma_f32 v88, v121, v88, v130
	v_fma_f32 v89, v122, v89, v131
	v_mul_f32_e32 v78, 0xbfb8aa3b, v78
	v_exp_f32_e32 v74, v74
	v_log_f32_e32 v86, v86
	v_log_f32_e32 v87, v87
	v_log_f32_e32 v88, v88
	v_log_f32_e32 v89, v89
	v_exp_f32_e32 v78, v78
	v_mul_f32_e32 v79, v79, v82
	v_max_f32_e32 v79, 0xc2a00000, v79
	v_mul_f32_e32 v75, v75, v82
	v_mul_f32_e32 v79, 0xbfb8aa3b, v79
	v_add_f32_e32 v74, 1.0, v74
	v_max_f32_e32 v75, 0xc2a00000, v75
	v_cvt_pk_f16_f32 v84, v86, v87
	v_cvt_pk_f16_f32 v85, v88, v89
	v_cvt_pk_f16_f32 v86, v90, v91
	v_cvt_pk_f16_f32 v87, v92, v93
	v_exp_f32_e32 v79, v79
	v_add_f32_e32 v78, 1.0, v78
	v_rcp_f32_e32 v74, v74
	v_mul_f32_e32 v75, 0xbfb8aa3b, v75
	s_waitcnt lgkmcnt(6)
	v_subrev_u32_e32 v236, s82, v236
	global_store_dwordx4 v236, v[232:235], s[82:83] offset:64
	ds_bpermute_b32 v244, v250, v84
	ds_bpermute_b32 v245, v250, v85
	ds_bpermute_b32 v246, v250, v86
	ds_bpermute_b32 v247, v250, v87
	ds_bpermute_b32 v248, v250, v94
	v_exp_f32_e32 v75, v75
	v_mul_f32_e32 v80, v80, v82
	v_rcp_f32_e32 v86, v78
	v_or_b32_e32 v84, 48, v152
	v_mul_f32_e32 v81, v81, v82
	v_ashrrev_i32_e32 v85, 31, v84
	v_add_f32_e32 v78, 1.0, v79
	v_max_f32_e32 v80, 0xc2a00000, v80
	v_max_f32_e32 v81, 0xc2a00000, v81
	v_fma_f32 v74, v171, v74, v132
	v_rcp_f32_e32 v87, v78
	v_lshlrev_b64 v[78:79], 12, v[84:85]
	v_fma_f32 v84, v180, v86, v136
	v_mul_f32_e32 v80, 0xbfb8aa3b, v80
	v_mul_f32_e32 v81, 0xbfb8aa3b, v81
	v_log_f32_e32 v86, v74
	v_add_f32_e32 v74, 1.0, v75
	v_mul_f32_e32 v75, v76, v82
	v_exp_f32_e32 v80, v80
	v_exp_f32_e32 v81, v81
	v_max_f32_e32 v75, 0xc2a00000, v75
	v_mul_f32_e32 v76, v77, v82
	v_mul_f32_e32 v75, 0xbfb8aa3b, v75
	v_max_f32_e32 v76, 0xc2a00000, v76
	v_exp_f32_e32 v75, v75
	v_mul_f32_e32 v76, 0xbfb8aa3b, v76
	v_exp_f32_e32 v76, v76
	v_add_f32_e32 v80, 1.0, v80
	v_add_f32_e32 v81, 1.0, v81
	v_rcp_f32_e32 v80, v80
	v_rcp_f32_e32 v81, v81
	v_mul_f32_e32 v66, v66, v82
	v_rcp_f32_e32 v74, v74
	v_add_f32_e32 v75, 1.0, v75
	v_max_f32_e32 v66, 0xc2a00000, v66
	v_rcp_f32_e32 v75, v75
	v_add_f32_e32 v76, 1.0, v76
	v_mul_f32_e32 v66, 0xbfb8aa3b, v66
	v_rcp_f32_e32 v76, v76
	v_exp_f32_e32 v66, v66
	v_fma_f32 v80, v178, v80, v138
	v_fma_f32 v81, v177, v81, v139
	v_log_f32_e32 v80, v80
	v_log_f32_e32 v81, v81
	v_fma_f32 v74, v170, v74, v133
	v_log_f32_e32 v77, v74
	v_fma_f32 v74, v169, v75, v134
	v_mul_f32_e32 v70, v70, v82
	v_mul_f32_e32 v67, v67, v82
	v_fma_f32 v85, v179, v87, v137
	v_log_f32_e32 v87, v74
	v_fma_f32 v74, v155, v76, v135
	v_max_f32_e32 v70, 0xc2a00000, v70
	v_add_f32_e32 v66, 1.0, v66
	v_max_f32_e32 v67, 0xc2a00000, v67
	v_log_f32_e32 v84, v84
	v_log_f32_e32 v85, v85
	v_log_f32_e32 v88, v74
	v_mul_f32_e32 v70, 0xbfb8aa3b, v70
	v_rcp_f32_e32 v66, v66
	v_mul_f32_e32 v67, 0xbfb8aa3b, v67
	v_cvt_pk_f16_f32 v75, v80, v81
	v_exp_f32_e32 v80, v70
	v_mul_f32_e32 v70, v71, v82
	v_exp_f32_e32 v67, v67
	v_max_f32_e32 v70, 0xc2a00000, v70
	v_lshl_add_u64 v[78:79], s[42:43], 0, v[78:79]
	v_mul_f32_e32 v70, 0xbfb8aa3b, v70
	v_cvt_pk_f16_f32 v74, v84, v85
	v_cvt_pk_f16_f32 v76, v86, v77
	v_cvt_pk_f16_f32 v77, v87, v88
	v_exp_f32_e32 v81, v70
	v_lshl_add_u64 v[70:71], v[78:79], 0, v[114:115]
	v_fma_f32 v66, v123, v66, v124
	s_waitcnt lgkmcnt(6)
	v_subrev_u32_e32 v242, s82, v242
	global_store_dwordx4 v242, v[238:241], s[82:83]
	ds_bpermute_b32 v232, v250, v74
	ds_bpermute_b32 v233, v250, v75
	ds_bpermute_b32 v234, v250, v76
	ds_bpermute_b32 v235, v250, v77
	ds_bpermute_b32 v236, v250, v70
	v_mul_f32_e32 v72, v72, v82
	v_mul_f32_e32 v73, v73, v82
	v_log_f32_e32 v76, v66
	v_add_f32_e32 v66, 1.0, v67
	v_mul_f32_e32 v67, v68, v82
	v_max_f32_e32 v67, 0xc2a00000, v67
	v_mul_f32_e32 v68, v69, v82
	v_max_f32_e32 v72, 0xc2a00000, v72
	v_max_f32_e32 v73, 0xc2a00000, v73
	v_mul_f32_e32 v67, 0xbfb8aa3b, v67
	v_max_f32_e32 v68, 0xc2a00000, v68
	v_mul_f32_e32 v72, 0xbfb8aa3b, v72
	v_mul_f32_e32 v73, 0xbfb8aa3b, v73
	v_exp_f32_e32 v67, v67
	v_mul_f32_e32 v68, 0xbfb8aa3b, v68
	v_exp_f32_e32 v72, v72
	v_exp_f32_e32 v73, v73
	v_exp_f32_e32 v68, v68
	v_mul_f32_e32 v58, v58, v83
	v_rcp_f32_e32 v66, v66
	v_add_f32_e32 v67, 1.0, v67
	v_max_f32_e32 v58, 0xc2a00000, v58
	v_add_f32_e32 v78, 1.0, v80
	v_add_f32_e32 v79, 1.0, v81
	v_add_f32_e32 v72, 1.0, v72
	v_add_f32_e32 v73, 1.0, v73
	v_rcp_f32_e32 v67, v67
	v_add_f32_e32 v68, 1.0, v68
	v_mul_f32_e32 v58, 0xbfb8aa3b, v58
	v_rcp_f32_e32 v78, v78
	v_rcp_f32_e32 v79, v79
	v_rcp_f32_e32 v72, v72
	v_rcp_f32_e32 v73, v73
	v_rcp_f32_e32 v68, v68
	v_exp_f32_e32 v58, v58
	v_fma_f32 v66, v120, v66, v125
	v_log_f32_e32 v69, v66
	v_fma_f32 v66, v118, v67, v126
	v_mul_f32_e32 v59, v59, v83
	v_fma_f32 v74, v153, v78, v128
	v_fma_f32 v75, v168, v79, v129
	v_fma_f32 v72, v121, v72, v130
	v_fma_f32 v73, v122, v73, v131
	v_log_f32_e32 v77, v66
	v_fma_f32 v66, v119, v68, v127
	v_add_f32_e32 v58, 1.0, v58
	v_max_f32_e32 v59, 0xc2a00000, v59
	v_log_f32_e32 v74, v74
	v_log_f32_e32 v75, v75
	v_log_f32_e32 v72, v72
	v_log_f32_e32 v73, v73
	v_log_f32_e32 v78, v66
	v_rcp_f32_e32 v58, v58
	v_mul_f32_e32 v59, 0xbfb8aa3b, v59
	v_exp_f32_e32 v59, v59
	v_mul_f32_e32 v64, v64, v83
	v_mul_f32_e32 v65, v65, v83
	v_max_f32_e32 v64, 0xc2a00000, v64
	v_max_f32_e32 v65, 0xc2a00000, v65
	v_cvt_pk_f16_f32 v66, v74, v75
	v_cvt_pk_f16_f32 v67, v72, v73
	v_cvt_pk_f16_f32 v68, v76, v69
	v_mul_f32_e32 v62, v62, v83
	v_mul_f32_e32 v63, v63, v83
	v_cvt_pk_f16_f32 v69, v77, v78
	v_mul_f32_e32 v64, 0xbfb8aa3b, v64
	v_mul_f32_e32 v65, 0xbfb8aa3b, v65
	v_fma_f32 v58, v171, v58, v132
	v_max_f32_e32 v62, 0xc2a00000, v62
	v_max_f32_e32 v63, 0xc2a00000, v63
	s_waitcnt lgkmcnt(5)
	v_subrev_u32_e32 v248, s82, v248
	global_store_dwordx4 v248, v[244:247], s[82:83] offset:64
	ds_bpermute_b32 v238, v250, v66
	ds_bpermute_b32 v239, v250, v67
	ds_bpermute_b32 v240, v250, v68
	ds_bpermute_b32 v241, v250, v69
	ds_bpermute_b32 v242, v250, v70
	v_exp_f32_e32 v64, v64
	v_exp_f32_e32 v65, v65
	v_log_f32_e32 v66, v58
	v_add_f32_e32 v58, 1.0, v59
	v_mul_f32_e32 v59, v60, v83
	v_mul_f32_e32 v62, 0xbfb8aa3b, v62
	v_mul_f32_e32 v63, 0xbfb8aa3b, v63
	v_max_f32_e32 v59, 0xc2a00000, v59
	v_mul_f32_e32 v60, v61, v83
	v_exp_f32_e32 v62, v62
	v_exp_f32_e32 v63, v63
	v_mul_f32_e32 v59, 0xbfb8aa3b, v59
	v_max_f32_e32 v60, 0xc2a00000, v60
	v_exp_f32_e32 v59, v59
	v_mul_f32_e32 v60, 0xbfb8aa3b, v60
	v_add_f32_e32 v64, 1.0, v64
	v_add_f32_e32 v65, 1.0, v65
	v_exp_f32_e32 v60, v60
	v_rcp_f32_e32 v64, v64
	v_rcp_f32_e32 v65, v65
	v_add_f32_e32 v62, 1.0, v62
	v_add_f32_e32 v63, 1.0, v63
	v_mul_f32_e32 v50, v50, v83
	v_rcp_f32_e32 v62, v62
	v_rcp_f32_e32 v63, v63
	v_rcp_f32_e32 v58, v58
	v_add_f32_e32 v59, 1.0, v59
	v_max_f32_e32 v50, 0xc2a00000, v50
	v_rcp_f32_e32 v59, v59
	v_add_f32_e32 v60, 1.0, v60
	v_mul_f32_e32 v50, 0xbfb8aa3b, v50
	v_fma_f32 v64, v178, v64, v138
	v_fma_f32 v65, v177, v65, v139
	v_rcp_f32_e32 v60, v60
	v_exp_f32_e32 v50, v50
	v_log_f32_e32 v64, v64
	v_log_f32_e32 v65, v65
	v_fma_f32 v62, v180, v62, v136
	v_fma_f32 v63, v179, v63, v137
	v_fma_f32 v58, v170, v58, v133
	v_mul_f32_e32 v54, v54, v83
	v_log_f32_e32 v62, v62
	v_log_f32_e32 v63, v63
	v_log_f32_e32 v61, v58
	v_fma_f32 v58, v169, v59, v134
	v_max_f32_e32 v54, 0xc2a00000, v54
	v_mul_f32_e32 v51, v51, v83
	v_log_f32_e32 v67, v58
	v_fma_f32 v58, v155, v60, v135
	v_mul_f32_e32 v54, 0xbfb8aa3b, v54
	v_add_f32_e32 v50, 1.0, v50
	v_max_f32_e32 v51, 0xc2a00000, v51
	v_log_f32_e32 v68, v58
	v_cvt_pk_f16_f32 v59, v64, v65
	v_exp_f32_e32 v64, v54
	v_mul_f32_e32 v54, v55, v83
	v_rcp_f32_e32 v50, v50
	v_mul_f32_e32 v51, 0xbfb8aa3b, v51
	v_max_f32_e32 v54, 0xc2a00000, v54
	v_exp_f32_e32 v51, v51
	v_cvt_pk_f16_f32 v58, v62, v63
	v_lshl_add_u64 v[62:63], v[166:167], 0, s[14:15]
	v_mul_f32_e32 v54, 0xbfb8aa3b, v54
	s_mov_b32 s14, 0x80000
	v_exp_f32_e32 v65, v54
	v_add_co_u32_e32 v54, vcc, s14, v166
	v_cvt_pk_f16_f32 v60, v66, v61
	v_cvt_pk_f16_f32 v61, v67, v68
	v_addc_co_u32_e32 v55, vcc, 0, v167, vcc
	v_fma_f32 v50, v123, v50, v124
	s_waitcnt lgkmcnt(5)
	v_subrev_u32_e32 v236, s82, v236
	global_store_dwordx4 v236, v[232:235], s[82:83]
	ds_bpermute_b32 v244, v250, v58
	ds_bpermute_b32 v245, v250, v59
	ds_bpermute_b32 v246, v250, v60
	ds_bpermute_b32 v247, v250, v61
	ds_bpermute_b32 v248, v250, v54
	v_mul_f32_e32 v56, v56, v83
	v_mul_f32_e32 v57, v57, v83
	v_log_f32_e32 v58, v50
	v_add_f32_e32 v50, 1.0, v51
	v_mul_f32_e32 v51, v52, v83
	v_max_f32_e32 v51, 0xc2a00000, v51
	v_mul_f32_e32 v51, 0xbfb8aa3b, v51
	v_exp_f32_e32 v51, v51
	v_rcp_f32_e32 v50, v50
	v_mul_f32_e32 v52, v53, v83
	v_max_f32_e32 v56, 0xc2a00000, v56
	v_add_f32_e32 v51, 1.0, v51
	v_rcp_f32_e32 v51, v51
	v_fma_f32 v50, v120, v50, v125
	v_log_f32_e32 v59, v50
	v_max_f32_e32 v57, 0xc2a00000, v57
	v_fma_f32 v50, v118, v51, v126
	v_log_f32_e32 v60, v50
	ds_read2_b32 v[50:51], v176 offset0:144 offset1:160
	v_max_f32_e32 v52, 0xc2a00000, v52
	v_mul_f32_e32 v56, 0xbfb8aa3b, v56
	v_mul_f32_e32 v57, 0xbfb8aa3b, v57
	v_mul_f32_e32 v52, 0xbfb8aa3b, v52
	v_exp_f32_e32 v56, v56
	v_exp_f32_e32 v57, v57
	v_exp_f32_e32 v52, v52
	s_waitcnt lgkmcnt(0)
	v_mul_f32_e32 v42, v42, v50
	v_max_f32_e32 v42, 0xc2a00000, v42
	v_add_f32_e32 v64, 1.0, v64
	v_add_f32_e32 v65, 1.0, v65
	v_add_f32_e32 v56, 1.0, v56
	v_add_f32_e32 v57, 1.0, v57
	v_add_f32_e32 v52, 1.0, v52
	v_mul_f32_e32 v42, 0xbfb8aa3b, v42
	v_rcp_f32_e32 v64, v64
	v_rcp_f32_e32 v65, v65
	v_rcp_f32_e32 v56, v56
	v_rcp_f32_e32 v57, v57
	v_rcp_f32_e32 v52, v52
	v_exp_f32_e32 v42, v42
	v_mul_f32_e32 v43, v43, v50
	v_fma_f32 v54, v153, v64, v128
	v_fma_f32 v55, v168, v65, v129
	v_fma_f32 v56, v121, v56, v130
	v_fma_f32 v57, v122, v57, v131
	v_fma_f32 v52, v119, v52, v127
	v_add_f32_e32 v42, 1.0, v42
	v_max_f32_e32 v43, 0xc2a00000, v43
	v_log_f32_e32 v54, v54
	v_log_f32_e32 v55, v55
	v_log_f32_e32 v56, v56
	v_log_f32_e32 v57, v57
	v_log_f32_e32 v61, v52
	v_rcp_f32_e32 v42, v42
	v_mul_f32_e32 v43, 0xbfb8aa3b, v43
	v_exp_f32_e32 v43, v43
	v_mul_f32_e32 v48, v48, v50
	v_mul_f32_e32 v49, v49, v50
	v_max_f32_e32 v48, 0xc2a00000, v48
	v_max_f32_e32 v49, 0xc2a00000, v49
	v_cvt_pk_f16_f32 v52, v54, v55
	v_cvt_pk_f16_f32 v53, v56, v57
	v_cvt_pk_f16_f32 v54, v58, v59
	v_mul_f32_e32 v46, v46, v50
	v_mul_f32_e32 v47, v47, v50
	v_cvt_pk_f16_f32 v55, v60, v61
	v_mul_f32_e32 v48, 0xbfb8aa3b, v48
	v_mul_f32_e32 v49, 0xbfb8aa3b, v49
	v_fma_f32 v42, v171, v42, v132
	v_max_f32_e32 v46, 0xc2a00000, v46
	v_max_f32_e32 v47, 0xc2a00000, v47
	s_waitcnt lgkmcnt(6)
	v_subrev_u32_e32 v242, s82, v242
	global_store_dwordx4 v242, v[238:241], s[82:83] offset:64
	ds_bpermute_b32 v232, v250, v52
	ds_bpermute_b32 v233, v250, v53
	ds_bpermute_b32 v234, v250, v54
	ds_bpermute_b32 v235, v250, v55
	ds_bpermute_b32 v236, v250, v62
	v_exp_f32_e32 v48, v48
	v_exp_f32_e32 v49, v49
	v_log_f32_e32 v52, v42
	v_add_f32_e32 v42, 1.0, v43
	v_mul_f32_e32 v43, v44, v50
	v_mul_f32_e32 v46, 0xbfb8aa3b, v46
	v_mul_f32_e32 v47, 0xbfb8aa3b, v47
	v_max_f32_e32 v43, 0xc2a00000, v43
	v_mul_f32_e32 v44, v45, v50
	v_exp_f32_e32 v46, v46
	v_exp_f32_e32 v47, v47
	v_mul_f32_e32 v43, 0xbfb8aa3b, v43
	v_max_f32_e32 v44, 0xc2a00000, v44
	v_exp_f32_e32 v43, v43
	v_mul_f32_e32 v44, 0xbfb8aa3b, v44
	v_add_f32_e32 v48, 1.0, v48
	v_add_f32_e32 v49, 1.0, v49
	v_exp_f32_e32 v44, v44
	v_rcp_f32_e32 v48, v48
	v_rcp_f32_e32 v49, v49
	v_add_f32_e32 v46, 1.0, v46
	v_add_f32_e32 v47, 1.0, v47
	v_mul_f32_e32 v34, v34, v50
	v_rcp_f32_e32 v46, v46
	v_rcp_f32_e32 v47, v47
	v_rcp_f32_e32 v42, v42
	v_add_f32_e32 v43, 1.0, v43
	v_max_f32_e32 v34, 0xc2a00000, v34
	v_rcp_f32_e32 v43, v43
	v_add_f32_e32 v44, 1.0, v44
	v_mul_f32_e32 v34, 0xbfb8aa3b, v34
	v_fma_f32 v48, v178, v48, v138
	v_fma_f32 v49, v177, v49, v139
	v_rcp_f32_e32 v44, v44
	v_exp_f32_e32 v34, v34
	v_log_f32_e32 v48, v48
	v_log_f32_e32 v49, v49
	v_fma_f32 v46, v180, v46, v136
	v_fma_f32 v47, v179, v47, v137
	v_fma_f32 v42, v170, v42, v133
	v_mul_f32_e32 v38, v38, v50
	v_log_f32_e32 v46, v46
	v_log_f32_e32 v47, v47
	v_log_f32_e32 v45, v42
	v_fma_f32 v42, v169, v43, v134
	v_max_f32_e32 v38, 0xc2a00000, v38
	v_mul_f32_e32 v35, v35, v50
	v_log_f32_e32 v53, v42
	v_fma_f32 v42, v155, v44, v135
	v_mul_f32_e32 v38, 0xbfb8aa3b, v38
	v_add_f32_e32 v34, 1.0, v34
	v_max_f32_e32 v35, 0xc2a00000, v35
	v_log_f32_e32 v54, v42
	v_cvt_pk_f16_f32 v43, v48, v49
	v_exp_f32_e32 v48, v38
	v_mul_f32_e32 v38, v39, v50
	v_rcp_f32_e32 v34, v34
	v_mul_f32_e32 v35, 0xbfb8aa3b, v35
	s_mov_b64 s[14:15], 0x90000
	v_max_f32_e32 v38, 0xc2a00000, v38
	v_exp_f32_e32 v35, v35
	v_cvt_pk_f16_f32 v42, v46, v47
	v_lshl_add_u64 v[46:47], v[166:167], 0, s[14:15]
	v_mul_f32_e32 v38, 0xbfb8aa3b, v38
	s_mov_b32 s14, 0x90000
	v_exp_f32_e32 v49, v38
	v_add_co_u32_e32 v38, vcc, s14, v166
	v_cvt_pk_f16_f32 v44, v52, v45
	v_cvt_pk_f16_f32 v45, v53, v54
	v_addc_co_u32_e32 v39, vcc, 0, v167, vcc
	v_fma_f32 v34, v123, v34, v124
	s_waitcnt lgkmcnt(6)
	v_subrev_u32_e32 v248, s82, v248
	global_store_dwordx4 v248, v[244:247], s[82:83]
	ds_bpermute_b32 v238, v250, v42
	ds_bpermute_b32 v239, v250, v43
	ds_bpermute_b32 v240, v250, v44
	ds_bpermute_b32 v241, v250, v45
	ds_bpermute_b32 v242, v250, v38
	v_mul_f32_e32 v40, v40, v50
	v_mul_f32_e32 v41, v41, v50
	v_log_f32_e32 v42, v34
	v_add_f32_e32 v34, 1.0, v35
	v_mul_f32_e32 v35, v36, v50
	v_max_f32_e32 v35, 0xc2a00000, v35
	v_mul_f32_e32 v36, v37, v50
	v_max_f32_e32 v40, 0xc2a00000, v40
	v_max_f32_e32 v41, 0xc2a00000, v41
	v_mul_f32_e32 v35, 0xbfb8aa3b, v35
	v_max_f32_e32 v36, 0xc2a00000, v36
	v_mul_f32_e32 v40, 0xbfb8aa3b, v40
	v_mul_f32_e32 v41, 0xbfb8aa3b, v41
	v_exp_f32_e32 v35, v35
	v_mul_f32_e32 v36, 0xbfb8aa3b, v36
	v_exp_f32_e32 v40, v40
	v_exp_f32_e32 v41, v41
	v_exp_f32_e32 v36, v36
	v_mul_f32_e32 v26, v26, v51
	v_rcp_f32_e32 v34, v34
	v_add_f32_e32 v35, 1.0, v35
	v_max_f32_e32 v26, 0xc2a00000, v26
	v_add_f32_e32 v48, 1.0, v48
	v_add_f32_e32 v49, 1.0, v49
	v_add_f32_e32 v40, 1.0, v40
	v_add_f32_e32 v41, 1.0, v41
	v_rcp_f32_e32 v35, v35
	v_add_f32_e32 v36, 1.0, v36
	v_mul_f32_e32 v26, 0xbfb8aa3b, v26
	v_rcp_f32_e32 v48, v48
	v_rcp_f32_e32 v49, v49
	v_rcp_f32_e32 v40, v40
	v_rcp_f32_e32 v41, v41
	v_rcp_f32_e32 v36, v36
	v_exp_f32_e32 v26, v26
	v_fma_f32 v34, v120, v34, v125
	v_log_f32_e32 v37, v34
	v_fma_f32 v34, v118, v35, v126
	v_mul_f32_e32 v27, v27, v51
	v_fma_f32 v38, v153, v48, v128
	v_fma_f32 v39, v168, v49, v129
	v_fma_f32 v40, v121, v40, v130
	v_fma_f32 v41, v122, v41, v131
	v_log_f32_e32 v43, v34
	v_fma_f32 v34, v119, v36, v127
	v_add_f32_e32 v26, 1.0, v26
	v_max_f32_e32 v27, 0xc2a00000, v27
	v_log_f32_e32 v38, v38
	v_log_f32_e32 v39, v39
	v_log_f32_e32 v40, v40
	v_log_f32_e32 v41, v41
	v_log_f32_e32 v44, v34
	v_rcp_f32_e32 v26, v26
	v_mul_f32_e32 v27, 0xbfb8aa3b, v27
	v_exp_f32_e32 v27, v27
	v_mul_f32_e32 v32, v32, v51
	v_mul_f32_e32 v33, v33, v51
	v_max_f32_e32 v32, 0xc2a00000, v32
	v_max_f32_e32 v33, 0xc2a00000, v33
	v_cvt_pk_f16_f32 v34, v38, v39
	v_cvt_pk_f16_f32 v35, v40, v41
	v_cvt_pk_f16_f32 v36, v42, v37
	v_mul_f32_e32 v30, v30, v51
	v_mul_f32_e32 v31, v31, v51
	v_cvt_pk_f16_f32 v37, v43, v44
	v_mul_f32_e32 v32, 0xbfb8aa3b, v32
	v_mul_f32_e32 v33, 0xbfb8aa3b, v33
	v_fma_f32 v26, v171, v26, v132
	v_max_f32_e32 v30, 0xc2a00000, v30
	v_max_f32_e32 v31, 0xc2a00000, v31
	s_waitcnt lgkmcnt(5)
	v_subrev_u32_e32 v236, s82, v236
	global_store_dwordx4 v236, v[232:235], s[82:83] offset:64
	ds_bpermute_b32 v244, v250, v34
	ds_bpermute_b32 v245, v250, v35
	ds_bpermute_b32 v246, v250, v36
	ds_bpermute_b32 v247, v250, v37
	ds_bpermute_b32 v248, v250, v46
	v_exp_f32_e32 v32, v32
	v_exp_f32_e32 v33, v33
	v_log_f32_e32 v34, v26
	v_add_f32_e32 v26, 1.0, v27
	v_mul_f32_e32 v27, v28, v51
	v_mul_f32_e32 v30, 0xbfb8aa3b, v30
	v_mul_f32_e32 v31, 0xbfb8aa3b, v31
	v_max_f32_e32 v27, 0xc2a00000, v27
	v_mul_f32_e32 v28, v29, v51
	v_exp_f32_e32 v30, v30
	v_exp_f32_e32 v31, v31
	v_mul_f32_e32 v27, 0xbfb8aa3b, v27
	v_max_f32_e32 v28, 0xc2a00000, v28
	v_exp_f32_e32 v27, v27
	v_mul_f32_e32 v28, 0xbfb8aa3b, v28
	v_add_f32_e32 v32, 1.0, v32
	v_add_f32_e32 v33, 1.0, v33
	v_exp_f32_e32 v28, v28
	v_rcp_f32_e32 v32, v32
	v_rcp_f32_e32 v33, v33
	v_add_f32_e32 v30, 1.0, v30
	v_add_f32_e32 v31, 1.0, v31
	v_mul_f32_e32 v18, v18, v51
	v_rcp_f32_e32 v30, v30
	v_rcp_f32_e32 v31, v31
	v_rcp_f32_e32 v26, v26
	v_add_f32_e32 v27, 1.0, v27
	v_max_f32_e32 v18, 0xc2a00000, v18
	v_rcp_f32_e32 v27, v27
	v_add_f32_e32 v28, 1.0, v28
	v_mul_f32_e32 v18, 0xbfb8aa3b, v18
	v_fma_f32 v32, v178, v32, v138
	v_fma_f32 v33, v177, v33, v139
	v_rcp_f32_e32 v28, v28
	v_exp_f32_e32 v18, v18
	v_log_f32_e32 v32, v32
	v_log_f32_e32 v33, v33
	v_fma_f32 v30, v180, v30, v136
	v_fma_f32 v31, v179, v31, v137
	v_fma_f32 v26, v170, v26, v133
	v_mul_f32_e32 v22, v22, v51
	v_log_f32_e32 v30, v30
	v_log_f32_e32 v31, v31
	v_log_f32_e32 v29, v26
	v_fma_f32 v26, v169, v27, v134
	v_max_f32_e32 v22, 0xc2a00000, v22
	v_mul_f32_e32 v19, v19, v51
	v_log_f32_e32 v35, v26
	v_fma_f32 v26, v155, v28, v135
	v_mul_f32_e32 v22, 0xbfb8aa3b, v22
	v_add_f32_e32 v18, 1.0, v18
	v_max_f32_e32 v19, 0xc2a00000, v19
	v_log_f32_e32 v36, v26
	v_cvt_pk_f16_f32 v27, v32, v33
	v_exp_f32_e32 v32, v22
	v_mul_f32_e32 v22, v23, v51
	v_rcp_f32_e32 v18, v18
	v_mul_f32_e32 v19, 0xbfb8aa3b, v19
	s_mov_b64 s[14:15], 0xa0000
	v_max_f32_e32 v22, 0xc2a00000, v22
	v_exp_f32_e32 v19, v19
	v_cvt_pk_f16_f32 v26, v30, v31
	v_lshl_add_u64 v[30:31], v[166:167], 0, s[14:15]
	v_mul_f32_e32 v22, 0xbfb8aa3b, v22
	s_mov_b32 s14, 0xa0000
	v_exp_f32_e32 v33, v22
	v_add_co_u32_e32 v22, vcc, s14, v166
	v_cvt_pk_f16_f32 v28, v34, v29
	v_cvt_pk_f16_f32 v29, v35, v36
	v_addc_co_u32_e32 v23, vcc, 0, v167, vcc
	v_fma_f32 v18, v123, v18, v124
	s_waitcnt lgkmcnt(5)
	v_subrev_u32_e32 v242, s82, v242
	global_store_dwordx4 v242, v[238:241], s[82:83]
	ds_bpermute_b32 v232, v250, v26
	ds_bpermute_b32 v233, v250, v27
	ds_bpermute_b32 v234, v250, v28
	ds_bpermute_b32 v235, v250, v29
	ds_bpermute_b32 v236, v250, v22
	v_mul_f32_e32 v24, v24, v51
	v_mul_f32_e32 v25, v25, v51
	v_log_f32_e32 v26, v18
	v_add_f32_e32 v18, 1.0, v19
	v_mul_f32_e32 v19, v20, v51
	v_max_f32_e32 v19, 0xc2a00000, v19
	v_mul_f32_e32 v20, v21, v51
	ds_read_b32 v28, v176 offset:704
	v_max_f32_e32 v24, 0xc2a00000, v24
	v_max_f32_e32 v25, 0xc2a00000, v25
	v_mul_f32_e32 v19, 0xbfb8aa3b, v19
	v_max_f32_e32 v20, 0xc2a00000, v20
	v_mul_f32_e32 v24, 0xbfb8aa3b, v24
	v_mul_f32_e32 v25, 0xbfb8aa3b, v25
	v_exp_f32_e32 v19, v19
	v_mul_f32_e32 v20, 0xbfb8aa3b, v20
	v_exp_f32_e32 v24, v24
	v_exp_f32_e32 v25, v25
	v_exp_f32_e32 v20, v20
	s_waitcnt lgkmcnt(0)
	v_mul_f32_e32 v10, v10, v28
	v_rcp_f32_e32 v18, v18
	v_add_f32_e32 v19, 1.0, v19
	v_max_f32_e32 v10, 0xc2a00000, v10
	v_add_f32_e32 v32, 1.0, v32
	v_add_f32_e32 v33, 1.0, v33
	v_add_f32_e32 v24, 1.0, v24
	v_add_f32_e32 v25, 1.0, v25
	v_rcp_f32_e32 v19, v19
	v_add_f32_e32 v20, 1.0, v20
	v_mul_f32_e32 v10, 0xbfb8aa3b, v10
	v_rcp_f32_e32 v32, v32
	v_rcp_f32_e32 v33, v33
	v_rcp_f32_e32 v24, v24
	v_rcp_f32_e32 v25, v25
	v_rcp_f32_e32 v20, v20
	v_exp_f32_e32 v10, v10
	v_fma_f32 v18, v120, v18, v125
	v_log_f32_e32 v21, v18
	v_fma_f32 v18, v118, v19, v126
	v_mul_f32_e32 v11, v11, v28
	v_fma_f32 v22, v153, v32, v128
	v_fma_f32 v23, v168, v33, v129
	v_fma_f32 v24, v121, v24, v130
	v_fma_f32 v25, v122, v25, v131
	v_log_f32_e32 v27, v18
	v_fma_f32 v18, v119, v20, v127
	v_add_f32_e32 v10, 1.0, v10
	v_max_f32_e32 v11, 0xc2a00000, v11
	v_log_f32_e32 v22, v22
	v_log_f32_e32 v23, v23
	v_log_f32_e32 v24, v24
	v_log_f32_e32 v25, v25
	v_log_f32_e32 v29, v18
	v_rcp_f32_e32 v10, v10
	v_mul_f32_e32 v11, 0xbfb8aa3b, v11
	v_mul_f32_e32 v14, v14, v28
	v_mul_f32_e32 v15, v15, v28
	v_exp_f32_e32 v11, v11
	v_max_f32_e32 v14, 0xc2a00000, v14
	v_max_f32_e32 v15, 0xc2a00000, v15
	v_mul_f32_e32 v14, 0xbfb8aa3b, v14
	v_mul_f32_e32 v15, 0xbfb8aa3b, v15
	v_cvt_pk_f16_f32 v18, v22, v23
	v_cvt_pk_f16_f32 v19, v24, v25
	v_cvt_pk_f16_f32 v20, v26, v21
	v_exp_f32_e32 v14, v14
	v_exp_f32_e32 v15, v15
	v_cvt_pk_f16_f32 v21, v27, v29
	v_fma_f32 v10, v171, v10, v132
	s_waitcnt lgkmcnt(6)
	v_subrev_u32_e32 v248, s82, v248
	global_store_dwordx4 v248, v[244:247], s[82:83] offset:64
	ds_bpermute_b32 v238, v250, v18
	ds_bpermute_b32 v239, v250, v19
	ds_bpermute_b32 v240, v250, v20
	ds_bpermute_b32 v241, v250, v21
	ds_bpermute_b32 v242, v250, v30
	v_add_f32_e32 v14, 1.0, v14
	v_add_f32_e32 v15, 1.0, v15
	v_log_f32_e32 v18, v10
	v_add_f32_e32 v10, 1.0, v11
	v_mul_f32_e32 v11, v12, v28
	v_max_f32_e32 v11, 0xc2a00000, v11
	v_mul_f32_e32 v11, 0xbfb8aa3b, v11
	v_exp_f32_e32 v11, v11
	v_rcp_f32_e32 v14, v14
	v_rcp_f32_e32 v15, v15
	v_mul_f32_e32 v16, v16, v28
	v_mul_f32_e32 v17, v17, v28
	v_rcp_f32_e32 v10, v10
	v_mul_f32_e32 v12, v13, v28
	v_add_f32_e32 v11, 1.0, v11
	v_fma_f32 v14, v180, v14, v136
	v_fma_f32 v15, v179, v15, v137
	v_max_f32_e32 v16, 0xc2a00000, v16
	v_max_f32_e32 v17, 0xc2a00000, v17
	v_max_f32_e32 v12, 0xc2a00000, v12
	v_rcp_f32_e32 v11, v11
	v_log_f32_e32 v14, v14
	v_mul_f32_e32 v16, 0xbfb8aa3b, v16
	v_mul_f32_e32 v17, 0xbfb8aa3b, v17
	v_log_f32_e32 v15, v15
	v_mul_f32_e32 v12, 0xbfb8aa3b, v12
	v_exp_f32_e32 v16, v16
	v_exp_f32_e32 v17, v17
	v_exp_f32_e32 v12, v12
	v_mul_f32_e32 v6, v6, v28
	v_fma_f32 v10, v170, v10, v133
	v_max_f32_e32 v6, 0xc2a00000, v6
	v_log_f32_e32 v13, v10
	v_fma_f32 v10, v169, v11, v134
	v_mul_f32_e32 v6, 0xbfb8aa3b, v6
	v_log_f32_e32 v19, v10
	v_cvt_pk_f16_f32 v10, v14, v15
	v_exp_f32_e32 v14, v6
	v_mul_f32_e32 v6, v7, v28
	v_mul_f32_e32 v8, v8, v28
	v_mul_f32_e32 v9, v9, v28
	v_mul_f32_e32 v2, v2, v28
	v_mul_f32_e32 v3, v3, v28
	v_mul_f32_e32 v4, v4, v28
	v_mul_f32_e32 v5, v5, v28
	v_add_f32_e32 v16, 1.0, v16
	v_add_f32_e32 v17, 1.0, v17
	v_add_f32_e32 v12, 1.0, v12
	v_max_f32_e32 v6, 0xc2a00000, v6
	v_max_f32_e32 v8, 0xc2a00000, v8
	v_max_f32_e32 v9, 0xc2a00000, v9
	v_max_f32_e32 v2, 0xc2a00000, v2
	v_max_f32_e32 v3, 0xc2a00000, v3
	v_max_f32_e32 v4, 0xc2a00000, v4
	v_max_f32_e32 v5, 0xc2a00000, v5
	v_rcp_f32_e32 v16, v16
	v_rcp_f32_e32 v17, v17
	v_rcp_f32_e32 v12, v12
	v_mul_f32_e32 v6, 0xbfb8aa3b, v6
	v_mul_f32_e32 v8, 0xbfb8aa3b, v8
	v_mul_f32_e32 v9, 0xbfb8aa3b, v9
	v_mul_f32_e32 v2, 0xbfb8aa3b, v2
	v_mul_f32_e32 v3, 0xbfb8aa3b, v3
	v_mul_f32_e32 v4, 0xbfb8aa3b, v4
	v_mul_f32_e32 v5, 0xbfb8aa3b, v5
	v_exp_f32_e32 v15, v6
	v_exp_f32_e32 v8, v8
	v_exp_f32_e32 v9, v9
	v_exp_f32_e32 v2, v2
	v_exp_f32_e32 v3, v3
	v_exp_f32_e32 v4, v4
	v_exp_f32_e32 v5, v5
	v_fma_f32 v16, v178, v16, v138
	v_fmac_f32_e32 v139, v177, v17
	v_fmac_f32_e32 v135, v155, v12
	v_log_f32_e32 v16, v16
	v_log_f32_e32 v17, v139
	v_log_f32_e32 v20, v135
	v_add_f32_e32 v14, 1.0, v14
	v_add_f32_e32 v15, 1.0, v15
	v_add_f32_e32 v8, 1.0, v8
	v_add_f32_e32 v9, 1.0, v9
	v_add_f32_e32 v2, 1.0, v2
	v_add_f32_e32 v3, 1.0, v3
	v_add_f32_e32 v4, 1.0, v4
	v_add_f32_e32 v5, 1.0, v5
	s_mov_b64 s[14:15], 0xb0000
	v_rcp_f32_e32 v14, v14
	v_rcp_f32_e32 v15, v15
	v_rcp_f32_e32 v8, v8
	v_rcp_f32_e32 v9, v9
	v_rcp_f32_e32 v2, v2
	v_rcp_f32_e32 v3, v3
	v_rcp_f32_e32 v4, v4
	v_rcp_f32_e32 v5, v5
	v_lshl_add_u64 v[136:137], v[166:167], 0, s[14:15]
	s_mov_b32 s14, 0xb0000
	v_add_co_u32_e32 v6, vcc, s14, v166
	v_cvt_pk_f16_f32 v11, v16, v17
	v_cvt_pk_f16_f32 v12, v18, v13
	v_cvt_pk_f16_f32 v13, v19, v20
	v_addc_co_u32_e32 v7, vcc, 0, v167, vcc
	s_waitcnt lgkmcnt(6)
	v_subrev_u32_e32 v236, s82, v236
	global_store_dwordx4 v236, v[232:235], s[82:83]
	ds_bpermute_b32 v244, v250, v10
	ds_bpermute_b32 v245, v250, v11
	ds_bpermute_b32 v246, v250, v12
	ds_bpermute_b32 v247, v250, v13
	ds_bpermute_b32 v248, v250, v6
	v_fma_f32 v6, v153, v14, v128
	v_fma_f32 v7, v168, v15, v129
	v_fma_f32 v8, v121, v8, v130
	v_fmac_f32_e32 v131, v122, v9
	v_fma_f32 v2, v123, v2, v124
	v_fma_f32 v3, v120, v3, v125
	v_fma_f32 v4, v118, v4, v126
	v_fmac_f32_e32 v127, v119, v5
	v_log_f32_e32 v6, v6
	v_log_f32_e32 v7, v7
	v_log_f32_e32 v8, v8
	v_log_f32_e32 v9, v131
	v_log_f32_e32 v2, v2
	v_log_f32_e32 v3, v3
	v_log_f32_e32 v4, v4
	v_log_f32_e32 v5, v127
	v_cvt_pk_f16_f32 v196, v181, v182
	v_cvt_pk_f16_f32 v132, v6, v7
	v_cvt_pk_f16_f32 v133, v8, v9
	v_cvt_pk_f16_f32 v134, v2, v3
	v_cvt_pk_f16_f32 v135, v4, v5
	s_waitcnt lgkmcnt(5)
	v_subrev_u32_e32 v242, s82, v242
	global_store_dwordx4 v242, v[238:241], s[82:83] offset:64
	ds_bpermute_b32 v232, v250, v194
	ds_bpermute_b32 v233, v250, v195
	ds_bpermute_b32 v234, v250, v196
	ds_bpermute_b32 v235, v250, v197
	ds_bpermute_b32 v236, v250, v166
	s_andn2_b64 vcc, exec, s[38:39]
	s_mov_b64 s[28:29], -1
	s_waitcnt lgkmcnt(5)
	v_subrev_u32_e32 v248, s82, v248
	global_store_dwordx4 v248, v[244:247], s[82:83]
	ds_bpermute_b32 v238, v250, v132
	ds_bpermute_b32 v239, v250, v133
	ds_bpermute_b32 v240, v250, v134
	ds_bpermute_b32 v241, v250, v135
	ds_bpermute_b32 v242, v250, v136
	s_waitcnt lgkmcnt(5)
	v_subrev_u32_e32 v236, s82, v236
	global_store_dwordx4 v236, v[232:235], s[82:83] offset:64
	s_waitcnt lgkmcnt(0)
	v_subrev_u32_e32 v242, s82, v242
	global_store_dwordx4 v242, v[238:241], s[82:83] offset:64
	s_cbranch_vccnz .LBB0_338

.LBB0_506:
	v_mbcnt_lo_u32_b32 v250, -1, 0
	v_mbcnt_hi_u32_b32 v250, -1, v250
	v_lshrrev_b32_e32 v251, 2, v250
	v_and_b32_e32 v250, 3, v250
	v_lshl_add_u32 v250, v250, 4, v251
	v_lshlrev_b32_e32 v250, 2, v250
	s_lshl_b32 s14, s14, 10
	v_add_u32_e32 v176, s14, v174
	ds_read_b32 v154, v176
	s_lshl_b32 s15, s28, 8
	s_ashr_i32 s56, s28, 3
	s_and_b32 s14, s15, 0x700
	v_lshl_add_u32 v152, s40, 8, v1
	v_or_b32_e32 v177, s14, v173
	s_cmp_lg_u32 s56, 1
	s_mov_b64 s[40:41], -1
	s_cbranch_scc0 .LBB0_541
	s_cmp_lt_u32 s28, 8
	s_cselect_b64 s[54:55], -1, 0
	s_cmp_gt_u32 s28, 7
	s_waitcnt lgkmcnt(0)
	v_pk_mul_f32 v[134:135], v[130:131], v[154:155] op_sel_hi:[1,0]
	v_pk_mul_f32 v[166:167], v[128:129], v[154:155] op_sel_hi:[1,0]
	v_pk_mul_f32 v[138:139], v[126:127], v[154:155] op_sel_hi:[1,0]
	v_pk_mul_f32 v[168:169], v[124:125], v[154:155] op_sel_hi:[1,0]
	s_cbranch_scc1 .LBB0_509
	v_max_f32_e32 v114, v166, v166
	v_max_f32_e32 v132, 0xc2a00000, v114
	v_max_f32_e32 v114, v168, v168
	v_max_f32_e32 v136, 0xc2a00000, v114
	v_mul_f32_e32 v114, 0xbfb8aa3b, v132
	v_exp_f32_e32 v114, v114
	v_mul_f32_e32 v133, 0xbfb8aa3b, v136
	v_exp_f32_e32 v133, v133
	v_max_f32_e32 v137, v169, v169
	v_add_f32_e32 v114, 1.0, v114
	v_rcp_f32_e32 v158, v114
	v_add_f32_e32 v114, 1.0, v133
	v_max_f32_e32 v133, v167, v167
	v_max_f32_e32 v133, 0xc2a00000, v133
	v_max_f32_e32 v137, 0xc2a00000, v137
	v_mul_f32_e32 v153, 0xbfb8aa3b, v133
	v_exp_f32_e32 v153, v153
	v_mul_f32_e32 v155, 0xbfb8aa3b, v137
	v_exp_f32_e32 v155, v155
	v_max_f32_e32 v134, v134, v134
	v_max_f32_e32 v134, 0xc2a00000, v134
	v_max_f32_e32 v138, v138, v138
	v_rcp_f32_e32 v160, v114
	v_add_f32_e32 v114, 1.0, v153
	v_max_f32_e32 v138, 0xc2a00000, v138
	v_mul_f32_e32 v153, 0xbfb8aa3b, v134
	v_rcp_f32_e32 v159, v114
	v_add_f32_e32 v114, 1.0, v155
	v_exp_f32_e32 v153, v153
	v_mul_f32_e32 v155, 0xbfb8aa3b, v138
	v_exp_f32_e32 v155, v155
	v_max_f32_e32 v135, v135, v135
	v_max_f32_e32 v135, 0xc2a00000, v135
	v_max_f32_e32 v139, v139, v139
	v_rcp_f32_e32 v161, v114
	v_add_f32_e32 v114, 1.0, v153
	v_max_f32_e32 v139, 0xc2a00000, v139
	v_mul_f32_e32 v153, 0xbfb8aa3b, v135
	v_rcp_f32_e32 v168, v114
	v_add_f32_e32 v114, 1.0, v155
	v_exp_f32_e32 v153, v153
	v_mul_f32_e32 v155, 0xbfb8aa3b, v139
	v_exp_f32_e32 v155, v155
	v_rcp_f32_e32 v170, v114
	v_add_f32_e32 v114, 1.0, v153
	v_rcp_f32_e32 v169, v114
	v_add_f32_e32 v114, 1.0, v155
	v_rcp_f32_e32 v171, v114
	v_pk_mul_f32 v[166:167], v[132:133], v[158:159]
	v_pk_mul_f32 v[134:135], v[134:135], v[168:169]
	v_pk_mul_f32 v[168:169], v[136:137], v[160:161]
	v_pk_mul_f32 v[138:139], v[138:139], v[170:171]
.LBB0_509:
	s_ashr_i32 s57, s56, 31
	s_lshl_b64 s[14:15], s[56:57], 25
	s_add_u32 s14, s24, s14
	s_addc_u32 s15, s37, s15
	v_lshlrev_b32_e32 v114, 1, v177
	v_ashrrev_i32_e32 v153, 31, v152
	v_lshl_add_u64 v[132:133], s[14:15], 0, v[114:115]
	v_lshlrev_b64 v[136:137], 12, v[152:153]
	v_mov_b32_e32 v155, v154
	v_lshl_add_u64 v[136:137], v[132:133], 0, v[136:137]
	v_cvt_pk_bf16_f32 v166, v166, v167
	v_cvt_pk_bf16_f32 v167, v134, v135
	v_cvt_pk_bf16_f32 v168, v168, v169
	v_cvt_pk_bf16_f32 v169, v138, v139
	v_mov_b32_e32 v158, v154
	v_mov_b32_e32 v159, v154
	v_cndmask_b32_e64 v114, 0, 1, s[54:55]
	ds_bpermute_b32 v232, v250, v166
	ds_bpermute_b32 v233, v250, v167
	ds_bpermute_b32 v234, v250, v168
	ds_bpermute_b32 v235, v250, v169
	ds_bpermute_b32 v236, v250, v136
	v_pk_mul_f32 v[138:139], v[122:123], v[158:159]
	v_pk_mul_f32 v[134:135], v[120:121], v[154:155]
	v_pk_mul_f32 v[166:167], v[118:119], v[158:159]
	v_cmp_ne_u32_e64 s[40:41], 1, v114
	s_andn2_b64 vcc, exec, s[54:55]
	v_pk_mul_f32 v[168:169], v[116:117], v[154:155]
	s_waitcnt lgkmcnt(0)
	v_subrev_u32_e32 v236, s82, v236
	global_store_dwordx4 v236, v[232:235], s[82:83]
	s_cbranch_vccnz .LBB0_511
	v_max_f32_e32 v114, v134, v134
	v_max_f32_e32 v134, 0xc2a00000, v114
	v_max_f32_e32 v114, v168, v168
	v_max_f32_e32 v158, 0xc2a00000, v114
	v_mul_f32_e32 v114, 0xbfb8aa3b, v134
	v_exp_f32_e32 v114, v114
	v_mul_f32_e32 v155, 0xbfb8aa3b, v158
	v_exp_f32_e32 v155, v155
	v_max_f32_e32 v135, v135, v135
	v_add_f32_e32 v114, 1.0, v114
	v_rcp_f32_e32 v160, v114
	v_add_f32_e32 v114, 1.0, v155
	v_max_f32_e32 v135, 0xc2a00000, v135
	v_max_f32_e32 v155, v169, v169
	v_max_f32_e32 v159, 0xc2a00000, v155
	v_mul_f32_e32 v155, 0xbfb8aa3b, v135
	v_exp_f32_e32 v155, v155
	v_mul_f32_e32 v161, 0xbfb8aa3b, v159
	v_exp_f32_e32 v169, v161
	v_max_f32_e32 v138, v138, v138
	v_rcp_f32_e32 v168, v114
	v_add_f32_e32 v114, 1.0, v155
	v_max_f32_e32 v138, 0xc2a00000, v138
	v_max_f32_e32 v155, v166, v166
	v_max_f32_e32 v166, 0xc2a00000, v155
	v_mul_f32_e32 v155, 0xbfb8aa3b, v138
	v_exp_f32_e32 v155, v155
	v_rcp_f32_e32 v161, v114
	v_add_f32_e32 v114, 1.0, v169
	v_mul_f32_e32 v169, 0xbfb8aa3b, v166
	v_exp_f32_e32 v171, v169
	v_max_f32_e32 v139, v139, v139
	v_rcp_f32_e32 v169, v114
	v_add_f32_e32 v114, 1.0, v155
	v_max_f32_e32 v139, 0xc2a00000, v139
	v_max_f32_e32 v155, v167, v167
	v_max_f32_e32 v167, 0xc2a00000, v155
	v_mul_f32_e32 v155, 0xbfb8aa3b, v139
	v_rcp_f32_e32 v170, v114
	v_add_f32_e32 v114, 1.0, v171
	v_exp_f32_e32 v155, v155
	v_mul_f32_e32 v171, 0xbfb8aa3b, v167
	v_exp_f32_e32 v179, v171
	v_rcp_f32_e32 v178, v114
	v_add_f32_e32 v114, 1.0, v155
	v_rcp_f32_e32 v171, v114
	v_add_f32_e32 v114, 1.0, v179
	v_rcp_f32_e32 v179, v114
	v_pk_mul_f32 v[134:135], v[134:135], v[160:161]
	v_pk_mul_f32 v[138:139], v[138:139], v[170:171]
	v_pk_mul_f32 v[168:169], v[158:159], v[168:169]
	v_pk_mul_f32 v[166:167], v[166:167], v[178:179]

.LBB0_541:
	s_and_b64 vcc, exec, s[40:41]
	s_cbranch_vccz .LBB0_540
	v_lshlrev_b32_e32 v155, 2, v177
	global_load_dwordx4 v[136:139], v155, s[42:43]
	global_load_dwordx4 v[132:135], v155, s[42:43] offset:16
	s_waitcnt lgkmcnt(0)
	v_mul_f32_e32 v160, v128, v154
	v_mul_f32_e32 v161, v129, v154
	v_mul_f32_e32 v166, v130, v154
	v_mul_f32_e32 v167, v131, v154
	v_mul_f32_e32 v168, v124, v154
	v_mul_f32_e32 v169, v125, v154
	v_mul_f32_e32 v170, v126, v154
	v_mul_f32_e32 v171, v127, v154
	global_load_dwordx4 v[124:127], v155, s[42:43] offset:144
	global_load_dwordx4 v[128:131], v155, s[42:43] offset:128
	v_ashrrev_i32_e32 v153, 31, v152
	v_lshlrev_b64 v[158:159], 12, v[152:153]
	v_max_f32_e32 v153, 0xc2a00000, v160
	v_max_f32_e32 v155, 0xc2a00000, v161
	v_max_f32_e32 v160, 0xc2a00000, v166
	v_max_f32_e32 v161, 0xc2a00000, v167
	v_max_f32_e32 v166, 0xc2a00000, v168
	v_max_f32_e32 v167, 0xc2a00000, v169
	v_max_f32_e32 v168, 0xc2a00000, v170
	v_max_f32_e32 v169, 0xc2a00000, v171
	v_mul_f32_e32 v153, 0xbfb8aa3b, v153
	v_mul_f32_e32 v155, 0xbfb8aa3b, v155
	v_mul_f32_e32 v168, 0xbfb8aa3b, v168
	v_mul_f32_e32 v169, 0xbfb8aa3b, v169
	v_exp_f32_e32 v153, v153
	v_exp_f32_e32 v155, v155
	v_mul_f32_e32 v160, 0xbfb8aa3b, v160
	v_mul_f32_e32 v161, 0xbfb8aa3b, v161
	v_exp_f32_e32 v168, v168
	v_exp_f32_e32 v169, v169
	v_exp_f32_e32 v160, v160
	v_exp_f32_e32 v161, v161
	v_mul_f32_e32 v120, v120, v154
	v_max_f32_e32 v120, 0xc2a00000, v120
	v_add_f32_e32 v153, 1.0, v153
	v_add_f32_e32 v155, 1.0, v155
	v_mul_f32_e32 v121, v121, v154
	v_lshlrev_b32_e32 v114, 1, v177
	v_mul_f32_e32 v166, 0xbfb8aa3b, v166
	v_mul_f32_e32 v167, 0xbfb8aa3b, v167
	v_lshl_add_u64 v[158:159], s[26:27], 0, v[158:159]
	v_add_f32_e32 v168, 1.0, v168
	v_add_f32_e32 v169, 1.0, v169
	v_rcp_f32_e32 v153, v153
	v_rcp_f32_e32 v181, v155
	v_mul_f32_e32 v120, 0xbfb8aa3b, v120
	v_max_f32_e32 v121, 0xc2a00000, v121
	v_exp_f32_e32 v170, v166
	v_exp_f32_e32 v171, v167
	v_lshl_add_u64 v[166:167], v[158:159], 0, v[114:115]
	v_add_f32_e32 v158, 1.0, v160
	v_add_f32_e32 v159, 1.0, v161
	v_rcp_f32_e32 v168, v168
	v_rcp_f32_e32 v182, v169
	v_exp_f32_e32 v120, v120
	v_mul_f32_e32 v121, 0xbfb8aa3b, v121
	v_rcp_f32_e32 v158, v158
	v_rcp_f32_e32 v159, v159
	v_exp_f32_e32 v121, v121
	v_add_f32_e32 v120, 1.0, v120
	v_rcp_f32_e32 v120, v120
	v_mul_f32_e32 v116, v116, v154
	v_add_f32_e32 v121, 1.0, v121
	v_rcp_f32_e32 v121, v121
	v_add_f32_e32 v160, 1.0, v170
	v_add_f32_e32 v161, 1.0, v171
	v_max_f32_e32 v116, 0xc2a00000, v116
	v_mul_f32_e32 v117, v117, v154
	v_rcp_f32_e32 v160, v160
	v_rcp_f32_e32 v161, v161
	v_mul_f32_e32 v116, 0xbfb8aa3b, v116
	v_max_f32_e32 v117, 0xc2a00000, v117
	v_exp_f32_e32 v116, v116
	v_mul_f32_e32 v117, 0xbfb8aa3b, v117
	v_exp_f32_e32 v117, v117
	s_mov_b64 s[14:15], 0x80000
	v_add_f32_e32 v116, 1.0, v116
	v_rcp_f32_e32 v116, v116
	v_add_f32_e32 v117, 1.0, v117
	s_waitcnt vmcnt(0)
	v_sub_f32_e32 v180, 1.0, v136
	v_sub_f32_e32 v179, 1.0, v137
	v_sub_f32_e32 v169, 1.0, v134
	v_sub_f32_e32 v155, 1.0, v135
	v_fma_f32 v153, v180, v153, v136
	v_fma_f32 v181, v179, v181, v137
	v_sub_f32_e32 v178, 1.0, v138
	v_sub_f32_e32 v177, 1.0, v139
	v_fma_f32 v168, v169, v168, v134
	v_fma_f32 v182, v155, v182, v135
	v_log_f32_e32 v153, v153
	v_log_f32_e32 v181, v181
	v_fma_f32 v158, v178, v158, v138
	v_fma_f32 v159, v177, v159, v139
	v_log_f32_e32 v168, v168
	v_log_f32_e32 v182, v182
	v_log_f32_e32 v158, v158
	v_log_f32_e32 v159, v159
	v_cvt_pk_f16_f32 v194, v153, v181
	v_sub_f32_e32 v153, 1.0, v128
	v_cvt_pk_f16_f32 v197, v168, v182
	v_fma_f32 v120, v153, v120, v128
	v_sub_f32_e32 v168, 1.0, v129
	v_cvt_pk_f16_f32 v195, v158, v159
	v_log_f32_e32 v158, v120
	v_fma_f32 v120, v168, v121, v129
	v_log_f32_e32 v159, v120
	v_mul_f32_e32 v120, v122, v154
	v_max_f32_e32 v120, 0xc2a00000, v120
	v_mul_f32_e32 v121, v123, v154
	v_mul_f32_e32 v120, 0xbfb8aa3b, v120
	v_max_f32_e32 v121, 0xc2a00000, v121
	v_exp_f32_e32 v120, v120
	v_mul_f32_e32 v121, 0xbfb8aa3b, v121
	v_exp_f32_e32 v122, v121
	v_sub_f32_e32 v171, 1.0, v132
	v_sub_f32_e32 v170, 1.0, v133
	v_add_f32_e32 v120, 1.0, v120
	v_fma_f32 v160, v171, v160, v132
	v_fma_f32 v161, v170, v161, v133
	v_rcp_f32_e32 v120, v120
	v_add_f32_e32 v122, 1.0, v122
	v_log_f32_e32 v160, v160
	v_log_f32_e32 v161, v161
	v_rcp_f32_e32 v123, v122
	v_sub_f32_e32 v121, 1.0, v130
	v_rcp_f32_e32 v117, v117
	v_fma_f32 v120, v121, v120, v130
	v_sub_f32_e32 v122, 1.0, v131
	v_cvt_pk_f16_f32 v196, v160, v161
	v_log_f32_e32 v160, v120
	v_fma_f32 v120, v122, v123, v131
	v_sub_f32_e32 v123, 1.0, v124
	v_log_f32_e32 v161, v120
	v_fma_f32 v116, v123, v116, v124
	v_sub_f32_e32 v120, 1.0, v125
	v_log_f32_e32 v181, v116
	v_fma_f32 v116, v120, v117, v125
	v_log_f32_e32 v182, v116
	v_mul_f32_e32 v116, v118, v154
	v_max_f32_e32 v116, 0xc2a00000, v116
	v_mul_f32_e32 v117, v119, v154
	v_mul_f32_e32 v116, 0xbfb8aa3b, v116
	v_max_f32_e32 v117, 0xc2a00000, v117
	v_exp_f32_e32 v116, v116
	v_mul_f32_e32 v117, 0xbfb8aa3b, v117
	v_exp_f32_e32 v117, v117
	v_sub_f32_e32 v118, 1.0, v126
	v_add_f32_e32 v116, 1.0, v116
	v_rcp_f32_e32 v116, v116
	v_add_f32_e32 v117, 1.0, v117
	v_rcp_f32_e32 v117, v117
	v_sub_f32_e32 v119, 1.0, v127
	v_fma_f32 v116, v118, v116, v126
	v_log_f32_e32 v154, v116
	v_fma_f32 v116, v119, v117, v127
	v_log_f32_e32 v183, v116
	ds_read2_b32 v[116:117], v176 offset0:16 offset1:32
	ds_bpermute_b32 v238, v250, v194
	ds_bpermute_b32 v239, v250, v195
	ds_bpermute_b32 v240, v250, v196
	ds_bpermute_b32 v241, v250, v197
	ds_bpermute_b32 v242, v250, v166
	s_waitcnt lgkmcnt(0)
	v_mul_f32_e32 v106, v106, v116
	v_max_f32_e32 v106, 0xc2a00000, v106
	v_mul_f32_e32 v106, 0xbfb8aa3b, v106
	v_exp_f32_e32 v106, v106
	v_mul_f32_e32 v110, v110, v116
	v_max_f32_e32 v110, 0xc2a00000, v110
	v_mul_f32_e32 v111, v111, v116
	v_mul_f32_e32 v110, 0xbfb8aa3b, v110
	v_max_f32_e32 v111, 0xc2a00000, v111
	v_mul_f32_e32 v107, v107, v116
	v_exp_f32_e32 v110, v110
	v_mul_f32_e32 v111, 0xbfb8aa3b, v111
	v_add_f32_e32 v106, 1.0, v106
	v_max_f32_e32 v107, 0xc2a00000, v107
	v_exp_f32_e32 v111, v111
	v_rcp_f32_e32 v106, v106
	v_mul_f32_e32 v107, 0xbfb8aa3b, v107
	v_exp_f32_e32 v107, v107
	v_cvt_pk_f16_f32 v194, v158, v159
	v_or_b32_e32 v158, 16, v152
	v_add_f32_e32 v110, 1.0, v110
	v_mul_f32_e32 v112, v112, v116
	v_mul_f32_e32 v113, v113, v116
	v_cvt_pk_f16_f32 v197, v154, v183
	v_ashrrev_i32_e32 v159, 31, v158
	v_rcp_f32_e32 v154, v110
	v_add_f32_e32 v110, 1.0, v111
	v_max_f32_e32 v112, 0xc2a00000, v112
	v_max_f32_e32 v113, 0xc2a00000, v113
	v_fma_f32 v106, v171, v106, v132
	v_cvt_pk_f16_f32 v195, v160, v161
	v_rcp_f32_e32 v160, v110
	v_lshlrev_b64 v[110:111], 12, v[158:159]
	v_mul_f32_e32 v112, 0xbfb8aa3b, v112
	v_mul_f32_e32 v113, 0xbfb8aa3b, v113
	v_log_f32_e32 v159, v106
	v_add_f32_e32 v106, 1.0, v107
	v_mul_f32_e32 v107, v108, v116
	v_exp_f32_e32 v112, v112
	v_exp_f32_e32 v113, v113
	v_max_f32_e32 v107, 0xc2a00000, v107
	v_mul_f32_e32 v108, v109, v116
	v_mul_f32_e32 v107, 0xbfb8aa3b, v107
	v_max_f32_e32 v108, 0xc2a00000, v108
	v_exp_f32_e32 v107, v107
	v_mul_f32_e32 v108, 0xbfb8aa3b, v108
	v_exp_f32_e32 v108, v108
	v_add_f32_e32 v112, 1.0, v112
	v_add_f32_e32 v113, 1.0, v113
	v_rcp_f32_e32 v112, v112
	v_rcp_f32_e32 v113, v113
	v_mul_f32_e32 v98, v98, v116
	v_rcp_f32_e32 v106, v106
	v_add_f32_e32 v107, 1.0, v107
	v_max_f32_e32 v98, 0xc2a00000, v98
	v_rcp_f32_e32 v107, v107
	v_add_f32_e32 v108, 1.0, v108
	v_mul_f32_e32 v98, 0xbfb8aa3b, v98
	v_rcp_f32_e32 v108, v108
	v_exp_f32_e32 v98, v98
	v_fma_f32 v112, v178, v112, v138
	v_fma_f32 v113, v177, v113, v139
	v_log_f32_e32 v112, v112
	v_log_f32_e32 v113, v113
	v_fma_f32 v106, v170, v106, v133
	v_log_f32_e32 v109, v106
	v_fma_f32 v106, v169, v107, v134
	v_mul_f32_e32 v102, v102, v116
	v_mul_f32_e32 v99, v99, v116
	v_fma_f32 v154, v180, v154, v136
	v_fma_f32 v158, v179, v160, v137
	v_log_f32_e32 v160, v106
	v_fma_f32 v106, v155, v108, v135
	v_max_f32_e32 v102, 0xc2a00000, v102
	v_add_f32_e32 v98, 1.0, v98
	v_max_f32_e32 v99, 0xc2a00000, v99
	v_log_f32_e32 v154, v154
	v_log_f32_e32 v158, v158
	v_log_f32_e32 v161, v106
	v_mul_f32_e32 v102, 0xbfb8aa3b, v102
	v_rcp_f32_e32 v98, v98
	v_mul_f32_e32 v99, 0xbfb8aa3b, v99
	v_cvt_pk_f16_f32 v107, v112, v113
	v_exp_f32_e32 v112, v102
	v_mul_f32_e32 v102, v103, v116
	v_exp_f32_e32 v99, v99
	v_max_f32_e32 v102, 0xc2a00000, v102
	v_lshl_add_u64 v[110:111], s[26:27], 0, v[110:111]
	v_mul_f32_e32 v102, 0xbfb8aa3b, v102
	v_cvt_pk_f16_f32 v106, v154, v158
	v_cvt_pk_f16_f32 v108, v159, v109
	v_cvt_pk_f16_f32 v109, v160, v161
	v_exp_f32_e32 v113, v102
	v_lshl_add_u64 v[102:103], v[110:111], 0, v[114:115]
	v_fma_f32 v98, v123, v98, v124
	ds_bpermute_b32 v244, v250, v106
	ds_bpermute_b32 v245, v250, v107
	ds_bpermute_b32 v246, v250, v108
	ds_bpermute_b32 v247, v250, v109
	ds_bpermute_b32 v248, v250, v102
	v_mul_f32_e32 v104, v104, v116
	v_mul_f32_e32 v105, v105, v116
	v_log_f32_e32 v108, v98
	v_add_f32_e32 v98, 1.0, v99
	v_mul_f32_e32 v99, v100, v116
	v_max_f32_e32 v99, 0xc2a00000, v99
	v_mul_f32_e32 v100, v101, v116
	v_max_f32_e32 v104, 0xc2a00000, v104
	v_max_f32_e32 v105, 0xc2a00000, v105
	v_mul_f32_e32 v99, 0xbfb8aa3b, v99
	v_max_f32_e32 v100, 0xc2a00000, v100
	v_mul_f32_e32 v104, 0xbfb8aa3b, v104
	v_mul_f32_e32 v105, 0xbfb8aa3b, v105
	v_exp_f32_e32 v99, v99
	v_mul_f32_e32 v100, 0xbfb8aa3b, v100
	v_exp_f32_e32 v104, v104
	v_exp_f32_e32 v105, v105
	v_exp_f32_e32 v100, v100
	v_rcp_f32_e32 v98, v98
	v_add_f32_e32 v99, 1.0, v99
	v_add_f32_e32 v110, 1.0, v112
	v_add_f32_e32 v111, 1.0, v113
	v_add_f32_e32 v104, 1.0, v104
	v_add_f32_e32 v105, 1.0, v105
	v_rcp_f32_e32 v99, v99
	v_add_f32_e32 v100, 1.0, v100
	v_rcp_f32_e32 v110, v110
	v_rcp_f32_e32 v111, v111
	v_rcp_f32_e32 v104, v104
	v_rcp_f32_e32 v105, v105
	v_rcp_f32_e32 v100, v100
	v_mul_f32_e32 v90, v90, v117
	v_fma_f32 v98, v120, v98, v125
	v_mul_f32_e32 v94, v94, v117
	v_max_f32_e32 v90, 0xc2a00000, v90
	v_log_f32_e32 v101, v98
	v_fma_f32 v98, v118, v99, v126
	v_max_f32_e32 v94, 0xc2a00000, v94
	v_mul_f32_e32 v90, 0xbfb8aa3b, v90
	v_fma_f32 v106, v153, v110, v128
	v_fma_f32 v107, v168, v111, v129
	v_fma_f32 v104, v121, v104, v130
	v_fma_f32 v105, v122, v105, v131
	v_log_f32_e32 v109, v98
	v_fma_f32 v98, v119, v100, v127
	v_mul_f32_e32 v94, 0xbfb8aa3b, v94
	v_exp_f32_e32 v90, v90
	v_log_f32_e32 v106, v106
	v_log_f32_e32 v107, v107
	v_log_f32_e32 v104, v104
	v_log_f32_e32 v105, v105
	v_log_f32_e32 v110, v98
	v_exp_f32_e32 v94, v94
	v_mul_f32_e32 v95, v95, v117
	v_max_f32_e32 v95, 0xc2a00000, v95
	v_mul_f32_e32 v91, v91, v117
	v_mul_f32_e32 v95, 0xbfb8aa3b, v95
	v_add_f32_e32 v90, 1.0, v90
	v_max_f32_e32 v91, 0xc2a00000, v91
	v_cvt_pk_f16_f32 v98, v106, v107
	v_cvt_pk_f16_f32 v99, v104, v105
	v_cvt_pk_f16_f32 v100, v108, v101
	v_cvt_pk_f16_f32 v101, v109, v110
	v_exp_f32_e32 v95, v95
	v_add_f32_e32 v94, 1.0, v94
	v_rcp_f32_e32 v90, v90
	v_mul_f32_e32 v91, 0xbfb8aa3b, v91
	s_waitcnt lgkmcnt(5)
	v_subrev_u32_e32 v242, s82, v242
	global_store_dwordx4 v242, v[238:241], s[82:83]
	ds_bpermute_b32 v232, v250, v98
	ds_bpermute_b32 v233, v250, v99
	ds_bpermute_b32 v234, v250, v100
	ds_bpermute_b32 v235, v250, v101
	ds_bpermute_b32 v236, v250, v102
	v_exp_f32_e32 v91, v91
	v_fma_f32 v90, v171, v90, v132
	v_rcp_f32_e32 v100, v94
	v_or_b32_e32 v98, 32, v152
	v_ashrrev_i32_e32 v99, 31, v98
	v_add_f32_e32 v94, 1.0, v95
	v_rcp_f32_e32 v101, v94
	v_lshlrev_b64 v[94:95], 12, v[98:99]
	v_fma_f32 v98, v180, v100, v136
	v_log_f32_e32 v100, v90
	v_add_f32_e32 v90, 1.0, v91
	v_mul_f32_e32 v91, v92, v117
	v_mul_f32_e32 v96, v96, v117
	v_mul_f32_e32 v97, v97, v117
	v_max_f32_e32 v91, 0xc2a00000, v91
	v_mul_f32_e32 v92, v93, v117
	v_max_f32_e32 v96, 0xc2a00000, v96
	v_max_f32_e32 v97, 0xc2a00000, v97
	v_mul_f32_e32 v91, 0xbfb8aa3b, v91
	v_max_f32_e32 v92, 0xc2a00000, v92
	v_mul_f32_e32 v96, 0xbfb8aa3b, v96
	v_mul_f32_e32 v97, 0xbfb8aa3b, v97
	v_exp_f32_e32 v91, v91
	v_mul_f32_e32 v92, 0xbfb8aa3b, v92
	v_exp_f32_e32 v96, v96
	v_exp_f32_e32 v97, v97
	v_exp_f32_e32 v92, v92
	v_mul_f32_e32 v82, v82, v117
	v_rcp_f32_e32 v90, v90
	v_add_f32_e32 v91, 1.0, v91
	v_max_f32_e32 v82, 0xc2a00000, v82
	v_add_f32_e32 v96, 1.0, v96
	v_add_f32_e32 v97, 1.0, v97
	v_rcp_f32_e32 v91, v91
	v_add_f32_e32 v92, 1.0, v92
	v_mul_f32_e32 v82, 0xbfb8aa3b, v82
	v_rcp_f32_e32 v96, v96
	v_rcp_f32_e32 v97, v97
	v_rcp_f32_e32 v92, v92
	v_exp_f32_e32 v82, v82
	v_fma_f32 v90, v170, v90, v133
	v_log_f32_e32 v93, v90
	v_fma_f32 v90, v169, v91, v134
	v_mul_f32_e32 v83, v83, v117
	v_fma_f32 v99, v179, v101, v137
	v_fma_f32 v96, v178, v96, v138
	v_fma_f32 v97, v177, v97, v139
	v_log_f32_e32 v101, v90
	v_fma_f32 v90, v155, v92, v135
	v_add_f32_e32 v82, 1.0, v82
	v_max_f32_e32 v83, 0xc2a00000, v83
	v_log_f32_e32 v98, v98
	v_log_f32_e32 v99, v99
	v_log_f32_e32 v96, v96
	v_log_f32_e32 v97, v97
	v_log_f32_e32 v102, v90
	v_rcp_f32_e32 v82, v82
	v_mul_f32_e32 v83, 0xbfb8aa3b, v83
	v_exp_f32_e32 v83, v83
	v_lshl_add_u64 v[94:95], s[26:27], 0, v[94:95]
	v_cvt_pk_f16_f32 v90, v98, v99
	v_cvt_pk_f16_f32 v91, v96, v97
	v_cvt_pk_f16_f32 v92, v100, v93
	v_cvt_pk_f16_f32 v93, v101, v102
	v_lshl_add_u64 v[94:95], v[94:95], 0, v[114:115]
	v_fma_f32 v82, v123, v82, v124
	s_waitcnt lgkmcnt(5)
	v_subrev_u32_e32 v248, s82, v248
	global_store_dwordx4 v248, v[244:247], s[82:83]
	ds_bpermute_b32 v238, v250, v90
	ds_bpermute_b32 v239, v250, v91
	ds_bpermute_b32 v240, v250, v92
	ds_bpermute_b32 v241, v250, v93
	ds_bpermute_b32 v242, v250, v94
	v_mul_f32_e32 v86, v86, v117
	v_mul_f32_e32 v87, v87, v117
	v_log_f32_e32 v90, v82
	v_add_f32_e32 v82, 1.0, v83
	v_mul_f32_e32 v83, v84, v117
	v_max_f32_e32 v83, 0xc2a00000, v83
	v_mul_f32_e32 v84, v85, v117
	v_mul_f32_e32 v83, 0xbfb8aa3b, v83
	v_max_f32_e32 v84, 0xc2a00000, v84
	v_exp_f32_e32 v83, v83
	v_mul_f32_e32 v84, 0xbfb8aa3b, v84
	v_exp_f32_e32 v84, v84
	v_rcp_f32_e32 v82, v82
	v_add_f32_e32 v83, 1.0, v83
	v_rcp_f32_e32 v83, v83
	v_add_f32_e32 v84, 1.0, v84
	v_rcp_f32_e32 v84, v84
	v_mul_f32_e32 v88, v88, v117
	v_mul_f32_e32 v89, v89, v117
	v_max_f32_e32 v86, 0xc2a00000, v86
	v_max_f32_e32 v87, 0xc2a00000, v87
	v_max_f32_e32 v88, 0xc2a00000, v88
	v_max_f32_e32 v89, 0xc2a00000, v89
	v_fma_f32 v82, v120, v82, v125
	v_mul_f32_e32 v86, 0xbfb8aa3b, v86
	v_mul_f32_e32 v87, 0xbfb8aa3b, v87
	v_mul_f32_e32 v88, 0xbfb8aa3b, v88
	v_mul_f32_e32 v89, 0xbfb8aa3b, v89
	v_log_f32_e32 v91, v82
	v_fma_f32 v82, v118, v83, v126
	v_exp_f32_e32 v86, v86
	v_exp_f32_e32 v87, v87
	v_exp_f32_e32 v88, v88
	v_exp_f32_e32 v89, v89
	v_log_f32_e32 v92, v82
	v_fma_f32 v82, v119, v84, v127
	v_log_f32_e32 v93, v82
	ds_read2_b32 v[82:83], v176 offset0:48 offset1:128
	v_add_f32_e32 v86, 1.0, v86
	v_add_f32_e32 v87, 1.0, v87
	v_add_f32_e32 v88, 1.0, v88
	v_add_f32_e32 v89, 1.0, v89
	v_rcp_f32_e32 v86, v86
	v_rcp_f32_e32 v87, v87
	v_rcp_f32_e32 v88, v88
	v_rcp_f32_e32 v89, v89
	s_waitcnt lgkmcnt(0)
	v_mul_f32_e32 v74, v74, v82
	v_mul_f32_e32 v78, v78, v82
	v_max_f32_e32 v74, 0xc2a00000, v74
	v_max_f32_e32 v78, 0xc2a00000, v78
	v_mul_f32_e32 v74, 0xbfb8aa3b, v74
	v_fma_f32 v86, v153, v86, v128
	v_fma_f32 v87, v168, v87, v129
	v_fma_f32 v88, v121, v88, v130
	v_fma_f32 v89, v122, v89, v131
	v_mul_f32_e32 v78, 0xbfb8aa3b, v78
	v_exp_f32_e32 v74, v74
	v_log_f32_e32 v86, v86
	v_log_f32_e32 v87, v87
	v_log_f32_e32 v88, v88
	v_log_f32_e32 v89, v89
	v_exp_f32_e32 v78, v78
	v_mul_f32_e32 v79, v79, v82
	v_max_f32_e32 v79, 0xc2a00000, v79
	v_mul_f32_e32 v75, v75, v82
	v_mul_f32_e32 v79, 0xbfb8aa3b, v79
	v_add_f32_e32 v74, 1.0, v74
	v_max_f32_e32 v75, 0xc2a00000, v75
	v_cvt_pk_f16_f32 v84, v86, v87
	v_cvt_pk_f16_f32 v85, v88, v89
	v_cvt_pk_f16_f32 v86, v90, v91
	v_cvt_pk_f16_f32 v87, v92, v93
	v_exp_f32_e32 v79, v79
	v_add_f32_e32 v78, 1.0, v78
	v_rcp_f32_e32 v74, v74
	v_mul_f32_e32 v75, 0xbfb8aa3b, v75
	s_waitcnt lgkmcnt(6)
	v_subrev_u32_e32 v236, s82, v236
	global_store_dwordx4 v236, v[232:235], s[82:83] offset:64
	ds_bpermute_b32 v244, v250, v84
	ds_bpermute_b32 v245, v250, v85
	ds_bpermute_b32 v246, v250, v86
	ds_bpermute_b32 v247, v250, v87
	ds_bpermute_b32 v248, v250, v94
	v_exp_f32_e32 v75, v75
	v_mul_f32_e32 v80, v80, v82
	v_rcp_f32_e32 v86, v78
	v_or_b32_e32 v84, 48, v152
	v_mul_f32_e32 v81, v81, v82
	v_ashrrev_i32_e32 v85, 31, v84
	v_add_f32_e32 v78, 1.0, v79
	v_max_f32_e32 v80, 0xc2a00000, v80
	v_max_f32_e32 v81, 0xc2a00000, v81
	v_fma_f32 v74, v171, v74, v132
	v_rcp_f32_e32 v87, v78
	v_lshlrev_b64 v[78:79], 12, v[84:85]
	v_fma_f32 v84, v180, v86, v136
	v_mul_f32_e32 v80, 0xbfb8aa3b, v80
	v_mul_f32_e32 v81, 0xbfb8aa3b, v81
	v_log_f32_e32 v86, v74
	v_add_f32_e32 v74, 1.0, v75
	v_mul_f32_e32 v75, v76, v82
	v_exp_f32_e32 v80, v80
	v_exp_f32_e32 v81, v81
	v_max_f32_e32 v75, 0xc2a00000, v75
	v_mul_f32_e32 v76, v77, v82
	v_mul_f32_e32 v75, 0xbfb8aa3b, v75
	v_max_f32_e32 v76, 0xc2a00000, v76
	v_exp_f32_e32 v75, v75
	v_mul_f32_e32 v76, 0xbfb8aa3b, v76
	v_exp_f32_e32 v76, v76
	v_add_f32_e32 v80, 1.0, v80
	v_add_f32_e32 v81, 1.0, v81
	v_rcp_f32_e32 v80, v80
	v_rcp_f32_e32 v81, v81
	v_mul_f32_e32 v66, v66, v82
	v_rcp_f32_e32 v74, v74
	v_add_f32_e32 v75, 1.0, v75
	v_max_f32_e32 v66, 0xc2a00000, v66
	v_rcp_f32_e32 v75, v75
	v_add_f32_e32 v76, 1.0, v76
	v_mul_f32_e32 v66, 0xbfb8aa3b, v66
	v_rcp_f32_e32 v76, v76
	v_exp_f32_e32 v66, v66
	v_fma_f32 v80, v178, v80, v138
	v_fma_f32 v81, v177, v81, v139
	v_log_f32_e32 v80, v80
	v_log_f32_e32 v81, v81
	v_fma_f32 v74, v170, v74, v133
	v_log_f32_e32 v77, v74
	v_fma_f32 v74, v169, v75, v134
	v_mul_f32_e32 v70, v70, v82
	v_mul_f32_e32 v67, v67, v82
	v_fma_f32 v85, v179, v87, v137
	v_log_f32_e32 v87, v74
	v_fma_f32 v74, v155, v76, v135
	v_max_f32_e32 v70, 0xc2a00000, v70
	v_add_f32_e32 v66, 1.0, v66
	v_max_f32_e32 v67, 0xc2a00000, v67
	v_log_f32_e32 v84, v84
	v_log_f32_e32 v85, v85
	v_log_f32_e32 v88, v74
	v_mul_f32_e32 v70, 0xbfb8aa3b, v70
	v_rcp_f32_e32 v66, v66
	v_mul_f32_e32 v67, 0xbfb8aa3b, v67
	v_cvt_pk_f16_f32 v75, v80, v81
	v_exp_f32_e32 v80, v70
	v_mul_f32_e32 v70, v71, v82
	v_exp_f32_e32 v67, v67
	v_max_f32_e32 v70, 0xc2a00000, v70
	v_lshl_add_u64 v[78:79], s[26:27], 0, v[78:79]
	v_mul_f32_e32 v70, 0xbfb8aa3b, v70
	v_cvt_pk_f16_f32 v74, v84, v85
	v_cvt_pk_f16_f32 v76, v86, v77
	v_cvt_pk_f16_f32 v77, v87, v88
	v_exp_f32_e32 v81, v70
	v_lshl_add_u64 v[70:71], v[78:79], 0, v[114:115]
	v_fma_f32 v66, v123, v66, v124
	s_waitcnt lgkmcnt(6)
	v_subrev_u32_e32 v242, s82, v242
	global_store_dwordx4 v242, v[238:241], s[82:83]
	ds_bpermute_b32 v232, v250, v74
	ds_bpermute_b32 v233, v250, v75
	ds_bpermute_b32 v234, v250, v76
	ds_bpermute_b32 v235, v250, v77
	ds_bpermute_b32 v236, v250, v70
	v_mul_f32_e32 v72, v72, v82
	v_mul_f32_e32 v73, v73, v82
	v_log_f32_e32 v76, v66
	v_add_f32_e32 v66, 1.0, v67
	v_mul_f32_e32 v67, v68, v82
	v_max_f32_e32 v67, 0xc2a00000, v67
	v_mul_f32_e32 v68, v69, v82
	v_max_f32_e32 v72, 0xc2a00000, v72
	v_max_f32_e32 v73, 0xc2a00000, v73
	v_mul_f32_e32 v67, 0xbfb8aa3b, v67
	v_max_f32_e32 v68, 0xc2a00000, v68
	v_mul_f32_e32 v72, 0xbfb8aa3b, v72
	v_mul_f32_e32 v73, 0xbfb8aa3b, v73
	v_exp_f32_e32 v67, v67
	v_mul_f32_e32 v68, 0xbfb8aa3b, v68
	v_exp_f32_e32 v72, v72
	v_exp_f32_e32 v73, v73
	v_exp_f32_e32 v68, v68
	v_mul_f32_e32 v58, v58, v83
	v_rcp_f32_e32 v66, v66
	v_add_f32_e32 v67, 1.0, v67
	v_max_f32_e32 v58, 0xc2a00000, v58
	v_add_f32_e32 v78, 1.0, v80
	v_add_f32_e32 v79, 1.0, v81
	v_add_f32_e32 v72, 1.0, v72
	v_add_f32_e32 v73, 1.0, v73
	v_rcp_f32_e32 v67, v67
	v_add_f32_e32 v68, 1.0, v68
	v_mul_f32_e32 v58, 0xbfb8aa3b, v58
	v_rcp_f32_e32 v78, v78
	v_rcp_f32_e32 v79, v79
	v_rcp_f32_e32 v72, v72
	v_rcp_f32_e32 v73, v73
	v_rcp_f32_e32 v68, v68
	v_exp_f32_e32 v58, v58
	v_fma_f32 v66, v120, v66, v125
	v_log_f32_e32 v69, v66
	v_fma_f32 v66, v118, v67, v126
	v_mul_f32_e32 v59, v59, v83
	v_fma_f32 v74, v153, v78, v128
	v_fma_f32 v75, v168, v79, v129
	v_fma_f32 v72, v121, v72, v130
	v_fma_f32 v73, v122, v73, v131
	v_log_f32_e32 v77, v66
	v_fma_f32 v66, v119, v68, v127
	v_add_f32_e32 v58, 1.0, v58
	v_max_f32_e32 v59, 0xc2a00000, v59
	v_log_f32_e32 v74, v74
	v_log_f32_e32 v75, v75
	v_log_f32_e32 v72, v72
	v_log_f32_e32 v73, v73
	v_log_f32_e32 v78, v66
	v_rcp_f32_e32 v58, v58
	v_mul_f32_e32 v59, 0xbfb8aa3b, v59
	v_exp_f32_e32 v59, v59
	v_mul_f32_e32 v64, v64, v83
	v_mul_f32_e32 v65, v65, v83
	v_max_f32_e32 v64, 0xc2a00000, v64
	v_max_f32_e32 v65, 0xc2a00000, v65
	v_cvt_pk_f16_f32 v66, v74, v75
	v_cvt_pk_f16_f32 v67, v72, v73
	v_cvt_pk_f16_f32 v68, v76, v69
	v_mul_f32_e32 v62, v62, v83
	v_mul_f32_e32 v63, v63, v83
	v_cvt_pk_f16_f32 v69, v77, v78
	v_mul_f32_e32 v64, 0xbfb8aa3b, v64
	v_mul_f32_e32 v65, 0xbfb8aa3b, v65
	v_fma_f32 v58, v171, v58, v132
	v_max_f32_e32 v62, 0xc2a00000, v62
	v_max_f32_e32 v63, 0xc2a00000, v63
	s_waitcnt lgkmcnt(5)
	v_subrev_u32_e32 v248, s82, v248
	global_store_dwordx4 v248, v[244:247], s[82:83] offset:64
	ds_bpermute_b32 v238, v250, v66
	ds_bpermute_b32 v239, v250, v67
	ds_bpermute_b32 v240, v250, v68
	ds_bpermute_b32 v241, v250, v69
	ds_bpermute_b32 v242, v250, v70
	v_exp_f32_e32 v64, v64
	v_exp_f32_e32 v65, v65
	v_log_f32_e32 v66, v58
	v_add_f32_e32 v58, 1.0, v59
	v_mul_f32_e32 v59, v60, v83
	v_mul_f32_e32 v62, 0xbfb8aa3b, v62
	v_mul_f32_e32 v63, 0xbfb8aa3b, v63
	v_max_f32_e32 v59, 0xc2a00000, v59
	v_mul_f32_e32 v60, v61, v83
	v_exp_f32_e32 v62, v62
	v_exp_f32_e32 v63, v63
	v_mul_f32_e32 v59, 0xbfb8aa3b, v59
	v_max_f32_e32 v60, 0xc2a00000, v60
	v_exp_f32_e32 v59, v59
	v_mul_f32_e32 v60, 0xbfb8aa3b, v60
	v_add_f32_e32 v64, 1.0, v64
	v_add_f32_e32 v65, 1.0, v65
	v_exp_f32_e32 v60, v60
	v_rcp_f32_e32 v64, v64
	v_rcp_f32_e32 v65, v65
	v_add_f32_e32 v62, 1.0, v62
	v_add_f32_e32 v63, 1.0, v63
	v_mul_f32_e32 v50, v50, v83
	v_rcp_f32_e32 v62, v62
	v_rcp_f32_e32 v63, v63
	v_rcp_f32_e32 v58, v58
	v_add_f32_e32 v59, 1.0, v59
	v_max_f32_e32 v50, 0xc2a00000, v50
	v_rcp_f32_e32 v59, v59
	v_add_f32_e32 v60, 1.0, v60
	v_mul_f32_e32 v50, 0xbfb8aa3b, v50
	v_fma_f32 v64, v178, v64, v138
	v_fma_f32 v65, v177, v65, v139
	v_rcp_f32_e32 v60, v60
	v_exp_f32_e32 v50, v50
	v_log_f32_e32 v64, v64
	v_log_f32_e32 v65, v65
	v_fma_f32 v62, v180, v62, v136
	v_fma_f32 v63, v179, v63, v137
	v_fma_f32 v58, v170, v58, v133
	v_mul_f32_e32 v54, v54, v83
	v_log_f32_e32 v62, v62
	v_log_f32_e32 v63, v63
	v_log_f32_e32 v61, v58
	v_fma_f32 v58, v169, v59, v134
	v_max_f32_e32 v54, 0xc2a00000, v54
	v_mul_f32_e32 v51, v51, v83
	v_log_f32_e32 v67, v58
	v_fma_f32 v58, v155, v60, v135
	v_mul_f32_e32 v54, 0xbfb8aa3b, v54
	v_add_f32_e32 v50, 1.0, v50
	v_max_f32_e32 v51, 0xc2a00000, v51
	v_log_f32_e32 v68, v58
	v_cvt_pk_f16_f32 v59, v64, v65
	v_exp_f32_e32 v64, v54
	v_mul_f32_e32 v54, v55, v83
	v_rcp_f32_e32 v50, v50
	v_mul_f32_e32 v51, 0xbfb8aa3b, v51
	v_max_f32_e32 v54, 0xc2a00000, v54
	v_exp_f32_e32 v51, v51
	v_cvt_pk_f16_f32 v58, v62, v63
	v_lshl_add_u64 v[62:63], v[166:167], 0, s[14:15]
	v_mul_f32_e32 v54, 0xbfb8aa3b, v54
	s_mov_b32 s14, 0x80000
	v_exp_f32_e32 v65, v54
	v_add_co_u32_e32 v54, vcc, s14, v166
	v_cvt_pk_f16_f32 v60, v66, v61
	v_cvt_pk_f16_f32 v61, v67, v68
	v_addc_co_u32_e32 v55, vcc, 0, v167, vcc
	v_fma_f32 v50, v123, v50, v124
	s_waitcnt lgkmcnt(5)
	v_subrev_u32_e32 v236, s82, v236
	global_store_dwordx4 v236, v[232:235], s[82:83]
	ds_bpermute_b32 v244, v250, v58
	ds_bpermute_b32 v245, v250, v59
	ds_bpermute_b32 v246, v250, v60
	ds_bpermute_b32 v247, v250, v61
	ds_bpermute_b32 v248, v250, v54
	v_mul_f32_e32 v56, v56, v83
	v_mul_f32_e32 v57, v57, v83
	v_log_f32_e32 v58, v50
	v_add_f32_e32 v50, 1.0, v51
	v_mul_f32_e32 v51, v52, v83
	v_max_f32_e32 v51, 0xc2a00000, v51
	v_mul_f32_e32 v51, 0xbfb8aa3b, v51
	v_exp_f32_e32 v51, v51
	v_rcp_f32_e32 v50, v50
	v_mul_f32_e32 v52, v53, v83
	v_max_f32_e32 v56, 0xc2a00000, v56
	v_add_f32_e32 v51, 1.0, v51
	v_rcp_f32_e32 v51, v51
	v_fma_f32 v50, v120, v50, v125
	v_log_f32_e32 v59, v50
	v_max_f32_e32 v57, 0xc2a00000, v57
	v_fma_f32 v50, v118, v51, v126
	v_log_f32_e32 v60, v50
	ds_read2_b32 v[50:51], v176 offset0:144 offset1:160
	v_max_f32_e32 v52, 0xc2a00000, v52
	v_mul_f32_e32 v56, 0xbfb8aa3b, v56
	v_mul_f32_e32 v57, 0xbfb8aa3b, v57
	v_mul_f32_e32 v52, 0xbfb8aa3b, v52
	v_exp_f32_e32 v56, v56
	v_exp_f32_e32 v57, v57
	v_exp_f32_e32 v52, v52
	s_waitcnt lgkmcnt(0)
	v_mul_f32_e32 v42, v42, v50
	v_max_f32_e32 v42, 0xc2a00000, v42
	v_add_f32_e32 v64, 1.0, v64
	v_add_f32_e32 v65, 1.0, v65
	v_add_f32_e32 v56, 1.0, v56
	v_add_f32_e32 v57, 1.0, v57
	v_add_f32_e32 v52, 1.0, v52
	v_mul_f32_e32 v42, 0xbfb8aa3b, v42
	v_rcp_f32_e32 v64, v64
	v_rcp_f32_e32 v65, v65
	v_rcp_f32_e32 v56, v56
	v_rcp_f32_e32 v57, v57
	v_rcp_f32_e32 v52, v52
	v_exp_f32_e32 v42, v42
	v_mul_f32_e32 v43, v43, v50
	v_fma_f32 v54, v153, v64, v128
	v_fma_f32 v55, v168, v65, v129
	v_fma_f32 v56, v121, v56, v130
	v_fma_f32 v57, v122, v57, v131
	v_fma_f32 v52, v119, v52, v127
	v_add_f32_e32 v42, 1.0, v42
	v_max_f32_e32 v43, 0xc2a00000, v43
	v_log_f32_e32 v54, v54
	v_log_f32_e32 v55, v55
	v_log_f32_e32 v56, v56
	v_log_f32_e32 v57, v57
	v_log_f32_e32 v61, v52
	v_rcp_f32_e32 v42, v42
	v_mul_f32_e32 v43, 0xbfb8aa3b, v43
	v_exp_f32_e32 v43, v43
	v_mul_f32_e32 v48, v48, v50
	v_mul_f32_e32 v49, v49, v50
	v_max_f32_e32 v48, 0xc2a00000, v48
	v_max_f32_e32 v49, 0xc2a00000, v49
	v_cvt_pk_f16_f32 v52, v54, v55
	v_cvt_pk_f16_f32 v53, v56, v57
	v_cvt_pk_f16_f32 v54, v58, v59
	v_mul_f32_e32 v46, v46, v50
	v_mul_f32_e32 v47, v47, v50
	v_cvt_pk_f16_f32 v55, v60, v61
	v_mul_f32_e32 v48, 0xbfb8aa3b, v48
	v_mul_f32_e32 v49, 0xbfb8aa3b, v49
	v_fma_f32 v42, v171, v42, v132
	v_max_f32_e32 v46, 0xc2a00000, v46
	v_max_f32_e32 v47, 0xc2a00000, v47
	s_waitcnt lgkmcnt(6)
	v_subrev_u32_e32 v242, s82, v242
	global_store_dwordx4 v242, v[238:241], s[82:83] offset:64
	ds_bpermute_b32 v232, v250, v52
	ds_bpermute_b32 v233, v250, v53
	ds_bpermute_b32 v234, v250, v54
	ds_bpermute_b32 v235, v250, v55
	ds_bpermute_b32 v236, v250, v62
	v_exp_f32_e32 v48, v48
	v_exp_f32_e32 v49, v49
	v_log_f32_e32 v52, v42
	v_add_f32_e32 v42, 1.0, v43
	v_mul_f32_e32 v43, v44, v50
	v_mul_f32_e32 v46, 0xbfb8aa3b, v46
	v_mul_f32_e32 v47, 0xbfb8aa3b, v47
	v_max_f32_e32 v43, 0xc2a00000, v43
	v_mul_f32_e32 v44, v45, v50
	v_exp_f32_e32 v46, v46
	v_exp_f32_e32 v47, v47
	v_mul_f32_e32 v43, 0xbfb8aa3b, v43
	v_max_f32_e32 v44, 0xc2a00000, v44
	v_exp_f32_e32 v43, v43
	v_mul_f32_e32 v44, 0xbfb8aa3b, v44
	v_add_f32_e32 v48, 1.0, v48
	v_add_f32_e32 v49, 1.0, v49
	v_exp_f32_e32 v44, v44
	v_rcp_f32_e32 v48, v48
	v_rcp_f32_e32 v49, v49
	v_add_f32_e32 v46, 1.0, v46
	v_add_f32_e32 v47, 1.0, v47
	v_mul_f32_e32 v34, v34, v50
	v_rcp_f32_e32 v46, v46
	v_rcp_f32_e32 v47, v47
	v_rcp_f32_e32 v42, v42
	v_add_f32_e32 v43, 1.0, v43
	v_max_f32_e32 v34, 0xc2a00000, v34
	v_rcp_f32_e32 v43, v43
	v_add_f32_e32 v44, 1.0, v44
	v_mul_f32_e32 v34, 0xbfb8aa3b, v34
	v_fma_f32 v48, v178, v48, v138
	v_fma_f32 v49, v177, v49, v139
	v_rcp_f32_e32 v44, v44
	v_exp_f32_e32 v34, v34
	v_log_f32_e32 v48, v48
	v_log_f32_e32 v49, v49
	v_fma_f32 v46, v180, v46, v136
	v_fma_f32 v47, v179, v47, v137
	v_fma_f32 v42, v170, v42, v133
	v_mul_f32_e32 v38, v38, v50
	v_log_f32_e32 v46, v46
	v_log_f32_e32 v47, v47
	v_log_f32_e32 v45, v42
	v_fma_f32 v42, v169, v43, v134
	v_max_f32_e32 v38, 0xc2a00000, v38
	v_mul_f32_e32 v35, v35, v50
	v_log_f32_e32 v53, v42
	v_fma_f32 v42, v155, v44, v135
	v_mul_f32_e32 v38, 0xbfb8aa3b, v38
	v_add_f32_e32 v34, 1.0, v34
	v_max_f32_e32 v35, 0xc2a00000, v35
	v_log_f32_e32 v54, v42
	v_cvt_pk_f16_f32 v43, v48, v49
	v_exp_f32_e32 v48, v38
	v_mul_f32_e32 v38, v39, v50
	v_rcp_f32_e32 v34, v34
	v_mul_f32_e32 v35, 0xbfb8aa3b, v35
	s_mov_b64 s[14:15], 0x90000
	v_max_f32_e32 v38, 0xc2a00000, v38
	v_exp_f32_e32 v35, v35
	v_cvt_pk_f16_f32 v42, v46, v47
	v_lshl_add_u64 v[46:47], v[166:167], 0, s[14:15]
	v_mul_f32_e32 v38, 0xbfb8aa3b, v38
	s_mov_b32 s14, 0x90000
	v_exp_f32_e32 v49, v38
	v_add_co_u32_e32 v38, vcc, s14, v166
	v_cvt_pk_f16_f32 v44, v52, v45
	v_cvt_pk_f16_f32 v45, v53, v54
	v_addc_co_u32_e32 v39, vcc, 0, v167, vcc
	v_fma_f32 v34, v123, v34, v124
	s_waitcnt lgkmcnt(6)
	v_subrev_u32_e32 v248, s82, v248
	global_store_dwordx4 v248, v[244:247], s[82:83]
	ds_bpermute_b32 v238, v250, v42
	ds_bpermute_b32 v239, v250, v43
	ds_bpermute_b32 v240, v250, v44
	ds_bpermute_b32 v241, v250, v45
	ds_bpermute_b32 v242, v250, v38
	v_mul_f32_e32 v40, v40, v50
	v_mul_f32_e32 v41, v41, v50
	v_log_f32_e32 v42, v34
	v_add_f32_e32 v34, 1.0, v35
	v_mul_f32_e32 v35, v36, v50
	v_max_f32_e32 v35, 0xc2a00000, v35
	v_mul_f32_e32 v36, v37, v50
	v_max_f32_e32 v40, 0xc2a00000, v40
	v_max_f32_e32 v41, 0xc2a00000, v41
	v_mul_f32_e32 v35, 0xbfb8aa3b, v35
	v_max_f32_e32 v36, 0xc2a00000, v36
	v_mul_f32_e32 v40, 0xbfb8aa3b, v40
	v_mul_f32_e32 v41, 0xbfb8aa3b, v41
	v_exp_f32_e32 v35, v35
	v_mul_f32_e32 v36, 0xbfb8aa3b, v36
	v_exp_f32_e32 v40, v40
	v_exp_f32_e32 v41, v41
	v_exp_f32_e32 v36, v36
	v_mul_f32_e32 v26, v26, v51
	v_rcp_f32_e32 v34, v34
	v_add_f32_e32 v35, 1.0, v35
	v_max_f32_e32 v26, 0xc2a00000, v26
	v_add_f32_e32 v48, 1.0, v48
	v_add_f32_e32 v49, 1.0, v49
	v_add_f32_e32 v40, 1.0, v40
	v_add_f32_e32 v41, 1.0, v41
	v_rcp_f32_e32 v35, v35
	v_add_f32_e32 v36, 1.0, v36
	v_mul_f32_e32 v26, 0xbfb8aa3b, v26
	v_rcp_f32_e32 v48, v48
	v_rcp_f32_e32 v49, v49
	v_rcp_f32_e32 v40, v40
	v_rcp_f32_e32 v41, v41
	v_rcp_f32_e32 v36, v36
	v_exp_f32_e32 v26, v26
	v_fma_f32 v34, v120, v34, v125
	v_log_f32_e32 v37, v34
	v_fma_f32 v34, v118, v35, v126
	v_mul_f32_e32 v27, v27, v51
	v_fma_f32 v38, v153, v48, v128
	v_fma_f32 v39, v168, v49, v129
	v_fma_f32 v40, v121, v40, v130
	v_fma_f32 v41, v122, v41, v131
	v_log_f32_e32 v43, v34
	v_fma_f32 v34, v119, v36, v127
	v_add_f32_e32 v26, 1.0, v26
	v_max_f32_e32 v27, 0xc2a00000, v27
	v_log_f32_e32 v38, v38
	v_log_f32_e32 v39, v39
	v_log_f32_e32 v40, v40
	v_log_f32_e32 v41, v41
	v_log_f32_e32 v44, v34
	v_rcp_f32_e32 v26, v26
	v_mul_f32_e32 v27, 0xbfb8aa3b, v27
	v_exp_f32_e32 v27, v27
	v_mul_f32_e32 v32, v32, v51
	v_mul_f32_e32 v33, v33, v51
	v_max_f32_e32 v32, 0xc2a00000, v32
	v_max_f32_e32 v33, 0xc2a00000, v33
	v_cvt_pk_f16_f32 v34, v38, v39
	v_cvt_pk_f16_f32 v35, v40, v41
	v_cvt_pk_f16_f32 v36, v42, v37
	v_mul_f32_e32 v30, v30, v51
	v_mul_f32_e32 v31, v31, v51
	v_cvt_pk_f16_f32 v37, v43, v44
	v_mul_f32_e32 v32, 0xbfb8aa3b, v32
	v_mul_f32_e32 v33, 0xbfb8aa3b, v33
	v_fma_f32 v26, v171, v26, v132
	v_max_f32_e32 v30, 0xc2a00000, v30
	v_max_f32_e32 v31, 0xc2a00000, v31
	s_waitcnt lgkmcnt(5)
	v_subrev_u32_e32 v236, s82, v236
	global_store_dwordx4 v236, v[232:235], s[82:83] offset:64
	ds_bpermute_b32 v244, v250, v34
	ds_bpermute_b32 v245, v250, v35
	ds_bpermute_b32 v246, v250, v36
	ds_bpermute_b32 v247, v250, v37
	ds_bpermute_b32 v248, v250, v46
	v_exp_f32_e32 v32, v32
	v_exp_f32_e32 v33, v33
	v_log_f32_e32 v34, v26
	v_add_f32_e32 v26, 1.0, v27
	v_mul_f32_e32 v27, v28, v51
	v_mul_f32_e32 v30, 0xbfb8aa3b, v30
	v_mul_f32_e32 v31, 0xbfb8aa3b, v31
	v_max_f32_e32 v27, 0xc2a00000, v27
	v_mul_f32_e32 v28, v29, v51
	v_exp_f32_e32 v30, v30
	v_exp_f32_e32 v31, v31
	v_mul_f32_e32 v27, 0xbfb8aa3b, v27
	v_max_f32_e32 v28, 0xc2a00000, v28
	v_exp_f32_e32 v27, v27
	v_mul_f32_e32 v28, 0xbfb8aa3b, v28
	v_add_f32_e32 v32, 1.0, v32
	v_add_f32_e32 v33, 1.0, v33
	v_exp_f32_e32 v28, v28
	v_rcp_f32_e32 v32, v32
	v_rcp_f32_e32 v33, v33
	v_add_f32_e32 v30, 1.0, v30
	v_add_f32_e32 v31, 1.0, v31
	v_mul_f32_e32 v18, v18, v51
	v_rcp_f32_e32 v30, v30
	v_rcp_f32_e32 v31, v31
	v_rcp_f32_e32 v26, v26
	v_add_f32_e32 v27, 1.0, v27
	v_max_f32_e32 v18, 0xc2a00000, v18
	v_rcp_f32_e32 v27, v27
	v_add_f32_e32 v28, 1.0, v28
	v_mul_f32_e32 v18, 0xbfb8aa3b, v18
	v_fma_f32 v32, v178, v32, v138
	v_fma_f32 v33, v177, v33, v139
	v_rcp_f32_e32 v28, v28
	v_exp_f32_e32 v18, v18
	v_log_f32_e32 v32, v32
	v_log_f32_e32 v33, v33
	v_fma_f32 v30, v180, v30, v136
	v_fma_f32 v31, v179, v31, v137
	v_fma_f32 v26, v170, v26, v133
	v_mul_f32_e32 v22, v22, v51
	v_log_f32_e32 v30, v30
	v_log_f32_e32 v31, v31
	v_log_f32_e32 v29, v26
	v_fma_f32 v26, v169, v27, v134
	v_max_f32_e32 v22, 0xc2a00000, v22
	v_mul_f32_e32 v19, v19, v51
	v_log_f32_e32 v35, v26
	v_fma_f32 v26, v155, v28, v135
	v_mul_f32_e32 v22, 0xbfb8aa3b, v22
	v_add_f32_e32 v18, 1.0, v18
	v_max_f32_e32 v19, 0xc2a00000, v19
	v_log_f32_e32 v36, v26
	v_cvt_pk_f16_f32 v27, v32, v33
	v_exp_f32_e32 v32, v22
	v_mul_f32_e32 v22, v23, v51
	v_rcp_f32_e32 v18, v18
	v_mul_f32_e32 v19, 0xbfb8aa3b, v19
	s_mov_b64 s[14:15], 0xa0000
	v_max_f32_e32 v22, 0xc2a00000, v22
	v_exp_f32_e32 v19, v19
	v_cvt_pk_f16_f32 v26, v30, v31
	v_lshl_add_u64 v[30:31], v[166:167], 0, s[14:15]
	v_mul_f32_e32 v22, 0xbfb8aa3b, v22
	s_mov_b32 s14, 0xa0000
	v_exp_f32_e32 v33, v22
	v_add_co_u32_e32 v22, vcc, s14, v166
	v_cvt_pk_f16_f32 v28, v34, v29
	v_cvt_pk_f16_f32 v29, v35, v36
	v_addc_co_u32_e32 v23, vcc, 0, v167, vcc
	v_fma_f32 v18, v123, v18, v124
	s_waitcnt lgkmcnt(5)
	v_subrev_u32_e32 v242, s82, v242
	global_store_dwordx4 v242, v[238:241], s[82:83]
	ds_bpermute_b32 v232, v250, v26
	ds_bpermute_b32 v233, v250, v27
	ds_bpermute_b32 v234, v250, v28
	ds_bpermute_b32 v235, v250, v29
	ds_bpermute_b32 v236, v250, v22
	v_mul_f32_e32 v24, v24, v51
	v_mul_f32_e32 v25, v25, v51
	v_log_f32_e32 v26, v18
	v_add_f32_e32 v18, 1.0, v19
	v_mul_f32_e32 v19, v20, v51
	v_max_f32_e32 v19, 0xc2a00000, v19
	v_mul_f32_e32 v20, v21, v51
	ds_read_b32 v28, v176 offset:704
	v_max_f32_e32 v24, 0xc2a00000, v24
	v_max_f32_e32 v25, 0xc2a00000, v25
	v_mul_f32_e32 v19, 0xbfb8aa3b, v19
	v_max_f32_e32 v20, 0xc2a00000, v20
	v_mul_f32_e32 v24, 0xbfb8aa3b, v24
	v_mul_f32_e32 v25, 0xbfb8aa3b, v25
	v_exp_f32_e32 v19, v19
	v_mul_f32_e32 v20, 0xbfb8aa3b, v20
	v_exp_f32_e32 v24, v24
	v_exp_f32_e32 v25, v25
	v_exp_f32_e32 v20, v20
	s_waitcnt lgkmcnt(0)
	v_mul_f32_e32 v10, v10, v28
	v_rcp_f32_e32 v18, v18
	v_add_f32_e32 v19, 1.0, v19
	v_max_f32_e32 v10, 0xc2a00000, v10
	v_add_f32_e32 v32, 1.0, v32
	v_add_f32_e32 v33, 1.0, v33
	v_add_f32_e32 v24, 1.0, v24
	v_add_f32_e32 v25, 1.0, v25
	v_rcp_f32_e32 v19, v19
	v_add_f32_e32 v20, 1.0, v20
	v_mul_f32_e32 v10, 0xbfb8aa3b, v10
	v_rcp_f32_e32 v32, v32
	v_rcp_f32_e32 v33, v33
	v_rcp_f32_e32 v24, v24
	v_rcp_f32_e32 v25, v25
	v_rcp_f32_e32 v20, v20
	v_exp_f32_e32 v10, v10
	v_fma_f32 v18, v120, v18, v125
	v_log_f32_e32 v21, v18
	v_fma_f32 v18, v118, v19, v126
	v_mul_f32_e32 v11, v11, v28
	v_fma_f32 v22, v153, v32, v128
	v_fma_f32 v23, v168, v33, v129
	v_fma_f32 v24, v121, v24, v130
	v_fma_f32 v25, v122, v25, v131
	v_log_f32_e32 v27, v18
	v_fma_f32 v18, v119, v20, v127
	v_add_f32_e32 v10, 1.0, v10
	v_max_f32_e32 v11, 0xc2a00000, v11
	v_log_f32_e32 v22, v22
	v_log_f32_e32 v23, v23
	v_log_f32_e32 v24, v24
	v_log_f32_e32 v25, v25
	v_log_f32_e32 v29, v18
	v_rcp_f32_e32 v10, v10
	v_mul_f32_e32 v11, 0xbfb8aa3b, v11
	v_mul_f32_e32 v14, v14, v28
	v_mul_f32_e32 v15, v15, v28
	v_exp_f32_e32 v11, v11
	v_max_f32_e32 v14, 0xc2a00000, v14
	v_max_f32_e32 v15, 0xc2a00000, v15
	v_mul_f32_e32 v14, 0xbfb8aa3b, v14
	v_mul_f32_e32 v15, 0xbfb8aa3b, v15
	v_cvt_pk_f16_f32 v18, v22, v23
	v_cvt_pk_f16_f32 v19, v24, v25
	v_cvt_pk_f16_f32 v20, v26, v21
	v_exp_f32_e32 v14, v14
	v_exp_f32_e32 v15, v15
	v_cvt_pk_f16_f32 v21, v27, v29
	v_fma_f32 v10, v171, v10, v132
	s_waitcnt lgkmcnt(6)
	v_subrev_u32_e32 v248, s82, v248
	global_store_dwordx4 v248, v[244:247], s[82:83] offset:64
	ds_bpermute_b32 v238, v250, v18
	ds_bpermute_b32 v239, v250, v19
	ds_bpermute_b32 v240, v250, v20
	ds_bpermute_b32 v241, v250, v21
	ds_bpermute_b32 v242, v250, v30
	v_add_f32_e32 v14, 1.0, v14
	v_add_f32_e32 v15, 1.0, v15
	v_log_f32_e32 v18, v10
	v_add_f32_e32 v10, 1.0, v11
	v_mul_f32_e32 v11, v12, v28
	v_max_f32_e32 v11, 0xc2a00000, v11
	v_mul_f32_e32 v11, 0xbfb8aa3b, v11
	v_exp_f32_e32 v11, v11
	v_rcp_f32_e32 v14, v14
	v_rcp_f32_e32 v15, v15
	v_mul_f32_e32 v16, v16, v28
	v_mul_f32_e32 v17, v17, v28
	v_rcp_f32_e32 v10, v10
	v_mul_f32_e32 v12, v13, v28
	v_add_f32_e32 v11, 1.0, v11
	v_fma_f32 v14, v180, v14, v136
	v_fma_f32 v15, v179, v15, v137
	v_max_f32_e32 v16, 0xc2a00000, v16
	v_max_f32_e32 v17, 0xc2a00000, v17
	v_max_f32_e32 v12, 0xc2a00000, v12
	v_rcp_f32_e32 v11, v11
	v_log_f32_e32 v14, v14
	v_mul_f32_e32 v16, 0xbfb8aa3b, v16
	v_mul_f32_e32 v17, 0xbfb8aa3b, v17
	v_log_f32_e32 v15, v15
	v_mul_f32_e32 v12, 0xbfb8aa3b, v12
	v_exp_f32_e32 v16, v16
	v_exp_f32_e32 v17, v17
	v_exp_f32_e32 v12, v12
	v_mul_f32_e32 v6, v6, v28
	v_fma_f32 v10, v170, v10, v133
	v_max_f32_e32 v6, 0xc2a00000, v6
	v_log_f32_e32 v13, v10
	v_fma_f32 v10, v169, v11, v134
	v_mul_f32_e32 v6, 0xbfb8aa3b, v6
	v_log_f32_e32 v19, v10
	v_cvt_pk_f16_f32 v10, v14, v15
	v_exp_f32_e32 v14, v6
	v_mul_f32_e32 v6, v7, v28
	v_mul_f32_e32 v8, v8, v28
	v_mul_f32_e32 v9, v9, v28
	v_mul_f32_e32 v2, v2, v28
	v_mul_f32_e32 v3, v3, v28
	v_mul_f32_e32 v4, v4, v28
	v_mul_f32_e32 v5, v5, v28
	v_add_f32_e32 v16, 1.0, v16
	v_add_f32_e32 v17, 1.0, v17
	v_add_f32_e32 v12, 1.0, v12
	v_max_f32_e32 v6, 0xc2a00000, v6
	v_max_f32_e32 v8, 0xc2a00000, v8
	v_max_f32_e32 v9, 0xc2a00000, v9
	v_max_f32_e32 v2, 0xc2a00000, v2
	v_max_f32_e32 v3, 0xc2a00000, v3
	v_max_f32_e32 v4, 0xc2a00000, v4
	v_max_f32_e32 v5, 0xc2a00000, v5
	v_rcp_f32_e32 v16, v16
	v_rcp_f32_e32 v17, v17
	v_rcp_f32_e32 v12, v12
	v_mul_f32_e32 v6, 0xbfb8aa3b, v6
	v_mul_f32_e32 v8, 0xbfb8aa3b, v8
	v_mul_f32_e32 v9, 0xbfb8aa3b, v9
	v_mul_f32_e32 v2, 0xbfb8aa3b, v2
	v_mul_f32_e32 v3, 0xbfb8aa3b, v3
	v_mul_f32_e32 v4, 0xbfb8aa3b, v4
	v_mul_f32_e32 v5, 0xbfb8aa3b, v5
	v_exp_f32_e32 v15, v6
	v_exp_f32_e32 v8, v8
	v_exp_f32_e32 v9, v9
	v_exp_f32_e32 v2, v2
	v_exp_f32_e32 v3, v3
	v_exp_f32_e32 v4, v4
	v_exp_f32_e32 v5, v5
	v_fma_f32 v16, v178, v16, v138
	v_fmac_f32_e32 v139, v177, v17
	v_fmac_f32_e32 v135, v155, v12
	v_log_f32_e32 v16, v16
	v_log_f32_e32 v17, v139
	v_log_f32_e32 v20, v135
	v_add_f32_e32 v14, 1.0, v14
	v_add_f32_e32 v15, 1.0, v15
	v_add_f32_e32 v8, 1.0, v8
	v_add_f32_e32 v9, 1.0, v9
	v_add_f32_e32 v2, 1.0, v2
	v_add_f32_e32 v3, 1.0, v3
	v_add_f32_e32 v4, 1.0, v4
	v_add_f32_e32 v5, 1.0, v5
	s_mov_b64 s[14:15], 0xb0000
	v_rcp_f32_e32 v14, v14
	v_rcp_f32_e32 v15, v15
	v_rcp_f32_e32 v8, v8
	v_rcp_f32_e32 v9, v9
	v_rcp_f32_e32 v2, v2
	v_rcp_f32_e32 v3, v3
	v_rcp_f32_e32 v4, v4
	v_rcp_f32_e32 v5, v5
	v_lshl_add_u64 v[136:137], v[166:167], 0, s[14:15]
	s_mov_b32 s14, 0xb0000
	v_add_co_u32_e32 v6, vcc, s14, v166
	v_cvt_pk_f16_f32 v11, v16, v17
	v_cvt_pk_f16_f32 v12, v18, v13
	v_cvt_pk_f16_f32 v13, v19, v20
	v_addc_co_u32_e32 v7, vcc, 0, v167, vcc
	s_waitcnt lgkmcnt(6)
	v_subrev_u32_e32 v236, s82, v236
	global_store_dwordx4 v236, v[232:235], s[82:83]
	ds_bpermute_b32 v244, v250, v10
	ds_bpermute_b32 v245, v250, v11
	ds_bpermute_b32 v246, v250, v12
	ds_bpermute_b32 v247, v250, v13
	ds_bpermute_b32 v248, v250, v6
	v_fma_f32 v6, v153, v14, v128
	v_fma_f32 v7, v168, v15, v129
	v_fma_f32 v8, v121, v8, v130
	v_fmac_f32_e32 v131, v122, v9
	v_fma_f32 v2, v123, v2, v124
	v_fma_f32 v3, v120, v3, v125
	v_fma_f32 v4, v118, v4, v126
	v_fmac_f32_e32 v127, v119, v5
	v_log_f32_e32 v6, v6
	v_log_f32_e32 v7, v7
	v_log_f32_e32 v8, v8
	v_log_f32_e32 v9, v131
	v_log_f32_e32 v2, v2
	v_log_f32_e32 v3, v3
	v_log_f32_e32 v4, v4
	v_log_f32_e32 v5, v127
	v_cvt_pk_f16_f32 v196, v181, v182
	v_cvt_pk_f16_f32 v132, v6, v7
	v_cvt_pk_f16_f32 v133, v8, v9
	v_cvt_pk_f16_f32 v134, v2, v3
	v_cvt_pk_f16_f32 v135, v4, v5
	s_waitcnt lgkmcnt(5)
	v_subrev_u32_e32 v242, s82, v242
	global_store_dwordx4 v242, v[238:241], s[82:83] offset:64
	ds_bpermute_b32 v232, v250, v194
	ds_bpermute_b32 v233, v250, v195
	ds_bpermute_b32 v234, v250, v196
	ds_bpermute_b32 v235, v250, v197
	ds_bpermute_b32 v236, v250, v166
	s_andn2_b64 vcc, exec, s[38:39]
	s_mov_b64 s[28:29], -1
	s_waitcnt lgkmcnt(5)
	v_subrev_u32_e32 v248, s82, v248
	global_store_dwordx4 v248, v[244:247], s[82:83]
	ds_bpermute_b32 v238, v250, v132
	ds_bpermute_b32 v239, v250, v133
	ds_bpermute_b32 v240, v250, v134
	ds_bpermute_b32 v241, v250, v135
	ds_bpermute_b32 v242, v250, v136
	s_waitcnt lgkmcnt(5)
	v_subrev_u32_e32 v236, s82, v236
	global_store_dwordx4 v236, v[232:235], s[82:83] offset:64
	s_waitcnt lgkmcnt(0)
	v_subrev_u32_e32 v242, s82, v242
	global_store_dwordx4 v242, v[238:241], s[82:83] offset:64
	s_cbranch_vccnz .LBB0_495

.LBB0_1082:
	v_mbcnt_lo_u32_b32 v250, -1, 0
	v_mbcnt_hi_u32_b32 v250, -1, v250
	v_lshrrev_b32_e32 v251, 2, v250
	v_and_b32_e32 v250, 3, v250
	v_lshl_add_u32 v250, v250, 4, v251
	v_lshlrev_b32_e32 v250, 2, v250
	v_pk_mul_f32 v[148:149], v[118:119], v[118:119]
	v_pk_mul_f32 v[150:151], v[126:127], v[126:127]
	v_pk_fma_f32 v[148:149], v[116:117], v[116:117], v[148:149]
	v_pk_fma_f32 v[150:151], v[124:125], v[124:125], v[150:151]
	v_lshl_add_u32 v144, s46, 8, v1
	v_pk_add_f32 v[152:153], v[148:149], v[150:151]
	v_cvt_pk_bf16_f32 v149, v118, v119
	v_cvt_pk_bf16_f32 v150, v124, v125
	v_pk_mul_f32 v[118:119], v[122:123], v[122:123]
	v_pk_mul_f32 v[124:125], v[130:131], v[130:131]
	v_pk_fma_f32 v[118:119], v[120:121], v[120:121], v[118:119]
	v_pk_fma_f32 v[124:125], v[128:129], v[128:129], v[124:125]
	s_lshl_b32 s16, s46, 5
	v_pk_add_f32 v[118:119], v[118:119], v[124:125]
	s_lshl_b32 s46, s48, 2
	v_pk_add_f32 v[124:125], v[152:153], v[118:119]
	s_or_b32 s17, s46, s12
	v_add_f32_e32 v124, v124, v125
	ds_swizzle_b32 v125, v124 offset:swizzle(SWAP,16)
	s_add_i32 s16, s17, s16
	s_ashr_i32 s17, s16, 31
	s_lshl_b64 s[16:17], s[16:17], 15
	v_cvt_pk_bf16_f32 v148, v116, v117
	v_lshl_add_u64 v[116:117], v[138:139], 0, s[16:17]
	v_cvt_pk_bf16_f32 v118, v120, v121
	v_cvt_pk_bf16_f32 v119, v122, v123
	v_cvt_pk_bf16_f32 v120, v128, v129
	v_cvt_pk_bf16_f32 v121, v130, v131
	ds_bpermute_b32 v232, v250, v118
	ds_bpermute_b32 v233, v250, v119
	ds_bpermute_b32 v234, v250, v120
	ds_bpermute_b32 v235, v250, v121
	ds_bpermute_b32 v236, v250, v116
	s_ashr_i32 s47, s46, 31
	v_cvt_pk_bf16_f32 v151, v126, v127
	ds_bpermute_b32 v238, v250, v148
	ds_bpermute_b32 v239, v250, v149
	ds_bpermute_b32 v240, v250, v150
	ds_bpermute_b32 v241, v250, v151
	ds_bpermute_b32 v242, v250, v116
	s_waitcnt lgkmcnt(0)
	v_add_f32_e32 v118, v124, v125
	v_mov_b32_e32 v119, v118
	s_nop 1
	v_permlane32_swap_b32_e32 v118, v119
	s_waitcnt lgkmcnt(5)
	v_subrev_u32_e32 v236, s82, v236
	global_store_dwordx4 v236, v[232:235], s[82:83] offset:64
	s_waitcnt lgkmcnt(0)
	v_subrev_u32_e32 v242, s82, v242
	global_store_dwordx4 v242, v[238:241], s[82:83]
	s_and_saveexec_b64 s[48:49], s[38:39]
	s_cbranch_execz .LBB0_1084
	v_ashrrev_i32_e32 v145, 31, v144
	v_add_f32_e32 v120, v118, v119
	v_lshlrev_b64 v[118:119], 7, v[144:145]
	v_lshl_add_u64 v[118:119], s[8:9], 0, v[118:119]
	v_lshl_add_u64 v[118:119], s[46:47], 2, v[118:119]
	s_lshl_b32 s24, s12, 2
	v_lshl_add_u64 v[118:119], v[118:119], 0, s[24:25]
	global_store_dword v[118:119], v120, off
.LBB0_1084:
	s_or_b64 exec, exec, s[48:49]
	v_pk_mul_f32 v[118:119], v[100:101], v[100:101]
	v_pk_mul_f32 v[120:121], v[104:105], v[104:105]
	v_pk_fma_f32 v[118:119], v[98:99], v[98:99], v[118:119]
	v_cvt_pk_bf16_f32 v98, v98, v99
	v_cvt_pk_bf16_f32 v99, v100, v101
	v_cvt_pk_bf16_f32 v100, v102, v103
	v_cvt_pk_bf16_f32 v101, v104, v105
	ds_bpermute_b32 v244, v250, v98
	ds_bpermute_b32 v245, v250, v99
	ds_bpermute_b32 v246, v250, v100
	ds_bpermute_b32 v247, v250, v101
	ds_bpermute_b32 v248, v250, v116
	v_pk_fma_f32 v[120:121], v[102:103], v[102:103], v[120:121]
	s_nop 0
	v_pk_mul_f32 v[98:99], v[108:109], v[108:109]
	v_pk_mul_f32 v[100:101], v[112:113], v[112:113]
	v_pk_fma_f32 v[98:99], v[106:107], v[106:107], v[98:99]
	v_pk_fma_f32 v[100:101], v[110:111], v[110:111], v[100:101]
	v_pk_add_f32 v[118:119], v[118:119], v[120:121]
	v_pk_add_f32 v[98:99], v[98:99], v[100:101]
	s_nop 0
	v_pk_add_f32 v[100:101], v[118:119], v[98:99]
	v_cvt_pk_bf16_f32 v98, v106, v107
	v_cvt_pk_bf16_f32 v99, v108, v109
	s_nop 0
	v_add_f32_e32 v102, v100, v101
	ds_swizzle_b32 v103, v102 offset:swizzle(SWAP,16)
	v_cvt_pk_bf16_f32 v100, v110, v111
	v_cvt_pk_bf16_f32 v101, v112, v113
	ds_bpermute_b32 v232, v250, v98
	ds_bpermute_b32 v233, v250, v99
	ds_bpermute_b32 v234, v250, v100
	ds_bpermute_b32 v235, v250, v101
	ds_bpermute_b32 v236, v250, v116
	s_waitcnt lgkmcnt(0)
	s_nop 0
	v_add_f32_e32 v98, v102, v103
	v_mov_b32_e32 v99, v98
	s_nop 1
	v_permlane32_swap_b32_e32 v98, v99
	s_waitcnt lgkmcnt(6)
	v_subrev_u32_e32 v248, s82, v248
	global_store_dwordx4 v248, v[244:247], s[82:83] offset:2048
	s_waitcnt lgkmcnt(0)
	v_subrev_u32_e32 v236, s82, v236
	global_store_dwordx4 v236, v[232:235], s[82:83] offset:2112
	s_and_saveexec_b64 s[48:49], s[38:39]
	s_cbranch_execz .LBB0_1086
	v_or_b32_e32 v100, 16, v144
	v_ashrrev_i32_e32 v101, 31, v100
	v_add_f32_e32 v102, v98, v99
	v_lshlrev_b64 v[98:99], 7, v[100:101]
	v_lshl_add_u64 v[98:99], s[8:9], 0, v[98:99]
	v_lshl_add_u64 v[98:99], s[46:47], 2, v[98:99]
	s_lshl_b32 s24, s12, 2
	v_lshl_add_u64 v[98:99], v[98:99], 0, s[24:25]
	global_store_dword v[98:99], v102, off
.LBB0_1086:
	s_or_b64 exec, exec, s[48:49]
	v_pk_mul_f32 v[98:99], v[84:85], v[84:85]
	v_pk_mul_f32 v[100:101], v[92:93], v[92:93]
	v_pk_fma_f32 v[98:99], v[82:83], v[82:83], v[98:99]
	v_pk_fma_f32 v[100:101], v[90:91], v[90:91], v[100:101]
	s_nop 0
	v_pk_add_f32 v[102:103], v[98:99], v[100:101]
	v_cvt_pk_bf16_f32 v99, v84, v85
	v_cvt_pk_bf16_f32 v100, v90, v91
	v_pk_mul_f32 v[84:85], v[88:89], v[88:89]
	v_pk_mul_f32 v[90:91], v[96:97], v[96:97]
	v_pk_fma_f32 v[84:85], v[86:87], v[86:87], v[84:85]
	v_pk_fma_f32 v[90:91], v[94:95], v[94:95], v[90:91]
	v_cvt_pk_bf16_f32 v98, v82, v83
	v_add_co_u32_e32 v82, vcc, s73, v116
	v_pk_add_f32 v[84:85], v[84:85], v[90:91]
	s_nop 0
	v_addc_co_u32_e32 v83, vcc, 0, v117, vcc
	v_pk_add_f32 v[90:91], v[102:103], v[84:85]
	v_cvt_pk_bf16_f32 v84, v86, v87
	v_cvt_pk_bf16_f32 v85, v88, v89
	v_cvt_pk_bf16_f32 v86, v94, v95
	v_cvt_pk_bf16_f32 v87, v96, v97
	ds_bpermute_b32 v238, v250, v84
	ds_bpermute_b32 v239, v250, v85
	ds_bpermute_b32 v240, v250, v86
	ds_bpermute_b32 v241, v250, v87
	ds_bpermute_b32 v242, v250, v82
	v_add_f32_e32 v90, v90, v91
	ds_swizzle_b32 v91, v90 offset:swizzle(SWAP,16)
	v_cvt_pk_bf16_f32 v101, v92, v93
	ds_bpermute_b32 v244, v250, v98
	ds_bpermute_b32 v245, v250, v99
	ds_bpermute_b32 v246, v250, v100
	ds_bpermute_b32 v247, v250, v101
	ds_bpermute_b32 v248, v250, v82
	s_waitcnt lgkmcnt(0)
	v_add_f32_e32 v84, v90, v91
	v_mov_b32_e32 v85, v84
	s_nop 1
	v_permlane32_swap_b32_e32 v84, v85
	s_waitcnt lgkmcnt(6)
	v_subrev_u32_e32 v242, s82, v242
	global_store_dwordx4 v242, v[238:241], s[82:83] offset:64
	s_waitcnt lgkmcnt(0)
	v_subrev_u32_e32 v248, s82, v248
	global_store_dwordx4 v248, v[244:247], s[82:83]
	s_and_saveexec_b64 s[48:49], s[38:39]
	s_cbranch_execz .LBB0_1088
	v_or_b32_e32 v86, 32, v144
	v_ashrrev_i32_e32 v87, 31, v86
	v_add_f32_e32 v88, v84, v85
	v_lshlrev_b64 v[84:85], 7, v[86:87]
	v_lshl_add_u64 v[84:85], s[8:9], 0, v[84:85]
	v_lshl_add_u64 v[84:85], s[46:47], 2, v[84:85]
	s_lshl_b32 s24, s12, 2
	v_lshl_add_u64 v[84:85], v[84:85], 0, s[24:25]
	global_store_dword v[84:85], v88, off
.LBB0_1088:
	s_or_b64 exec, exec, s[48:49]
	v_pk_mul_f32 v[84:85], v[60:61], v[60:61]
	v_pk_mul_f32 v[86:87], v[72:73], v[72:73]
	v_pk_fma_f32 v[84:85], v[58:59], v[58:59], v[84:85]
	v_cvt_pk_bf16_f32 v58, v58, v59
	v_cvt_pk_bf16_f32 v59, v60, v61
	v_cvt_pk_bf16_f32 v60, v70, v71
	v_cvt_pk_bf16_f32 v61, v72, v73
	ds_bpermute_b32 v232, v250, v58
	ds_bpermute_b32 v233, v250, v59
	ds_bpermute_b32 v234, v250, v60
	ds_bpermute_b32 v235, v250, v61
	ds_bpermute_b32 v236, v250, v82
	v_pk_fma_f32 v[86:87], v[70:71], v[70:71], v[86:87]
	s_nop 0
	v_pk_mul_f32 v[58:59], v[76:77], v[76:77]
	v_pk_mul_f32 v[60:61], v[80:81], v[80:81]
	v_pk_fma_f32 v[58:59], v[74:75], v[74:75], v[58:59]
	v_pk_fma_f32 v[60:61], v[78:79], v[78:79], v[60:61]
	v_pk_add_f32 v[84:85], v[84:85], v[86:87]
	v_pk_add_f32 v[58:59], v[58:59], v[60:61]
	s_nop 0
	v_pk_add_f32 v[60:61], v[84:85], v[58:59]
	v_cvt_pk_bf16_f32 v58, v74, v75
	v_cvt_pk_bf16_f32 v59, v76, v77
	s_nop 0
	v_add_f32_e32 v70, v60, v61
	ds_swizzle_b32 v71, v70 offset:swizzle(SWAP,16)
	v_cvt_pk_bf16_f32 v60, v78, v79
	v_cvt_pk_bf16_f32 v61, v80, v81
	ds_bpermute_b32 v238, v250, v58
	ds_bpermute_b32 v239, v250, v59
	ds_bpermute_b32 v240, v250, v60
	ds_bpermute_b32 v241, v250, v61
	ds_bpermute_b32 v242, v250, v82
	s_waitcnt lgkmcnt(0)
	s_nop 0
	v_add_f32_e32 v58, v70, v71
	v_mov_b32_e32 v59, v58
	s_nop 1
	v_permlane32_swap_b32_e32 v58, v59
	s_waitcnt lgkmcnt(6)
	v_subrev_u32_e32 v236, s82, v236
	global_store_dwordx4 v236, v[232:235], s[82:83] offset:2048
	s_waitcnt lgkmcnt(0)
	v_subrev_u32_e32 v242, s82, v242
	global_store_dwordx4 v242, v[238:241], s[82:83] offset:2112
	s_and_saveexec_b64 s[48:49], s[38:39]
	s_cbranch_execz .LBB0_1090
	v_or_b32_e32 v60, 48, v144
	v_ashrrev_i32_e32 v61, 31, v60
	v_add_f32_e32 v70, v58, v59
	v_lshlrev_b64 v[58:59], 7, v[60:61]
	v_lshl_add_u64 v[58:59], s[8:9], 0, v[58:59]
	v_lshl_add_u64 v[58:59], s[46:47], 2, v[58:59]
	s_lshl_b32 s24, s12, 2
	v_lshl_add_u64 v[58:59], v[58:59], 0, s[24:25]
	global_store_dword v[58:59], v70, off
.LBB0_1090:
	s_or_b64 exec, exec, s[48:49]
	v_pk_mul_f32 v[58:59], v[52:53], v[52:53]
	v_pk_mul_f32 v[60:61], v[64:65], v[64:65]
	v_pk_fma_f32 v[58:59], v[50:51], v[50:51], v[58:59]
	v_pk_fma_f32 v[60:61], v[62:63], v[62:63], v[60:61]
	s_nop 0
	v_pk_add_f32 v[70:71], v[58:59], v[60:61]
	v_cvt_pk_bf16_f32 v58, v50, v51
	v_add_co_u32_e32 v50, vcc, s72, v116
	v_cvt_pk_bf16_f32 v59, v52, v53
	v_cvt_pk_bf16_f32 v60, v62, v63
	v_cvt_pk_bf16_f32 v61, v64, v65
	v_pk_mul_f32 v[52:53], v[56:57], v[56:57]
	s_nop 0
	v_addc_co_u32_e32 v51, vcc, 0, v117, vcc
	ds_bpermute_b32 v244, v250, v58
	ds_bpermute_b32 v245, v250, v59
	ds_bpermute_b32 v246, v250, v60
	ds_bpermute_b32 v247, v250, v61
	ds_bpermute_b32 v248, v250, v50
	v_pk_fma_f32 v[52:53], v[54:55], v[54:55], v[52:53]
	s_nop 0
	v_pk_mul_f32 v[58:59], v[68:69], v[68:69]
	s_nop 0
	v_pk_fma_f32 v[58:59], v[66:67], v[66:67], v[58:59]
	s_nop 0
	v_pk_add_f32 v[52:53], v[52:53], v[58:59]
	s_nop 0
	v_pk_add_f32 v[58:59], v[70:71], v[52:53]
	v_cvt_pk_bf16_f32 v52, v54, v55
	v_cvt_pk_bf16_f32 v53, v56, v57
	v_cvt_pk_bf16_f32 v54, v66, v67
	v_cvt_pk_bf16_f32 v55, v68, v69
	ds_bpermute_b32 v232, v250, v52
	ds_bpermute_b32 v233, v250, v53
	ds_bpermute_b32 v234, v250, v54
	ds_bpermute_b32 v235, v250, v55
	ds_bpermute_b32 v236, v250, v50
	v_add_f32_e32 v58, v58, v59
	ds_swizzle_b32 v59, v58 offset:swizzle(SWAP,16)
	s_waitcnt lgkmcnt(0)
	v_add_f32_e32 v52, v58, v59
	v_mov_b32_e32 v53, v52
	s_nop 1
	v_permlane32_swap_b32_e32 v52, v53
	s_waitcnt lgkmcnt(6)
	v_subrev_u32_e32 v248, s82, v248
	global_store_dwordx4 v248, v[244:247], s[82:83]
	s_waitcnt lgkmcnt(1)
	v_subrev_u32_e32 v236, s82, v236
	global_store_dwordx4 v236, v[232:235], s[82:83] offset:64
	s_and_saveexec_b64 s[48:49], s[38:39]
	s_cbranch_execz .LBB0_1092
	v_ashrrev_i32_e32 v145, 31, v144
	v_add_f32_e32 v54, v52, v53
	v_lshlrev_b64 v[52:53], 7, v[144:145]
	v_lshl_add_u64 v[52:53], s[8:9], 0, v[52:53]
	v_lshl_add_u64 v[52:53], s[46:47], 2, v[52:53]
	s_lshl_b32 s24, s12, 2
	v_lshl_add_u64 v[52:53], v[52:53], 0, s[24:25]
	v_add_co_u32_e32 v52, vcc, 0x4000, v52
	s_nop 1
	v_addc_co_u32_e32 v53, vcc, 0, v53, vcc
	global_store_dword v[52:53], v54, off
.LBB0_1092:
	s_or_b64 exec, exec, s[48:49]
	v_pk_mul_f32 v[52:53], v[36:37], v[36:37]
	v_pk_mul_f32 v[54:55], v[40:41], v[40:41]
	v_pk_fma_f32 v[52:53], v[34:35], v[34:35], v[52:53]
	v_cvt_pk_bf16_f32 v34, v34, v35
	v_cvt_pk_bf16_f32 v35, v36, v37
	v_cvt_pk_bf16_f32 v36, v38, v39
	v_cvt_pk_bf16_f32 v37, v40, v41
	ds_bpermute_b32 v238, v250, v34
	ds_bpermute_b32 v239, v250, v35
	ds_bpermute_b32 v240, v250, v36
	ds_bpermute_b32 v241, v250, v37
	ds_bpermute_b32 v242, v250, v50
	v_pk_fma_f32 v[54:55], v[38:39], v[38:39], v[54:55]
	s_nop 0
	v_pk_mul_f32 v[34:35], v[44:45], v[44:45]
	v_pk_mul_f32 v[36:37], v[48:49], v[48:49]
	v_pk_fma_f32 v[34:35], v[42:43], v[42:43], v[34:35]
	v_pk_fma_f32 v[36:37], v[46:47], v[46:47], v[36:37]
	v_pk_add_f32 v[52:53], v[52:53], v[54:55]
	v_pk_add_f32 v[34:35], v[34:35], v[36:37]
	s_nop 0
	v_pk_add_f32 v[36:37], v[52:53], v[34:35]
	v_cvt_pk_bf16_f32 v34, v42, v43
	v_cvt_pk_bf16_f32 v35, v44, v45
	s_nop 0
	v_add_f32_e32 v38, v36, v37
	ds_swizzle_b32 v39, v38 offset:swizzle(SWAP,16)
	v_cvt_pk_bf16_f32 v36, v46, v47
	v_cvt_pk_bf16_f32 v37, v48, v49
	ds_bpermute_b32 v244, v250, v34
	ds_bpermute_b32 v245, v250, v35
	ds_bpermute_b32 v246, v250, v36
	ds_bpermute_b32 v247, v250, v37
	ds_bpermute_b32 v248, v250, v50
	s_waitcnt lgkmcnt(0)
	s_nop 0
	v_add_f32_e32 v34, v38, v39
	v_mov_b32_e32 v35, v34
	s_nop 1
	v_permlane32_swap_b32_e32 v34, v35
	s_waitcnt lgkmcnt(6)
	v_subrev_u32_e32 v242, s82, v242
	global_store_dwordx4 v242, v[238:241], s[82:83] offset:2048
	s_waitcnt lgkmcnt(0)
	v_subrev_u32_e32 v248, s82, v248
	global_store_dwordx4 v248, v[244:247], s[82:83] offset:2112
	s_and_saveexec_b64 s[48:49], s[38:39]
	s_cbranch_execz .LBB0_1094
	v_ashrrev_i32_e32 v145, 31, v144
	v_add_f32_e32 v36, v34, v35
	v_lshlrev_b64 v[34:35], 7, v[144:145]
	v_lshl_add_u64 v[34:35], s[8:9], 0, v[34:35]
	v_lshl_add_u64 v[34:35], s[46:47], 2, v[34:35]
	s_lshl_b32 s24, s12, 2
	v_lshl_add_u64 v[34:35], v[34:35], 0, s[24:25]
	v_add_co_u32_e32 v34, vcc, 0x4000, v34
	s_nop 1
	v_addc_co_u32_e32 v35, vcc, 0, v35, vcc
	global_store_dword v[34:35], v36, off offset:2048
.LBB0_1094:
	s_or_b64 exec, exec, s[48:49]
	v_pk_mul_f32 v[34:35], v[20:21], v[20:21]
	v_pk_mul_f32 v[36:37], v[28:29], v[28:29]
	v_pk_fma_f32 v[34:35], v[18:19], v[18:19], v[34:35]
	v_pk_fma_f32 v[36:37], v[26:27], v[26:27], v[36:37]
	s_nop 0
	v_pk_add_f32 v[38:39], v[34:35], v[36:37]
	v_cvt_pk_bf16_f32 v35, v20, v21
	v_cvt_pk_bf16_f32 v36, v26, v27
	v_pk_mul_f32 v[20:21], v[24:25], v[24:25]
	v_pk_mul_f32 v[26:27], v[32:33], v[32:33]
	v_pk_fma_f32 v[20:21], v[22:23], v[22:23], v[20:21]
	v_pk_fma_f32 v[26:27], v[30:31], v[30:31], v[26:27]
	v_cvt_pk_bf16_f32 v34, v18, v19
	v_add_co_u32_e32 v18, vcc, s31, v116
	v_pk_add_f32 v[20:21], v[20:21], v[26:27]
	s_nop 0
	v_addc_co_u32_e32 v19, vcc, 0, v117, vcc
	v_pk_add_f32 v[26:27], v[38:39], v[20:21]
	v_cvt_pk_bf16_f32 v20, v22, v23
	v_cvt_pk_bf16_f32 v21, v24, v25
	v_cvt_pk_bf16_f32 v22, v30, v31
	v_cvt_pk_bf16_f32 v23, v32, v33
	ds_bpermute_b32 v232, v250, v20
	ds_bpermute_b32 v233, v250, v21
	ds_bpermute_b32 v234, v250, v22
	ds_bpermute_b32 v235, v250, v23
	ds_bpermute_b32 v236, v250, v18
	v_add_f32_e32 v26, v26, v27
	ds_swizzle_b32 v27, v26 offset:swizzle(SWAP,16)
	v_cvt_pk_bf16_f32 v37, v28, v29
	ds_bpermute_b32 v238, v250, v34
	ds_bpermute_b32 v239, v250, v35
	ds_bpermute_b32 v240, v250, v36
	ds_bpermute_b32 v241, v250, v37
	ds_bpermute_b32 v242, v250, v18
	s_waitcnt lgkmcnt(0)
	v_add_f32_e32 v20, v26, v27
	v_mov_b32_e32 v21, v20
	s_nop 1
	v_permlane32_swap_b32_e32 v20, v21
	s_waitcnt lgkmcnt(6)
	v_subrev_u32_e32 v236, s82, v236
	global_store_dwordx4 v236, v[232:235], s[82:83] offset:64
	s_waitcnt lgkmcnt(0)
	v_subrev_u32_e32 v242, s82, v242
	global_store_dwordx4 v242, v[238:241], s[82:83]
	s_and_saveexec_b64 s[48:49], s[38:39]
	s_cbranch_execz .LBB0_1096
	v_ashrrev_i32_e32 v145, 31, v144
	v_add_f32_e32 v22, v20, v21
	v_lshlrev_b64 v[20:21], 7, v[144:145]
	v_lshl_add_u64 v[20:21], s[8:9], 0, v[20:21]
	v_lshl_add_u64 v[20:21], s[46:47], 2, v[20:21]
	s_lshl_b32 s24, s12, 2
	v_lshl_add_u64 v[20:21], v[20:21], 0, s[24:25]
	v_add_co_u32_e32 v20, vcc, 0x5000, v20
	s_nop 1
	v_addc_co_u32_e32 v21, vcc, 0, v21, vcc
	global_store_dword v[20:21], v22, off
.LBB0_1096:
	s_or_b64 exec, exec, s[48:49]
	v_pk_mul_f32 v[20:21], v[4:5], v[4:5]
	v_pk_mul_f32 v[22:23], v[8:9], v[8:9]
	v_pk_fma_f32 v[20:21], v[2:3], v[2:3], v[20:21]
	v_cvt_pk_bf16_f32 v2, v2, v3
	v_cvt_pk_bf16_f32 v3, v4, v5
	v_cvt_pk_bf16_f32 v4, v6, v7
	v_cvt_pk_bf16_f32 v5, v8, v9
	ds_bpermute_b32 v244, v250, v2
	ds_bpermute_b32 v245, v250, v3
	ds_bpermute_b32 v246, v250, v4
	ds_bpermute_b32 v247, v250, v5
	ds_bpermute_b32 v248, v250, v18
	v_pk_fma_f32 v[22:23], v[6:7], v[6:7], v[22:23]
	s_nop 0
	v_pk_mul_f32 v[2:3], v[12:13], v[12:13]
	v_pk_mul_f32 v[4:5], v[16:17], v[16:17]
	v_pk_fma_f32 v[2:3], v[10:11], v[10:11], v[2:3]
	v_pk_fma_f32 v[4:5], v[14:15], v[14:15], v[4:5]
	v_pk_add_f32 v[20:21], v[20:21], v[22:23]
	v_pk_add_f32 v[2:3], v[2:3], v[4:5]
	s_nop 0
	v_pk_add_f32 v[4:5], v[20:21], v[2:3]
	v_cvt_pk_bf16_f32 v2, v10, v11
	v_cvt_pk_bf16_f32 v3, v12, v13
	s_nop 0
	v_add_f32_e32 v6, v4, v5
	ds_swizzle_b32 v7, v6 offset:swizzle(SWAP,16)
	v_cvt_pk_bf16_f32 v4, v14, v15
	v_cvt_pk_bf16_f32 v5, v16, v17
	ds_bpermute_b32 v232, v250, v2
	ds_bpermute_b32 v233, v250, v3
	ds_bpermute_b32 v234, v250, v4
	ds_bpermute_b32 v235, v250, v5
	ds_bpermute_b32 v236, v250, v18
	s_waitcnt lgkmcnt(0)
	s_nop 0
	v_add_f32_e32 v2, v6, v7
	v_mov_b32_e32 v3, v2
	s_nop 1
	v_permlane32_swap_b32_e32 v2, v3
	s_waitcnt lgkmcnt(6)
	v_subrev_u32_e32 v248, s82, v248
	global_store_dwordx4 v248, v[244:247], s[82:83] offset:2048
	s_waitcnt lgkmcnt(0)
	v_subrev_u32_e32 v236, s82, v236
	global_store_dwordx4 v236, v[232:235], s[82:83] offset:2112
	s_and_saveexec_b64 s[48:49], s[38:39]
	s_cbranch_execz .LBB0_1098
	v_ashrrev_i32_e32 v145, 31, v144
	v_add_f32_e32 v4, v2, v3
	v_lshlrev_b64 v[2:3], 7, v[144:145]
	v_lshl_add_u64 v[2:3], s[8:9], 0, v[2:3]
	v_lshl_add_u64 v[2:3], s[46:47], 2, v[2:3]
	s_lshl_b32 s24, s12, 2
	v_lshl_add_u64 v[2:3], v[2:3], 0, s[24:25]
	v_add_co_u32_e32 v2, vcc, 0x5000, v2
	s_nop 1
	v_addc_co_u32_e32 v3, vcc, 0, v3, vcc
	global_store_dword v[2:3], v4, off offset:2048

.LBB0_1233:
	v_mbcnt_lo_u32_b32 v250, -1, 0
	v_mbcnt_hi_u32_b32 v250, -1, v250
	v_lshrrev_b32_e32 v251, 2, v250
	v_and_b32_e32 v250, 3, v250
	v_lshl_add_u32 v250, v250, 4, v251
	v_lshlrev_b32_e32 v250, 2, v250
	v_lshl_add_u32 v148, s59, 10, v146
	ds_read2_b32 v[150:151], v148 offset1:16
	s_lshl_b32 s17, s58, 2
	v_med3_f32 v124, v124, 0, v193
	v_med3_f32 v125, v125, 0, v193
	s_lshl_b32 s16, s44, 7
	s_or_b32 s17, s17, s45
	s_waitcnt lgkmcnt(0)
	v_mul_f32_e32 v150, v150, v150
	v_pk_mul_f32 v[124:125], v[124:125], v[124:125]
	s_add_i32 s16, s17, s16
	v_pk_mul_f32 v[152:153], v[124:125], v[150:151] op_sel_hi:[1,0]
	v_med3_f32 v124, v130, 0, v193
	v_med3_f32 v125, v131, 0, v193
	s_ashr_i32 s17, s16, 31
	v_med3_f32 v128, v128, 0, v193
	v_med3_f32 v129, v129, 0, v193
	v_med3_f32 v126, v126, 0, v193
	v_med3_f32 v127, v127, 0, v193
	v_pk_mul_f32 v[124:125], v[124:125], v[124:125]
	s_lshl_b64 s[16:17], s[16:17], 15
	v_pk_mul_f32 v[128:129], v[128:129], v[128:129]
	v_pk_mul_f32 v[130:131], v[124:125], v[150:151] op_sel_hi:[1,0]
	v_pk_mul_f32 v[124:125], v[126:127], v[126:127]
	v_med3_f32 v116, v116, 0, v193
	v_med3_f32 v117, v117, 0, v193
	v_lshl_add_u64 v[144:145], v[138:139], 0, s[16:17]
	v_pk_mul_f32 v[128:129], v[128:129], v[150:151] op_sel_hi:[1,0]
	v_pk_mul_f32 v[154:155], v[124:125], v[150:151] op_sel_hi:[1,0]
	v_cvt_pk_bf16_f32 v124, v128, v129
	v_cvt_pk_bf16_f32 v125, v130, v131
	v_pk_mul_f32 v[116:117], v[116:117], v[116:117]
	v_cvt_pk_bf16_f32 v126, v152, v153
	v_cvt_pk_bf16_f32 v127, v154, v155
	ds_bpermute_b32 v232, v250, v124
	ds_bpermute_b32 v233, v250, v125
	ds_bpermute_b32 v234, v250, v126
	ds_bpermute_b32 v235, v250, v127
	ds_bpermute_b32 v236, v250, v144
	v_med3_f32 v120, v120, 0, v193
	v_med3_f32 v121, v121, 0, v193
	v_pk_mul_f32 v[124:125], v[116:117], v[150:151] op_sel_hi:[1,0]
	v_med3_f32 v116, v122, 0, v193
	v_med3_f32 v117, v123, 0, v193
	v_med3_f32 v118, v118, 0, v193
	v_med3_f32 v119, v119, 0, v193
	v_pk_mul_f32 v[116:117], v[116:117], v[116:117]
	v_pk_mul_f32 v[120:121], v[120:121], v[120:121]
	v_pk_mul_f32 v[122:123], v[116:117], v[150:151] op_sel_hi:[1,0]
	v_pk_mul_f32 v[116:117], v[118:119], v[118:119]
	v_pk_mul_f32 v[120:121], v[120:121], v[150:151] op_sel_hi:[1,0]
	v_pk_mul_f32 v[126:127], v[116:117], v[150:151] op_sel_hi:[1,0]
	v_cvt_pk_bf16_f32 v116, v120, v121
	v_med3_f32 v106, v106, 0, v193
	v_med3_f32 v107, v107, 0, v193
	v_cvt_pk_bf16_f32 v117, v122, v123
	v_cvt_pk_bf16_f32 v118, v124, v125
	v_cvt_pk_bf16_f32 v119, v126, v127
	ds_bpermute_b32 v238, v250, v116
	ds_bpermute_b32 v239, v250, v117
	ds_bpermute_b32 v240, v250, v118
	ds_bpermute_b32 v241, v250, v119
	ds_bpermute_b32 v242, v250, v144
	v_pk_mul_f32 v[106:107], v[106:107], v[106:107]
	v_med3_f32 v110, v110, 0, v193
	v_mul_f32_e32 v116, v151, v151
	v_pk_mul_f32 v[118:119], v[106:107], v[116:117] op_sel_hi:[1,0]
	v_med3_f32 v106, v112, 0, v193
	v_med3_f32 v107, v113, 0, v193
	v_med3_f32 v111, v111, 0, v193
	v_med3_f32 v108, v108, 0, v193
	v_med3_f32 v109, v109, 0, v193
	v_pk_mul_f32 v[106:107], v[106:107], v[106:107]
	v_pk_mul_f32 v[110:111], v[110:111], v[110:111]
	v_pk_mul_f32 v[112:113], v[106:107], v[116:117] op_sel_hi:[1,0]
	v_pk_mul_f32 v[106:107], v[108:109], v[108:109]
	v_med3_f32 v98, v98, 0, v193
	v_med3_f32 v99, v99, 0, v193
	v_pk_mul_f32 v[110:111], v[110:111], v[116:117] op_sel_hi:[1,0]
	v_pk_mul_f32 v[120:121], v[106:107], v[116:117] op_sel_hi:[1,0]
	v_cvt_pk_bf16_f32 v106, v110, v111
	v_cvt_pk_bf16_f32 v107, v112, v113
	v_pk_mul_f32 v[98:99], v[98:99], v[98:99]
	v_cvt_pk_bf16_f32 v108, v118, v119
	v_cvt_pk_bf16_f32 v109, v120, v121
	s_waitcnt lgkmcnt(5)
	v_subrev_u32_e32 v236, s82, v236
	global_store_dwordx4 v236, v[232:235], s[82:83]
	ds_bpermute_b32 v244, v250, v106
	ds_bpermute_b32 v245, v250, v107
	ds_bpermute_b32 v246, v250, v108
	ds_bpermute_b32 v247, v250, v109
	ds_bpermute_b32 v248, v250, v144
	v_med3_f32 v102, v102, 0, v193
	v_med3_f32 v103, v103, 0, v193
	v_pk_mul_f32 v[106:107], v[98:99], v[116:117] op_sel_hi:[1,0]
	v_med3_f32 v98, v104, 0, v193
	v_med3_f32 v99, v105, 0, v193
	v_pk_mul_f32 v[102:103], v[102:103], v[102:103]
	v_med3_f32 v100, v100, 0, v193
	v_med3_f32 v101, v101, 0, v193
	v_pk_mul_f32 v[98:99], v[98:99], v[98:99]
	v_pk_mul_f32 v[102:103], v[102:103], v[116:117] op_sel_hi:[1,0]
	v_pk_mul_f32 v[104:105], v[98:99], v[116:117] op_sel_hi:[1,0]
	v_pk_mul_f32 v[98:99], v[100:101], v[100:101]
	v_med3_f32 v90, v90, 0, v193
	v_pk_mul_f32 v[108:109], v[98:99], v[116:117] op_sel_hi:[1,0]
	v_cvt_pk_bf16_f32 v98, v102, v103
	ds_read2_b32 v[102:103], v148 offset0:32 offset1:48
	v_med3_f32 v91, v91, 0, v193
	v_cvt_pk_bf16_f32 v99, v104, v105
	v_cvt_pk_bf16_f32 v100, v106, v107
	v_cvt_pk_bf16_f32 v101, v108, v109
	s_waitcnt lgkmcnt(6)
	v_subrev_u32_e32 v242, s82, v242
	global_store_dwordx4 v242, v[238:241], s[82:83] offset:64
	ds_bpermute_b32 v232, v250, v98
	ds_bpermute_b32 v233, v250, v99
	ds_bpermute_b32 v234, v250, v100
	ds_bpermute_b32 v235, v250, v101
	ds_bpermute_b32 v236, v250, v144
	v_pk_mul_f32 v[90:91], v[90:91], v[90:91]
	v_med3_f32 v94, v94, 0, v193
	s_waitcnt lgkmcnt(0)
	v_mul_f32_e32 v98, v102, v102
	v_med3_f32 v95, v95, 0, v193
	v_pk_mul_f32 v[100:101], v[90:91], v[98:99] op_sel_hi:[1,0]
	v_med3_f32 v90, v96, 0, v193
	v_med3_f32 v91, v97, 0, v193
	v_pk_mul_f32 v[94:95], v[94:95], v[94:95]
	v_med3_f32 v92, v92, 0, v193
	v_med3_f32 v93, v93, 0, v193
	v_pk_mul_f32 v[90:91], v[90:91], v[90:91]
	v_pk_mul_f32 v[94:95], v[94:95], v[98:99] op_sel_hi:[1,0]
	v_pk_mul_f32 v[96:97], v[90:91], v[98:99] op_sel_hi:[1,0]
	v_pk_mul_f32 v[90:91], v[92:93], v[92:93]
	v_med3_f32 v82, v82, 0, v193
	v_pk_mul_f32 v[104:105], v[90:91], v[98:99] op_sel_hi:[1,0]
	v_cvt_pk_bf16_f32 v90, v94, v95
	v_add_co_u32_e32 v94, vcc, s73, v144
	v_med3_f32 v83, v83, 0, v193
	v_cvt_pk_bf16_f32 v91, v96, v97
	s_nop 0
	v_addc_co_u32_e32 v95, vcc, 0, v145, vcc
	v_pk_mul_f32 v[82:83], v[82:83], v[82:83]
	v_cvt_pk_bf16_f32 v92, v100, v101
	v_cvt_pk_bf16_f32 v93, v104, v105
	s_waitcnt lgkmcnt(6)
	v_subrev_u32_e32 v248, s82, v248
	global_store_dwordx4 v248, v[244:247], s[82:83] offset:2048
	ds_bpermute_b32 v238, v250, v90
	ds_bpermute_b32 v239, v250, v91
	ds_bpermute_b32 v240, v250, v92
	ds_bpermute_b32 v241, v250, v93
	ds_bpermute_b32 v242, v250, v94
	v_med3_f32 v86, v86, 0, v193
	v_med3_f32 v87, v87, 0, v193
	v_pk_mul_f32 v[90:91], v[82:83], v[98:99] op_sel_hi:[1,0]
	v_med3_f32 v82, v88, 0, v193
	v_med3_f32 v83, v89, 0, v193
	v_med3_f32 v84, v84, 0, v193
	v_med3_f32 v85, v85, 0, v193
	v_pk_mul_f32 v[82:83], v[82:83], v[82:83]
	v_pk_mul_f32 v[86:87], v[86:87], v[86:87]
	v_pk_mul_f32 v[88:89], v[82:83], v[98:99] op_sel_hi:[1,0]
	v_pk_mul_f32 v[82:83], v[84:85], v[84:85]
	v_pk_mul_f32 v[86:87], v[86:87], v[98:99] op_sel_hi:[1,0]
	v_pk_mul_f32 v[92:93], v[82:83], v[98:99] op_sel_hi:[1,0]
	v_cvt_pk_bf16_f32 v82, v86, v87
	v_med3_f32 v74, v74, 0, v193
	v_med3_f32 v75, v75, 0, v193
	v_cvt_pk_bf16_f32 v83, v88, v89
	v_cvt_pk_bf16_f32 v84, v90, v91
	v_cvt_pk_bf16_f32 v85, v92, v93
	s_waitcnt lgkmcnt(5)
	v_subrev_u32_e32 v236, s82, v236
	global_store_dwordx4 v236, v[232:235], s[82:83] offset:2112
	ds_bpermute_b32 v244, v250, v82
	ds_bpermute_b32 v245, v250, v83
	ds_bpermute_b32 v246, v250, v84
	ds_bpermute_b32 v247, v250, v85
	ds_bpermute_b32 v248, v250, v94
	v_pk_mul_f32 v[74:75], v[74:75], v[74:75]
	v_med3_f32 v78, v78, 0, v193
	v_mul_f32_e32 v82, v103, v103
	v_pk_mul_f32 v[84:85], v[74:75], v[82:83] op_sel_hi:[1,0]
	v_med3_f32 v74, v80, 0, v193
	v_med3_f32 v75, v81, 0, v193
	v_med3_f32 v79, v79, 0, v193
	v_med3_f32 v76, v76, 0, v193
	v_med3_f32 v77, v77, 0, v193
	v_pk_mul_f32 v[74:75], v[74:75], v[74:75]
	v_pk_mul_f32 v[78:79], v[78:79], v[78:79]
	v_pk_mul_f32 v[80:81], v[74:75], v[82:83] op_sel_hi:[1,0]
	v_pk_mul_f32 v[74:75], v[76:77], v[76:77]
	v_med3_f32 v66, v66, 0, v193
	v_med3_f32 v67, v67, 0, v193
	v_pk_mul_f32 v[78:79], v[78:79], v[82:83] op_sel_hi:[1,0]
	v_pk_mul_f32 v[86:87], v[74:75], v[82:83] op_sel_hi:[1,0]
	v_cvt_pk_bf16_f32 v74, v78, v79
	v_cvt_pk_bf16_f32 v75, v80, v81
	v_pk_mul_f32 v[66:67], v[66:67], v[66:67]
	v_cvt_pk_bf16_f32 v76, v84, v85
	v_cvt_pk_bf16_f32 v77, v86, v87
	s_waitcnt lgkmcnt(5)
	v_subrev_u32_e32 v242, s82, v242
	global_store_dwordx4 v242, v[238:241], s[82:83]
	ds_bpermute_b32 v232, v250, v74
	ds_bpermute_b32 v233, v250, v75
	ds_bpermute_b32 v234, v250, v76
	ds_bpermute_b32 v235, v250, v77
	ds_bpermute_b32 v236, v250, v94
	v_med3_f32 v70, v70, 0, v193
	v_med3_f32 v71, v71, 0, v193
	v_pk_mul_f32 v[74:75], v[66:67], v[82:83] op_sel_hi:[1,0]
	v_med3_f32 v66, v72, 0, v193
	v_med3_f32 v67, v73, 0, v193
	v_pk_mul_f32 v[70:71], v[70:71], v[70:71]
	v_med3_f32 v68, v68, 0, v193
	v_med3_f32 v69, v69, 0, v193
	v_pk_mul_f32 v[66:67], v[66:67], v[66:67]
	v_pk_mul_f32 v[70:71], v[70:71], v[82:83] op_sel_hi:[1,0]
	v_pk_mul_f32 v[72:73], v[66:67], v[82:83] op_sel_hi:[1,0]
	v_pk_mul_f32 v[66:67], v[68:69], v[68:69]
	v_med3_f32 v64, v64, 0, v193
	v_pk_mul_f32 v[76:77], v[66:67], v[82:83] op_sel_hi:[1,0]
	v_cvt_pk_bf16_f32 v66, v70, v71
	ds_read2_b32 v[70:71], v148 offset0:128 offset1:144
	v_med3_f32 v65, v65, 0, v193
	v_cvt_pk_bf16_f32 v67, v72, v73
	v_cvt_pk_bf16_f32 v68, v74, v75
	v_cvt_pk_bf16_f32 v69, v76, v77
	s_waitcnt lgkmcnt(6)
	v_subrev_u32_e32 v248, s82, v248
	global_store_dwordx4 v248, v[244:247], s[82:83] offset:64
	ds_bpermute_b32 v238, v250, v66
	ds_bpermute_b32 v239, v250, v67
	ds_bpermute_b32 v240, v250, v68
	ds_bpermute_b32 v241, v250, v69
	ds_bpermute_b32 v242, v250, v94
	v_med3_f32 v60, v60, 0, v193
	v_med3_f32 v61, v61, 0, v193
	s_waitcnt lgkmcnt(0)
	v_mul_f32_e32 v66, v70, v70
	v_pk_mul_f32 v[64:65], v[64:65], v[64:65]
	v_med3_f32 v62, v62, 0, v193
	v_med3_f32 v63, v63, 0, v193
	v_med3_f32 v58, v58, 0, v193
	v_med3_f32 v59, v59, 0, v193
	v_pk_mul_f32 v[64:65], v[64:65], v[66:67] op_sel_hi:[1,0]
	v_pk_mul_f32 v[60:61], v[60:61], v[60:61]
	v_pk_mul_f32 v[62:63], v[62:63], v[62:63]
	v_pk_mul_f32 v[58:59], v[58:59], v[58:59]
	v_pk_mul_f32 v[68:69], v[60:61], v[66:67] op_sel_hi:[1,0]
	v_cvt_pk_bf16_f32 v61, v64, v65
	v_add_co_u32_e32 v64, vcc, s72, v144
	v_pk_mul_f32 v[62:63], v[62:63], v[66:67] op_sel_hi:[1,0]
	v_pk_mul_f32 v[58:59], v[58:59], v[66:67] op_sel_hi:[1,0]
	v_addc_co_u32_e32 v65, vcc, 0, v145, vcc
	v_cvt_pk_bf16_f32 v60, v62, v63
	v_cvt_pk_bf16_f32 v62, v58, v59
	v_add_co_u32_e32 v58, vcc, s31, v144
	v_med3_f32 v50, v50, 0, v193
	v_med3_f32 v51, v51, 0, v193
	v_addc_co_u32_e32 v59, vcc, 0, v145, vcc
	v_pk_mul_f32 v[50:51], v[50:51], v[50:51]
	v_cvt_pk_bf16_f32 v63, v68, v69
	s_waitcnt lgkmcnt(6)
	v_subrev_u32_e32 v236, s82, v236
	global_store_dwordx4 v236, v[232:235], s[82:83] offset:2048
	ds_bpermute_b32 v244, v250, v60
	ds_bpermute_b32 v245, v250, v61
	ds_bpermute_b32 v246, v250, v62
	ds_bpermute_b32 v247, v250, v63
	ds_bpermute_b32 v248, v250, v58
	v_med3_f32 v54, v54, 0, v193
	v_med3_f32 v55, v55, 0, v193
	v_pk_mul_f32 v[60:61], v[50:51], v[66:67] op_sel_hi:[1,0]
	v_med3_f32 v50, v56, 0, v193
	v_med3_f32 v51, v57, 0, v193
	v_med3_f32 v52, v52, 0, v193
	v_med3_f32 v53, v53, 0, v193
	v_pk_mul_f32 v[50:51], v[50:51], v[50:51]
	v_pk_mul_f32 v[54:55], v[54:55], v[54:55]
	v_pk_mul_f32 v[56:57], v[50:51], v[66:67] op_sel_hi:[1,0]
	v_pk_mul_f32 v[50:51], v[52:53], v[52:53]
	v_pk_mul_f32 v[54:55], v[54:55], v[66:67] op_sel_hi:[1,0]
	v_pk_mul_f32 v[62:63], v[50:51], v[66:67] op_sel_hi:[1,0]
	v_cvt_pk_bf16_f32 v50, v54, v55
	v_med3_f32 v42, v42, 0, v193
	v_med3_f32 v43, v43, 0, v193
	v_cvt_pk_bf16_f32 v51, v56, v57
	v_cvt_pk_bf16_f32 v52, v60, v61
	v_cvt_pk_bf16_f32 v53, v62, v63
	s_waitcnt lgkmcnt(5)
	v_subrev_u32_e32 v242, s82, v242
	global_store_dwordx4 v242, v[238:241], s[82:83] offset:2112
	ds_bpermute_b32 v232, v250, v50
	ds_bpermute_b32 v233, v250, v51
	ds_bpermute_b32 v234, v250, v52
	ds_bpermute_b32 v235, v250, v53
	ds_bpermute_b32 v236, v250, v64
	v_pk_mul_f32 v[42:43], v[42:43], v[42:43]
	v_med3_f32 v46, v46, 0, v193
	v_mul_f32_e32 v50, v71, v71
	v_pk_mul_f32 v[52:53], v[42:43], v[50:51] op_sel_hi:[1,0]
	v_med3_f32 v42, v48, 0, v193
	v_med3_f32 v43, v49, 0, v193
	v_med3_f32 v47, v47, 0, v193
	v_med3_f32 v44, v44, 0, v193
	v_med3_f32 v45, v45, 0, v193
	v_pk_mul_f32 v[42:43], v[42:43], v[42:43]
	v_pk_mul_f32 v[46:47], v[46:47], v[46:47]
	v_pk_mul_f32 v[48:49], v[42:43], v[50:51] op_sel_hi:[1,0]
	v_pk_mul_f32 v[42:43], v[44:45], v[44:45]
	v_med3_f32 v34, v34, 0, v193
	v_med3_f32 v35, v35, 0, v193
	v_pk_mul_f32 v[46:47], v[46:47], v[50:51] op_sel_hi:[1,0]
	v_pk_mul_f32 v[54:55], v[42:43], v[50:51] op_sel_hi:[1,0]
	v_cvt_pk_bf16_f32 v42, v46, v47
	v_cvt_pk_bf16_f32 v43, v48, v49
	v_pk_mul_f32 v[34:35], v[34:35], v[34:35]
	v_cvt_pk_bf16_f32 v44, v52, v53
	v_cvt_pk_bf16_f32 v45, v54, v55
	s_waitcnt lgkmcnt(5)
	v_subrev_u32_e32 v248, s82, v248
	global_store_dwordx4 v248, v[244:247], s[82:83] offset:-4096
	ds_bpermute_b32 v238, v250, v42
	ds_bpermute_b32 v239, v250, v43
	ds_bpermute_b32 v240, v250, v44
	ds_bpermute_b32 v241, v250, v45
	ds_bpermute_b32 v242, v250, v64
	v_med3_f32 v38, v38, 0, v193
	v_med3_f32 v39, v39, 0, v193
	v_pk_mul_f32 v[42:43], v[34:35], v[50:51] op_sel_hi:[1,0]
	v_med3_f32 v34, v40, 0, v193
	v_med3_f32 v35, v41, 0, v193
	v_pk_mul_f32 v[38:39], v[38:39], v[38:39]
	v_med3_f32 v36, v36, 0, v193
	v_med3_f32 v37, v37, 0, v193
	v_pk_mul_f32 v[34:35], v[34:35], v[34:35]
	v_pk_mul_f32 v[38:39], v[38:39], v[50:51] op_sel_hi:[1,0]
	v_pk_mul_f32 v[40:41], v[34:35], v[50:51] op_sel_hi:[1,0]
	v_pk_mul_f32 v[34:35], v[36:37], v[36:37]
	v_med3_f32 v26, v26, 0, v193
	v_pk_mul_f32 v[44:45], v[34:35], v[50:51] op_sel_hi:[1,0]
	v_cvt_pk_bf16_f32 v34, v38, v39
	ds_read2_b32 v[38:39], v148 offset0:160 offset1:176
	v_med3_f32 v27, v27, 0, v193
	v_cvt_pk_bf16_f32 v35, v40, v41
	v_cvt_pk_bf16_f32 v36, v42, v43
	v_cvt_pk_bf16_f32 v37, v44, v45
	s_waitcnt lgkmcnt(6)
	v_subrev_u32_e32 v236, s82, v236
	global_store_dwordx4 v236, v[232:235], s[82:83] offset:64
	ds_bpermute_b32 v244, v250, v34
	ds_bpermute_b32 v245, v250, v35
	ds_bpermute_b32 v246, v250, v36
	ds_bpermute_b32 v247, v250, v37
	ds_bpermute_b32 v248, v250, v64
	v_pk_mul_f32 v[26:27], v[26:27], v[26:27]
	v_med3_f32 v30, v30, 0, v193
	s_waitcnt lgkmcnt(0)
	v_mul_f32_e32 v34, v38, v38
	v_pk_mul_f32 v[36:37], v[26:27], v[34:35] op_sel_hi:[1,0]
	v_med3_f32 v26, v32, 0, v193
	v_med3_f32 v27, v33, 0, v193
	v_med3_f32 v31, v31, 0, v193
	v_med3_f32 v28, v28, 0, v193
	v_med3_f32 v29, v29, 0, v193
	v_pk_mul_f32 v[26:27], v[26:27], v[26:27]
	v_pk_mul_f32 v[30:31], v[30:31], v[30:31]
	v_pk_mul_f32 v[32:33], v[26:27], v[34:35] op_sel_hi:[1,0]
	v_pk_mul_f32 v[26:27], v[28:29], v[28:29]
	v_med3_f32 v18, v18, 0, v193
	v_med3_f32 v19, v19, 0, v193
	v_pk_mul_f32 v[30:31], v[30:31], v[34:35] op_sel_hi:[1,0]
	v_pk_mul_f32 v[40:41], v[26:27], v[34:35] op_sel_hi:[1,0]
	v_cvt_pk_bf16_f32 v26, v30, v31
	v_cvt_pk_bf16_f32 v27, v32, v33
	v_pk_mul_f32 v[18:19], v[18:19], v[18:19]
	v_cvt_pk_bf16_f32 v28, v36, v37
	v_cvt_pk_bf16_f32 v29, v40, v41
	s_waitcnt lgkmcnt(6)
	v_subrev_u32_e32 v242, s82, v242
	global_store_dwordx4 v242, v[238:241], s[82:83] offset:2048
	ds_bpermute_b32 v232, v250, v26
	ds_bpermute_b32 v233, v250, v27
	ds_bpermute_b32 v234, v250, v28
	ds_bpermute_b32 v235, v250, v29
	ds_bpermute_b32 v236, v250, v58
	v_med3_f32 v22, v22, 0, v193
	v_med3_f32 v23, v23, 0, v193
	v_pk_mul_f32 v[26:27], v[18:19], v[34:35] op_sel_hi:[1,0]
	v_med3_f32 v18, v24, 0, v193
	v_med3_f32 v19, v25, 0, v193
	v_med3_f32 v20, v20, 0, v193
	v_med3_f32 v21, v21, 0, v193
	v_pk_mul_f32 v[18:19], v[18:19], v[18:19]
	v_pk_mul_f32 v[22:23], v[22:23], v[22:23]
	v_pk_mul_f32 v[24:25], v[18:19], v[34:35] op_sel_hi:[1,0]
	v_pk_mul_f32 v[18:19], v[20:21], v[20:21]
	v_pk_mul_f32 v[22:23], v[22:23], v[34:35] op_sel_hi:[1,0]
	v_pk_mul_f32 v[28:29], v[18:19], v[34:35] op_sel_hi:[1,0]
	v_cvt_pk_bf16_f32 v18, v22, v23
	v_med3_f32 v10, v10, 0, v193
	v_med3_f32 v11, v11, 0, v193
	v_cvt_pk_bf16_f32 v19, v24, v25
	v_cvt_pk_bf16_f32 v20, v26, v27
	v_cvt_pk_bf16_f32 v21, v28, v29
	s_waitcnt lgkmcnt(5)
	v_subrev_u32_e32 v248, s82, v248
	global_store_dwordx4 v248, v[244:247], s[82:83] offset:2112
	ds_bpermute_b32 v238, v250, v18
	ds_bpermute_b32 v239, v250, v19
	ds_bpermute_b32 v240, v250, v20
	ds_bpermute_b32 v241, v250, v21
	ds_bpermute_b32 v242, v250, v58
	v_pk_mul_f32 v[10:11], v[10:11], v[10:11]
	v_med3_f32 v14, v14, 0, v193
	v_mul_f32_e32 v18, v39, v39
	v_pk_mul_f32 v[20:21], v[10:11], v[18:19] op_sel_hi:[1,0]
	v_med3_f32 v10, v16, 0, v193
	v_med3_f32 v11, v17, 0, v193
	v_med3_f32 v15, v15, 0, v193
	v_med3_f32 v12, v12, 0, v193
	v_med3_f32 v13, v13, 0, v193
	v_pk_mul_f32 v[10:11], v[10:11], v[10:11]
	v_pk_mul_f32 v[14:15], v[14:15], v[14:15]
	v_pk_mul_f32 v[16:17], v[10:11], v[18:19] op_sel_hi:[1,0]
	v_pk_mul_f32 v[10:11], v[12:13], v[12:13]
	v_med3_f32 v2, v2, 0, v193
	v_med3_f32 v3, v3, 0, v193
	v_pk_mul_f32 v[14:15], v[14:15], v[18:19] op_sel_hi:[1,0]
	v_pk_mul_f32 v[22:23], v[10:11], v[18:19] op_sel_hi:[1,0]
	v_cvt_pk_bf16_f32 v10, v14, v15
	v_cvt_pk_bf16_f32 v11, v16, v17
	v_pk_mul_f32 v[2:3], v[2:3], v[2:3]
	v_cvt_pk_bf16_f32 v12, v20, v21
	v_cvt_pk_bf16_f32 v13, v22, v23
	s_waitcnt lgkmcnt(5)
	v_subrev_u32_e32 v236, s82, v236
	global_store_dwordx4 v236, v[232:235], s[82:83]
	ds_bpermute_b32 v244, v250, v10
	ds_bpermute_b32 v245, v250, v11
	ds_bpermute_b32 v246, v250, v12
	ds_bpermute_b32 v247, v250, v13
	ds_bpermute_b32 v248, v250, v58
	v_med3_f32 v6, v6, 0, v193
	v_med3_f32 v7, v7, 0, v193
	v_pk_mul_f32 v[10:11], v[2:3], v[18:19] op_sel_hi:[1,0]
	v_med3_f32 v2, v8, 0, v193
	v_med3_f32 v3, v9, 0, v193
	v_med3_f32 v4, v4, 0, v193
	v_med3_f32 v5, v5, 0, v193
	v_pk_mul_f32 v[2:3], v[2:3], v[2:3]
	v_pk_mul_f32 v[6:7], v[6:7], v[6:7]
	v_pk_mul_f32 v[8:9], v[2:3], v[18:19] op_sel_hi:[1,0]
	v_pk_mul_f32 v[2:3], v[4:5], v[4:5]
	s_andn2_b64 vcc, exec, s[38:39]
	s_mov_b64 s[38:39], -1
	v_pk_mul_f32 v[6:7], v[6:7], v[18:19] op_sel_hi:[1,0]
	v_pk_mul_f32 v[12:13], v[2:3], v[18:19] op_sel_hi:[1,0]
	v_cvt_pk_bf16_f32 v2, v6, v7
	v_cvt_pk_bf16_f32 v3, v8, v9
	v_cvt_pk_bf16_f32 v4, v10, v11
	s_nop 0
	v_cvt_pk_bf16_f32 v5, v12, v13
	s_waitcnt lgkmcnt(5)
	v_subrev_u32_e32 v242, s82, v242
	global_store_dwordx4 v242, v[238:241], s[82:83] offset:64
	ds_bpermute_b32 v232, v250, v2
	ds_bpermute_b32 v233, v250, v3
	ds_bpermute_b32 v234, v250, v4
	ds_bpermute_b32 v235, v250, v5
	ds_bpermute_b32 v236, v250, v58
	s_waitcnt lgkmcnt(5)
	v_subrev_u32_e32 v248, s82, v248
	global_store_dwordx4 v248, v[244:247], s[82:83] offset:2048
	s_waitcnt lgkmcnt(0)
	v_subrev_u32_e32 v236, s82, v236
	global_store_dwordx4 v236, v[232:235], s[82:83] offset:2112
	s_cbranch_vccnz .LBB0_1222
	s_andn2_b64 vcc, exec, s[0:1]
	s_cbranch_vccnz .LBB0_1221
	s_barrier
	s_branch .LBB0_1221

.LBB0_1337:
	v_mbcnt_lo_u32_b32 v250, -1, 0
	v_mbcnt_hi_u32_b32 v250, -1, v250
	v_lshrrev_b32_e32 v251, 2, v250
	v_and_b32_e32 v250, 3, v250
	v_lshl_add_u32 v250, v250, 4, v251
	v_lshlrev_b32_e32 v250, 2, v250
	v_pk_mul_f32 v[148:149], v[118:119], v[118:119]
	v_pk_mul_f32 v[150:151], v[126:127], v[126:127]
	v_pk_fma_f32 v[148:149], v[116:117], v[116:117], v[148:149]
	v_pk_fma_f32 v[150:151], v[124:125], v[124:125], v[150:151]
	v_lshl_add_u32 v144, s46, 8, v1
	v_pk_add_f32 v[152:153], v[148:149], v[150:151]
	v_cvt_pk_bf16_f32 v149, v118, v119
	v_cvt_pk_bf16_f32 v150, v124, v125
	v_pk_mul_f32 v[118:119], v[122:123], v[122:123]
	v_pk_mul_f32 v[124:125], v[130:131], v[130:131]
	v_pk_fma_f32 v[118:119], v[120:121], v[120:121], v[118:119]
	v_pk_fma_f32 v[124:125], v[128:129], v[128:129], v[124:125]
	s_lshl_b32 s16, s46, 5
	v_pk_add_f32 v[118:119], v[118:119], v[124:125]
	s_lshl_b32 s46, s48, 2
	v_pk_add_f32 v[124:125], v[152:153], v[118:119]
	s_or_b32 s17, s46, s14
	v_add_f32_e32 v124, v124, v125
	ds_swizzle_b32 v125, v124 offset:swizzle(SWAP,16)
	s_add_i32 s16, s17, s16
	s_ashr_i32 s17, s16, 31
	s_lshl_b64 s[16:17], s[16:17], 15
	v_cvt_pk_bf16_f32 v148, v116, v117
	v_lshl_add_u64 v[116:117], v[138:139], 0, s[16:17]
	v_cvt_pk_bf16_f32 v118, v120, v121
	v_cvt_pk_bf16_f32 v119, v122, v123
	v_cvt_pk_bf16_f32 v120, v128, v129
	v_cvt_pk_bf16_f32 v121, v130, v131
	ds_bpermute_b32 v232, v250, v118
	ds_bpermute_b32 v233, v250, v119
	ds_bpermute_b32 v234, v250, v120
	ds_bpermute_b32 v235, v250, v121
	ds_bpermute_b32 v236, v250, v116
	s_ashr_i32 s47, s46, 31
	v_cvt_pk_bf16_f32 v151, v126, v127
	ds_bpermute_b32 v238, v250, v148
	ds_bpermute_b32 v239, v250, v149
	ds_bpermute_b32 v240, v250, v150
	ds_bpermute_b32 v241, v250, v151
	ds_bpermute_b32 v242, v250, v116
	s_waitcnt lgkmcnt(0)
	v_add_f32_e32 v118, v124, v125
	v_mov_b32_e32 v119, v118
	s_nop 1
	v_permlane32_swap_b32_e32 v118, v119
	s_waitcnt lgkmcnt(5)
	v_subrev_u32_e32 v236, s82, v236
	global_store_dwordx4 v236, v[232:235], s[82:83] offset:64
	s_waitcnt lgkmcnt(0)
	v_subrev_u32_e32 v242, s82, v242
	global_store_dwordx4 v242, v[238:241], s[82:83]
	s_and_saveexec_b64 s[48:49], s[38:39]
	s_cbranch_execz .LBB0_1339
	v_ashrrev_i32_e32 v145, 31, v144
	v_add_f32_e32 v120, v118, v119
	v_lshlrev_b64 v[118:119], 7, v[144:145]
	v_lshl_add_u64 v[118:119], s[8:9], 0, v[118:119]
	v_lshl_add_u64 v[118:119], s[46:47], 2, v[118:119]
	s_lshl_b32 s24, s14, 2
	v_lshl_add_u64 v[118:119], v[118:119], 0, s[24:25]
	global_store_dword v[118:119], v120, off
.LBB0_1339:
	s_or_b64 exec, exec, s[48:49]
	v_pk_mul_f32 v[118:119], v[100:101], v[100:101]
	v_pk_mul_f32 v[120:121], v[104:105], v[104:105]
	v_pk_fma_f32 v[118:119], v[98:99], v[98:99], v[118:119]
	v_cvt_pk_bf16_f32 v98, v98, v99
	v_cvt_pk_bf16_f32 v99, v100, v101
	v_cvt_pk_bf16_f32 v100, v102, v103
	v_cvt_pk_bf16_f32 v101, v104, v105
	ds_bpermute_b32 v244, v250, v98
	ds_bpermute_b32 v245, v250, v99
	ds_bpermute_b32 v246, v250, v100
	ds_bpermute_b32 v247, v250, v101
	ds_bpermute_b32 v248, v250, v116
	v_pk_fma_f32 v[120:121], v[102:103], v[102:103], v[120:121]
	s_nop 0
	v_pk_mul_f32 v[98:99], v[108:109], v[108:109]
	v_pk_mul_f32 v[100:101], v[112:113], v[112:113]
	v_pk_fma_f32 v[98:99], v[106:107], v[106:107], v[98:99]
	v_pk_fma_f32 v[100:101], v[110:111], v[110:111], v[100:101]
	v_pk_add_f32 v[118:119], v[118:119], v[120:121]
	v_pk_add_f32 v[98:99], v[98:99], v[100:101]
	s_nop 0
	v_pk_add_f32 v[100:101], v[118:119], v[98:99]
	v_cvt_pk_bf16_f32 v98, v106, v107
	v_cvt_pk_bf16_f32 v99, v108, v109
	s_nop 0
	v_add_f32_e32 v102, v100, v101
	ds_swizzle_b32 v103, v102 offset:swizzle(SWAP,16)
	v_cvt_pk_bf16_f32 v100, v110, v111
	v_cvt_pk_bf16_f32 v101, v112, v113
	ds_bpermute_b32 v232, v250, v98
	ds_bpermute_b32 v233, v250, v99
	ds_bpermute_b32 v234, v250, v100
	ds_bpermute_b32 v235, v250, v101
	ds_bpermute_b32 v236, v250, v116
	s_waitcnt lgkmcnt(0)
	s_nop 0
	v_add_f32_e32 v98, v102, v103
	v_mov_b32_e32 v99, v98
	s_nop 1
	v_permlane32_swap_b32_e32 v98, v99
	s_waitcnt lgkmcnt(6)
	v_subrev_u32_e32 v248, s82, v248
	global_store_dwordx4 v248, v[244:247], s[82:83] offset:2048
	s_waitcnt lgkmcnt(0)
	v_subrev_u32_e32 v236, s82, v236
	global_store_dwordx4 v236, v[232:235], s[82:83] offset:2112
	s_and_saveexec_b64 s[48:49], s[38:39]
	s_cbranch_execz .LBB0_1341
	v_or_b32_e32 v100, 16, v144
	v_ashrrev_i32_e32 v101, 31, v100
	v_add_f32_e32 v102, v98, v99
	v_lshlrev_b64 v[98:99], 7, v[100:101]
	v_lshl_add_u64 v[98:99], s[8:9], 0, v[98:99]
	v_lshl_add_u64 v[98:99], s[46:47], 2, v[98:99]
	s_lshl_b32 s24, s14, 2
	v_lshl_add_u64 v[98:99], v[98:99], 0, s[24:25]
	global_store_dword v[98:99], v102, off
.LBB0_1341:
	s_or_b64 exec, exec, s[48:49]
	v_pk_mul_f32 v[98:99], v[84:85], v[84:85]
	v_pk_mul_f32 v[100:101], v[92:93], v[92:93]
	v_pk_fma_f32 v[98:99], v[82:83], v[82:83], v[98:99]
	v_pk_fma_f32 v[100:101], v[90:91], v[90:91], v[100:101]
	s_nop 0
	v_pk_add_f32 v[102:103], v[98:99], v[100:101]
	v_cvt_pk_bf16_f32 v99, v84, v85
	v_cvt_pk_bf16_f32 v100, v90, v91
	v_pk_mul_f32 v[84:85], v[88:89], v[88:89]
	v_pk_mul_f32 v[90:91], v[96:97], v[96:97]
	v_pk_fma_f32 v[84:85], v[86:87], v[86:87], v[84:85]
	v_pk_fma_f32 v[90:91], v[94:95], v[94:95], v[90:91]
	v_cvt_pk_bf16_f32 v98, v82, v83
	v_add_co_u32_e32 v82, vcc, s73, v116
	v_pk_add_f32 v[84:85], v[84:85], v[90:91]
	s_nop 0
	v_addc_co_u32_e32 v83, vcc, 0, v117, vcc
	v_pk_add_f32 v[90:91], v[102:103], v[84:85]
	v_cvt_pk_bf16_f32 v84, v86, v87
	v_cvt_pk_bf16_f32 v85, v88, v89
	v_cvt_pk_bf16_f32 v86, v94, v95
	v_cvt_pk_bf16_f32 v87, v96, v97
	ds_bpermute_b32 v238, v250, v84
	ds_bpermute_b32 v239, v250, v85
	ds_bpermute_b32 v240, v250, v86
	ds_bpermute_b32 v241, v250, v87
	ds_bpermute_b32 v242, v250, v82
	v_add_f32_e32 v90, v90, v91
	ds_swizzle_b32 v91, v90 offset:swizzle(SWAP,16)
	v_cvt_pk_bf16_f32 v101, v92, v93
	ds_bpermute_b32 v244, v250, v98
	ds_bpermute_b32 v245, v250, v99
	ds_bpermute_b32 v246, v250, v100
	ds_bpermute_b32 v247, v250, v101
	ds_bpermute_b32 v248, v250, v82
	s_waitcnt lgkmcnt(0)
	v_add_f32_e32 v84, v90, v91
	v_mov_b32_e32 v85, v84
	s_nop 1
	v_permlane32_swap_b32_e32 v84, v85
	s_waitcnt lgkmcnt(6)
	v_subrev_u32_e32 v242, s82, v242
	global_store_dwordx4 v242, v[238:241], s[82:83] offset:64
	s_waitcnt lgkmcnt(0)
	v_subrev_u32_e32 v248, s82, v248
	global_store_dwordx4 v248, v[244:247], s[82:83]
	s_and_saveexec_b64 s[48:49], s[38:39]
	s_cbranch_execz .LBB0_1343
	v_or_b32_e32 v86, 32, v144
	v_ashrrev_i32_e32 v87, 31, v86
	v_add_f32_e32 v88, v84, v85
	v_lshlrev_b64 v[84:85], 7, v[86:87]
	v_lshl_add_u64 v[84:85], s[8:9], 0, v[84:85]
	v_lshl_add_u64 v[84:85], s[46:47], 2, v[84:85]
	s_lshl_b32 s24, s14, 2
	v_lshl_add_u64 v[84:85], v[84:85], 0, s[24:25]
	global_store_dword v[84:85], v88, off
.LBB0_1343:
	s_or_b64 exec, exec, s[48:49]
	v_pk_mul_f32 v[84:85], v[60:61], v[60:61]
	v_pk_mul_f32 v[86:87], v[72:73], v[72:73]
	v_pk_fma_f32 v[84:85], v[58:59], v[58:59], v[84:85]
	v_cvt_pk_bf16_f32 v58, v58, v59
	v_cvt_pk_bf16_f32 v59, v60, v61
	v_cvt_pk_bf16_f32 v60, v70, v71
	v_cvt_pk_bf16_f32 v61, v72, v73
	ds_bpermute_b32 v232, v250, v58
	ds_bpermute_b32 v233, v250, v59
	ds_bpermute_b32 v234, v250, v60
	ds_bpermute_b32 v235, v250, v61
	ds_bpermute_b32 v236, v250, v82
	v_pk_fma_f32 v[86:87], v[70:71], v[70:71], v[86:87]
	s_nop 0
	v_pk_mul_f32 v[58:59], v[76:77], v[76:77]
	v_pk_mul_f32 v[60:61], v[80:81], v[80:81]
	v_pk_fma_f32 v[58:59], v[74:75], v[74:75], v[58:59]
	v_pk_fma_f32 v[60:61], v[78:79], v[78:79], v[60:61]
	v_pk_add_f32 v[84:85], v[84:85], v[86:87]
	v_pk_add_f32 v[58:59], v[58:59], v[60:61]
	s_nop 0
	v_pk_add_f32 v[60:61], v[84:85], v[58:59]
	v_cvt_pk_bf16_f32 v58, v74, v75
	v_cvt_pk_bf16_f32 v59, v76, v77
	s_nop 0
	v_add_f32_e32 v70, v60, v61
	ds_swizzle_b32 v71, v70 offset:swizzle(SWAP,16)
	v_cvt_pk_bf16_f32 v60, v78, v79
	v_cvt_pk_bf16_f32 v61, v80, v81
	ds_bpermute_b32 v238, v250, v58
	ds_bpermute_b32 v239, v250, v59
	ds_bpermute_b32 v240, v250, v60
	ds_bpermute_b32 v241, v250, v61
	ds_bpermute_b32 v242, v250, v82
	s_waitcnt lgkmcnt(0)
	s_nop 0
	v_add_f32_e32 v58, v70, v71
	v_mov_b32_e32 v59, v58
	s_nop 1
	v_permlane32_swap_b32_e32 v58, v59
	s_waitcnt lgkmcnt(6)
	v_subrev_u32_e32 v236, s82, v236
	global_store_dwordx4 v236, v[232:235], s[82:83] offset:2048
	s_waitcnt lgkmcnt(0)
	v_subrev_u32_e32 v242, s82, v242
	global_store_dwordx4 v242, v[238:241], s[82:83] offset:2112
	s_and_saveexec_b64 s[48:49], s[38:39]
	s_cbranch_execz .LBB0_1345
	v_or_b32_e32 v60, 48, v144
	v_ashrrev_i32_e32 v61, 31, v60
	v_add_f32_e32 v70, v58, v59
	v_lshlrev_b64 v[58:59], 7, v[60:61]
	v_lshl_add_u64 v[58:59], s[8:9], 0, v[58:59]
	v_lshl_add_u64 v[58:59], s[46:47], 2, v[58:59]
	s_lshl_b32 s24, s14, 2
	v_lshl_add_u64 v[58:59], v[58:59], 0, s[24:25]
	global_store_dword v[58:59], v70, off
.LBB0_1345:
	s_or_b64 exec, exec, s[48:49]
	v_pk_mul_f32 v[58:59], v[52:53], v[52:53]
	v_pk_mul_f32 v[60:61], v[64:65], v[64:65]
	v_pk_fma_f32 v[58:59], v[50:51], v[50:51], v[58:59]
	v_pk_fma_f32 v[60:61], v[62:63], v[62:63], v[60:61]
	s_nop 0
	v_pk_add_f32 v[70:71], v[58:59], v[60:61]
	v_cvt_pk_bf16_f32 v58, v50, v51
	v_add_co_u32_e32 v50, vcc, s72, v116
	v_cvt_pk_bf16_f32 v59, v52, v53
	v_cvt_pk_bf16_f32 v60, v62, v63
	v_cvt_pk_bf16_f32 v61, v64, v65
	v_pk_mul_f32 v[52:53], v[56:57], v[56:57]
	s_nop 0
	v_addc_co_u32_e32 v51, vcc, 0, v117, vcc
	ds_bpermute_b32 v244, v250, v58
	ds_bpermute_b32 v245, v250, v59
	ds_bpermute_b32 v246, v250, v60
	ds_bpermute_b32 v247, v250, v61
	ds_bpermute_b32 v248, v250, v50
	v_pk_fma_f32 v[52:53], v[54:55], v[54:55], v[52:53]
	s_nop 0
	v_pk_mul_f32 v[58:59], v[68:69], v[68:69]
	s_nop 0
	v_pk_fma_f32 v[58:59], v[66:67], v[66:67], v[58:59]
	s_nop 0
	v_pk_add_f32 v[52:53], v[52:53], v[58:59]
	s_nop 0
	v_pk_add_f32 v[58:59], v[70:71], v[52:53]
	v_cvt_pk_bf16_f32 v52, v54, v55
	v_cvt_pk_bf16_f32 v53, v56, v57
	v_cvt_pk_bf16_f32 v54, v66, v67
	v_cvt_pk_bf16_f32 v55, v68, v69
	ds_bpermute_b32 v232, v250, v52
	ds_bpermute_b32 v233, v250, v53
	ds_bpermute_b32 v234, v250, v54
	ds_bpermute_b32 v235, v250, v55
	ds_bpermute_b32 v236, v250, v50
	v_add_f32_e32 v58, v58, v59
	ds_swizzle_b32 v59, v58 offset:swizzle(SWAP,16)
	s_waitcnt lgkmcnt(0)
	v_add_f32_e32 v52, v58, v59
	v_mov_b32_e32 v53, v52
	s_nop 1
	v_permlane32_swap_b32_e32 v52, v53
	s_waitcnt lgkmcnt(6)
	v_subrev_u32_e32 v248, s82, v248
	global_store_dwordx4 v248, v[244:247], s[82:83]
	s_waitcnt lgkmcnt(1)
	v_subrev_u32_e32 v236, s82, v236
	global_store_dwordx4 v236, v[232:235], s[82:83] offset:64
	s_and_saveexec_b64 s[48:49], s[38:39]
	s_cbranch_execz .LBB0_1347
	v_ashrrev_i32_e32 v145, 31, v144
	v_add_f32_e32 v54, v52, v53
	v_lshlrev_b64 v[52:53], 7, v[144:145]
	v_lshl_add_u64 v[52:53], s[8:9], 0, v[52:53]
	v_lshl_add_u64 v[52:53], s[46:47], 2, v[52:53]
	s_lshl_b32 s24, s14, 2
	v_lshl_add_u64 v[52:53], v[52:53], 0, s[24:25]
	v_add_co_u32_e32 v52, vcc, 0x4000, v52
	s_nop 1
	v_addc_co_u32_e32 v53, vcc, 0, v53, vcc
	global_store_dword v[52:53], v54, off
.LBB0_1347:
	s_or_b64 exec, exec, s[48:49]
	v_pk_mul_f32 v[52:53], v[36:37], v[36:37]
	v_pk_mul_f32 v[54:55], v[40:41], v[40:41]
	v_pk_fma_f32 v[52:53], v[34:35], v[34:35], v[52:53]
	v_cvt_pk_bf16_f32 v34, v34, v35
	v_cvt_pk_bf16_f32 v35, v36, v37
	v_cvt_pk_bf16_f32 v36, v38, v39
	v_cvt_pk_bf16_f32 v37, v40, v41
	ds_bpermute_b32 v238, v250, v34
	ds_bpermute_b32 v239, v250, v35
	ds_bpermute_b32 v240, v250, v36
	ds_bpermute_b32 v241, v250, v37
	ds_bpermute_b32 v242, v250, v50
	v_pk_fma_f32 v[54:55], v[38:39], v[38:39], v[54:55]
	s_nop 0
	v_pk_mul_f32 v[34:35], v[44:45], v[44:45]
	v_pk_mul_f32 v[36:37], v[48:49], v[48:49]
	v_pk_fma_f32 v[34:35], v[42:43], v[42:43], v[34:35]
	v_pk_fma_f32 v[36:37], v[46:47], v[46:47], v[36:37]
	v_pk_add_f32 v[52:53], v[52:53], v[54:55]
	v_pk_add_f32 v[34:35], v[34:35], v[36:37]
	s_nop 0
	v_pk_add_f32 v[36:37], v[52:53], v[34:35]
	v_cvt_pk_bf16_f32 v34, v42, v43
	v_cvt_pk_bf16_f32 v35, v44, v45
	s_nop 0
	v_add_f32_e32 v38, v36, v37
	ds_swizzle_b32 v39, v38 offset:swizzle(SWAP,16)
	v_cvt_pk_bf16_f32 v36, v46, v47
	v_cvt_pk_bf16_f32 v37, v48, v49
	ds_bpermute_b32 v244, v250, v34
	ds_bpermute_b32 v245, v250, v35
	ds_bpermute_b32 v246, v250, v36
	ds_bpermute_b32 v247, v250, v37
	ds_bpermute_b32 v248, v250, v50
	s_waitcnt lgkmcnt(0)
	s_nop 0
	v_add_f32_e32 v34, v38, v39
	v_mov_b32_e32 v35, v34
	s_nop 1
	v_permlane32_swap_b32_e32 v34, v35
	s_waitcnt lgkmcnt(6)
	v_subrev_u32_e32 v242, s82, v242
	global_store_dwordx4 v242, v[238:241], s[82:83] offset:2048
	s_waitcnt lgkmcnt(0)
	v_subrev_u32_e32 v248, s82, v248
	global_store_dwordx4 v248, v[244:247], s[82:83] offset:2112
	s_and_saveexec_b64 s[48:49], s[38:39]
	s_cbranch_execz .LBB0_1349
	v_ashrrev_i32_e32 v145, 31, v144
	v_add_f32_e32 v36, v34, v35
	v_lshlrev_b64 v[34:35], 7, v[144:145]
	v_lshl_add_u64 v[34:35], s[8:9], 0, v[34:35]
	v_lshl_add_u64 v[34:35], s[46:47], 2, v[34:35]
	s_lshl_b32 s24, s14, 2
	v_lshl_add_u64 v[34:35], v[34:35], 0, s[24:25]
	v_add_co_u32_e32 v34, vcc, 0x4000, v34
	s_nop 1
	v_addc_co_u32_e32 v35, vcc, 0, v35, vcc
	global_store_dword v[34:35], v36, off offset:2048
.LBB0_1349:
	s_or_b64 exec, exec, s[48:49]
	v_pk_mul_f32 v[34:35], v[20:21], v[20:21]
	v_pk_mul_f32 v[36:37], v[28:29], v[28:29]
	v_pk_fma_f32 v[34:35], v[18:19], v[18:19], v[34:35]
	v_pk_fma_f32 v[36:37], v[26:27], v[26:27], v[36:37]
	s_nop 0
	v_pk_add_f32 v[38:39], v[34:35], v[36:37]
	v_cvt_pk_bf16_f32 v35, v20, v21
	v_cvt_pk_bf16_f32 v36, v26, v27
	v_pk_mul_f32 v[20:21], v[24:25], v[24:25]
	v_pk_mul_f32 v[26:27], v[32:33], v[32:33]
	v_pk_fma_f32 v[20:21], v[22:23], v[22:23], v[20:21]
	v_pk_fma_f32 v[26:27], v[30:31], v[30:31], v[26:27]
	v_cvt_pk_bf16_f32 v34, v18, v19
	v_add_co_u32_e32 v18, vcc, s31, v116
	v_pk_add_f32 v[20:21], v[20:21], v[26:27]
	s_nop 0
	v_addc_co_u32_e32 v19, vcc, 0, v117, vcc
	v_pk_add_f32 v[26:27], v[38:39], v[20:21]
	v_cvt_pk_bf16_f32 v20, v22, v23
	v_cvt_pk_bf16_f32 v21, v24, v25
	v_cvt_pk_bf16_f32 v22, v30, v31
	v_cvt_pk_bf16_f32 v23, v32, v33
	ds_bpermute_b32 v232, v250, v20
	ds_bpermute_b32 v233, v250, v21
	ds_bpermute_b32 v234, v250, v22
	ds_bpermute_b32 v235, v250, v23
	ds_bpermute_b32 v236, v250, v18
	v_add_f32_e32 v26, v26, v27
	ds_swizzle_b32 v27, v26 offset:swizzle(SWAP,16)
	v_cvt_pk_bf16_f32 v37, v28, v29
	ds_bpermute_b32 v238, v250, v34
	ds_bpermute_b32 v239, v250, v35
	ds_bpermute_b32 v240, v250, v36
	ds_bpermute_b32 v241, v250, v37
	ds_bpermute_b32 v242, v250, v18
	s_waitcnt lgkmcnt(0)
	v_add_f32_e32 v20, v26, v27
	v_mov_b32_e32 v21, v20
	s_nop 1
	v_permlane32_swap_b32_e32 v20, v21
	s_waitcnt lgkmcnt(6)
	v_subrev_u32_e32 v236, s82, v236
	global_store_dwordx4 v236, v[232:235], s[82:83] offset:64
	s_waitcnt lgkmcnt(0)
	v_subrev_u32_e32 v242, s82, v242
	global_store_dwordx4 v242, v[238:241], s[82:83]
	s_and_saveexec_b64 s[48:49], s[38:39]
	s_cbranch_execz .LBB0_1351
	v_ashrrev_i32_e32 v145, 31, v144
	v_add_f32_e32 v22, v20, v21
	v_lshlrev_b64 v[20:21], 7, v[144:145]
	v_lshl_add_u64 v[20:21], s[8:9], 0, v[20:21]
	v_lshl_add_u64 v[20:21], s[46:47], 2, v[20:21]
	s_lshl_b32 s24, s14, 2
	v_lshl_add_u64 v[20:21], v[20:21], 0, s[24:25]
	v_add_co_u32_e32 v20, vcc, 0x5000, v20
	s_nop 1
	v_addc_co_u32_e32 v21, vcc, 0, v21, vcc
	global_store_dword v[20:21], v22, off
.LBB0_1351:
	s_or_b64 exec, exec, s[48:49]
	v_pk_mul_f32 v[20:21], v[4:5], v[4:5]
	v_pk_mul_f32 v[22:23], v[8:9], v[8:9]
	v_pk_fma_f32 v[20:21], v[2:3], v[2:3], v[20:21]
	v_cvt_pk_bf16_f32 v2, v2, v3
	v_cvt_pk_bf16_f32 v3, v4, v5
	v_cvt_pk_bf16_f32 v4, v6, v7
	v_cvt_pk_bf16_f32 v5, v8, v9
	ds_bpermute_b32 v244, v250, v2
	ds_bpermute_b32 v245, v250, v3
	ds_bpermute_b32 v246, v250, v4
	ds_bpermute_b32 v247, v250, v5
	ds_bpermute_b32 v248, v250, v18
	v_pk_fma_f32 v[22:23], v[6:7], v[6:7], v[22:23]
	s_nop 0
	v_pk_mul_f32 v[2:3], v[12:13], v[12:13]
	v_pk_mul_f32 v[4:5], v[16:17], v[16:17]
	v_pk_fma_f32 v[2:3], v[10:11], v[10:11], v[2:3]
	v_pk_fma_f32 v[4:5], v[14:15], v[14:15], v[4:5]
	v_pk_add_f32 v[20:21], v[20:21], v[22:23]
	v_pk_add_f32 v[2:3], v[2:3], v[4:5]
	s_nop 0
	v_pk_add_f32 v[4:5], v[20:21], v[2:3]
	v_cvt_pk_bf16_f32 v2, v10, v11
	v_cvt_pk_bf16_f32 v3, v12, v13
	s_nop 0
	v_add_f32_e32 v6, v4, v5
	ds_swizzle_b32 v7, v6 offset:swizzle(SWAP,16)
	v_cvt_pk_bf16_f32 v4, v14, v15
	v_cvt_pk_bf16_f32 v5, v16, v17
	ds_bpermute_b32 v232, v250, v2
	ds_bpermute_b32 v233, v250, v3
	ds_bpermute_b32 v234, v250, v4
	ds_bpermute_b32 v235, v250, v5
	ds_bpermute_b32 v236, v250, v18
	s_waitcnt lgkmcnt(0)
	s_nop 0
	v_add_f32_e32 v2, v6, v7
	v_mov_b32_e32 v3, v2
	s_nop 1
	v_permlane32_swap_b32_e32 v2, v3
	s_waitcnt lgkmcnt(6)
	v_subrev_u32_e32 v248, s82, v248
	global_store_dwordx4 v248, v[244:247], s[82:83] offset:2048
	s_waitcnt lgkmcnt(0)
	v_subrev_u32_e32 v236, s82, v236
	global_store_dwordx4 v236, v[232:235], s[82:83] offset:2112
	s_and_saveexec_b64 s[48:49], s[38:39]
	s_cbranch_execz .LBB0_1353
	v_ashrrev_i32_e32 v145, 31, v144
	v_add_f32_e32 v4, v2, v3
	v_lshlrev_b64 v[2:3], 7, v[144:145]
	v_lshl_add_u64 v[2:3], s[8:9], 0, v[2:3]
	v_lshl_add_u64 v[2:3], s[46:47], 2, v[2:3]
	s_lshl_b32 s24, s14, 2
	v_lshl_add_u64 v[2:3], v[2:3], 0, s[24:25]
	v_add_co_u32_e32 v2, vcc, 0x5000, v2
	s_nop 1
	v_addc_co_u32_e32 v3, vcc, 0, v3, vcc
	global_store_dword v[2:3], v4, off offset:2048
